# K-loop sub-phases issue their LDS-DMA loads before the ds_read fragment reads (9 dense GEMM loops)
# baseline (speedup 1.0000x reference)
.LBB0_261:
	s_add_i32 s0, s67, s10
	s_add_u32 s0, s4, s0
	s_addc_u32 s1, s5, 0
	s_add_i32 m0, s22, 0xc000
	s_add_i32 s30, s22, 0xe000
	s_add_i32 s31, s10, 0xfff80080
	s_cmp_eq_u32 s18, 28
	s_cselect_b32 s19, s45, s67
	s_cselect_b32 s68, s44, s66
	v_lshl_add_u64 v[208:209], s[0:1], 0, v[128:129]
	global_load_lds_dwordx4 v[208:209], off
	v_lshl_add_u64 v[208:209], s[0:1], 0, v[130:131]
	s_mov_b32 m0, s30
	s_nop 0
	global_load_lds_dwordx4 v[208:209], off
	ds_read_b128 v[144:147], v141
	ds_read_b128 v[148:151], v141 offset:1024
	ds_read_b128 v[152:155], v141 offset:2048
	ds_read_b128 v[156:159], v141 offset:3072
	ds_read_b128 v[160:163], v142
	ds_read_b128 v[164:167], v142 offset:1024
	ds_read_b128 v[168:171], v142 offset:2048
	ds_read_b128 v[172:175], v142 offset:3072
	ds_read_b128 v[176:179], v143
	ds_read_b128 v[180:183], v143 offset:1024
	ds_read_b128 v[184:187], v143 offset:2048
	ds_read_b128 v[188:191], v143 offset:3072
	ds_read_b128 v[192:195], v143 offset:4096
	ds_read_b128 v[196:199], v143 offset:5120
	ds_read_b128 v[200:203], v143 offset:6144
	ds_read_b128 v[204:207], v143 offset:7168
	s_waitcnt vmcnt(8)
	s_waitcnt lgkmcnt(0)
	s_barrier
	s_waitcnt lgkmcnt(0)
	v_mfma_f32_16x16x32_bf16 v[124:127], v[144:147], v[176:179], v[124:127]
	v_mfma_f32_16x16x32_bf16 v[120:123], v[152:155], v[176:179], v[120:123]
	v_mfma_f32_16x16x32_bf16 v[116:119], v[144:147], v[184:187], v[116:119]
	v_mfma_f32_16x16x32_bf16 v[112:115], v[152:155], v[184:187], v[112:115]
	v_mfma_f32_16x16x32_bf16 v[108:111], v[144:147], v[192:195], v[108:111]
	v_mfma_f32_16x16x32_bf16 v[100:103], v[152:155], v[192:195], v[100:103]
	v_mfma_f32_16x16x32_bf16 v[92:95], v[144:147], v[200:203], v[92:95]
	v_mfma_f32_16x16x32_bf16 v[84:87], v[152:155], v[200:203], v[84:87]
	v_mfma_f32_16x16x32_bf16 v[124:127], v[148:151], v[180:183], v[124:127]
	v_mfma_f32_16x16x32_bf16 v[120:123], v[156:159], v[180:183], v[120:123]
	v_mfma_f32_16x16x32_bf16 v[116:119], v[148:151], v[188:191], v[116:119]
	v_mfma_f32_16x16x32_bf16 v[112:115], v[156:159], v[188:191], v[112:115]
	v_mfma_f32_16x16x32_bf16 v[108:111], v[148:151], v[196:199], v[108:111]
	v_mfma_f32_16x16x32_bf16 v[100:103], v[156:159], v[196:199], v[100:103]
	v_mfma_f32_16x16x32_bf16 v[92:95], v[148:151], v[204:207], v[92:95]
	v_mfma_f32_16x16x32_bf16 v[84:87], v[156:159], v[204:207], v[84:87]
	v_mfma_f32_16x16x32_bf16 v[104:107], v[160:163], v[176:179], v[104:107]
	v_mfma_f32_16x16x32_bf16 v[96:99], v[168:171], v[176:179], v[96:99]
	v_mfma_f32_16x16x32_bf16 v[88:91], v[160:163], v[184:187], v[88:91]
	v_mfma_f32_16x16x32_bf16 v[80:83], v[168:171], v[184:187], v[80:83]
	v_mfma_f32_16x16x32_bf16 v[76:79], v[160:163], v[192:195], v[76:79]
	v_mfma_f32_16x16x32_bf16 v[72:75], v[168:171], v[192:195], v[72:75]
	v_mfma_f32_16x16x32_bf16 v[68:71], v[160:163], v[200:203], v[68:71]
	v_mfma_f32_16x16x32_bf16 v[64:67], v[168:171], v[200:203], v[64:67]
	v_mfma_f32_16x16x32_bf16 v[104:107], v[164:167], v[180:183], v[104:107]
	v_mfma_f32_16x16x32_bf16 v[96:99], v[172:175], v[180:183], v[96:99]
	v_mfma_f32_16x16x32_bf16 v[88:91], v[164:167], v[188:191], v[88:91]
	v_mfma_f32_16x16x32_bf16 v[80:83], v[172:175], v[188:191], v[80:83]
	v_mfma_f32_16x16x32_bf16 v[76:79], v[164:167], v[196:199], v[76:79]
	v_mfma_f32_16x16x32_bf16 v[72:75], v[172:175], v[196:199], v[72:75]
	v_mfma_f32_16x16x32_bf16 v[68:71], v[164:167], v[204:207], v[68:71]
	v_mfma_f32_16x16x32_bf16 v[64:67], v[172:175], v[204:207], v[64:67]
	s_barrier
	s_cselect_b32 s30, 0, s31
	s_add_i32 s0, s30, s68
	s_ashr_i32 s1, s0, 31
	s_add_u32 s0, s6, s0
	s_addc_u32 s1, s7, s1
	s_add_i32 s31, s38, s27
	v_lshl_add_u64 v[208:209], s[0:1], 0, v[128:129]
	s_mov_b32 m0, s31
	s_nop 0
	global_load_lds_dwordx4 v[208:209], off
	s_add_i32 m0, s31, 0x2000
	s_add_i32 s31, s68, 0x80000
	v_lshl_add_u64 v[208:209], s[0:1], 0, v[130:131]
	s_add_i32 s0, s31, s30
	s_ashr_i32 s1, s0, 31
	s_add_u32 s0, s6, s0
	s_addc_u32 s1, s7, s1
	s_add_i32 s69, s39, s27
	global_load_lds_dwordx4 v[208:209], off
	v_lshl_add_u64 v[208:209], s[0:1], 0, v[128:129]
	s_mov_b32 m0, s69
	s_nop 0
	global_load_lds_dwordx4 v[208:209], off
	s_add_i32 m0, s69, 0x2000
	s_add_i32 s69, s30, s19
	v_lshl_add_u64 v[208:209], s[0:1], 0, v[130:131]
	s_add_u32 s0, s4, s69
	s_addc_u32 s1, s5, 0
	global_load_lds_dwordx4 v[208:209], off
	v_lshl_add_u64 v[208:209], s[0:1], 0, v[128:129]
	s_mov_b32 m0, s22
	s_nop 0
	global_load_lds_dwordx4 v[208:209], off
	v_lshl_add_u64 v[208:209], s[0:1], 0, v[130:131]
	s_mov_b32 m0, s23
	s_nop 0
	global_load_lds_dwordx4 v[208:209], off
	ds_read_b128 v[176:179], v143 offset:16384
	ds_read_b128 v[180:183], v143 offset:17408
	ds_read_b128 v[184:187], v143 offset:18432
	ds_read_b128 v[188:191], v143 offset:19456
	ds_read_b128 v[192:195], v143 offset:20480
	ds_read_b128 v[196:199], v143 offset:21504
	ds_read_b128 v[200:203], v143 offset:22528
	ds_read_b128 v[204:207], v143 offset:23552
	s_waitcnt vmcnt(8)
	s_waitcnt lgkmcnt(0)
	s_barrier
	s_waitcnt lgkmcnt(0)
	v_mfma_f32_16x16x32_bf16 v[60:63], v[144:147], v[176:179], v[60:63]
	v_mfma_f32_16x16x32_bf16 v[56:59], v[152:155], v[176:179], v[56:59]
	v_mfma_f32_16x16x32_bf16 v[52:55], v[144:147], v[184:187], v[52:55]
	v_mfma_f32_16x16x32_bf16 v[48:51], v[152:155], v[184:187], v[48:51]
	v_mfma_f32_16x16x32_bf16 v[44:47], v[144:147], v[192:195], v[44:47]
	v_mfma_f32_16x16x32_bf16 v[36:39], v[152:155], v[192:195], v[36:39]
	v_mfma_f32_16x16x32_bf16 v[28:31], v[144:147], v[200:203], v[28:31]
	v_mfma_f32_16x16x32_bf16 v[20:23], v[152:155], v[200:203], v[20:23]
	v_mfma_f32_16x16x32_bf16 v[60:63], v[148:151], v[180:183], v[60:63]
	v_mfma_f32_16x16x32_bf16 v[56:59], v[156:159], v[180:183], v[56:59]
	v_mfma_f32_16x16x32_bf16 v[52:55], v[148:151], v[188:191], v[52:55]
	v_mfma_f32_16x16x32_bf16 v[48:51], v[156:159], v[188:191], v[48:51]
	v_mfma_f32_16x16x32_bf16 v[44:47], v[148:151], v[196:199], v[44:47]
	v_mfma_f32_16x16x32_bf16 v[36:39], v[156:159], v[196:199], v[36:39]
	v_mfma_f32_16x16x32_bf16 v[28:31], v[148:151], v[204:207], v[28:31]
	v_mfma_f32_16x16x32_bf16 v[20:23], v[156:159], v[204:207], v[20:23]
	v_mfma_f32_16x16x32_bf16 v[40:43], v[160:163], v[176:179], v[40:43]
	v_mfma_f32_16x16x32_bf16 v[32:35], v[168:171], v[176:179], v[32:35]
	v_mfma_f32_16x16x32_bf16 v[24:27], v[160:163], v[184:187], v[24:27]
	v_mfma_f32_16x16x32_bf16 v[16:19], v[168:171], v[184:187], v[16:19]
	v_mfma_f32_16x16x32_bf16 v[12:15], v[160:163], v[192:195], v[12:15]
	v_mfma_f32_16x16x32_bf16 v[8:11], v[168:171], v[192:195], v[8:11]
	v_mfma_f32_16x16x32_bf16 v[4:7], v[160:163], v[200:203], v[4:7]
	v_mfma_f32_16x16x32_bf16 v[0:3], v[168:171], v[200:203], v[0:3]
	v_mfma_f32_16x16x32_bf16 v[40:43], v[164:167], v[180:183], v[40:43]
	v_mfma_f32_16x16x32_bf16 v[32:35], v[172:175], v[180:183], v[32:35]
	v_mfma_f32_16x16x32_bf16 v[24:27], v[164:167], v[188:191], v[24:27]
	v_mfma_f32_16x16x32_bf16 v[16:19], v[172:175], v[188:191], v[16:19]
	v_mfma_f32_16x16x32_bf16 v[12:15], v[164:167], v[196:199], v[12:15]
	v_mfma_f32_16x16x32_bf16 v[8:11], v[172:175], v[196:199], v[8:11]
	v_mfma_f32_16x16x32_bf16 v[4:7], v[164:167], v[204:207], v[4:7]
	v_mfma_f32_16x16x32_bf16 v[0:3], v[172:175], v[204:207], v[0:3]
	s_barrier
	s_add_i32 s70, 0, 0x18000
	s_add_i32 s71, 0, 0x1c000
	s_add_i32 s69, s69, 0x80000
	s_add_u32 s0, s4, s69
	s_addc_u32 s1, s5, 0
	s_mov_b32 m0, s24
	v_lshl_add_u64 v[208:209], s[0:1], 0, v[128:129]
	global_load_lds_dwordx4 v[208:209], off
	v_lshl_add_u64 v[208:209], s[0:1], 0, v[130:131]
	s_mov_b32 m0, s25
	s_nop 0
	global_load_lds_dwordx4 v[208:209], off
	v_add_u32_e32 v156, s70, v140
	v_add_u32_e32 v172, s71, v140
	ds_read_b128 v[144:147], v156
	ds_read_b128 v[148:151], v156 offset:1024
	ds_read_b128 v[152:155], v156 offset:2048
	ds_read_b128 v[156:159], v156 offset:3072
	ds_read_b128 v[160:163], v172
	ds_read_b128 v[164:167], v172 offset:1024
	ds_read_b128 v[168:171], v172 offset:2048
	ds_read_b128 v[172:175], v172 offset:3072
	ds_read_b128 v[176:179], v143 offset:32768
	ds_read_b128 v[180:183], v143 offset:33792
	ds_read_b128 v[184:187], v143 offset:34816
	ds_read_b128 v[188:191], v143 offset:35840
	ds_read_b128 v[192:195], v143 offset:36864
	ds_read_b128 v[196:199], v143 offset:37888
	ds_read_b128 v[200:203], v143 offset:38912
	ds_read_b128 v[204:207], v143 offset:39936
	s_waitcnt vmcnt(8)
	s_waitcnt lgkmcnt(0)
	s_barrier
	s_waitcnt lgkmcnt(0)
	v_mfma_f32_16x16x32_bf16 v[124:127], v[144:147], v[176:179], v[124:127]
	v_mfma_f32_16x16x32_bf16 v[120:123], v[152:155], v[176:179], v[120:123]
	v_mfma_f32_16x16x32_bf16 v[116:119], v[144:147], v[184:187], v[116:119]
	v_mfma_f32_16x16x32_bf16 v[112:115], v[152:155], v[184:187], v[112:115]
	v_mfma_f32_16x16x32_bf16 v[108:111], v[144:147], v[192:195], v[108:111]
	v_mfma_f32_16x16x32_bf16 v[100:103], v[152:155], v[192:195], v[100:103]
	v_mfma_f32_16x16x32_bf16 v[92:95], v[144:147], v[200:203], v[92:95]
	v_mfma_f32_16x16x32_bf16 v[84:87], v[152:155], v[200:203], v[84:87]
	v_mfma_f32_16x16x32_bf16 v[124:127], v[148:151], v[180:183], v[124:127]
	v_mfma_f32_16x16x32_bf16 v[120:123], v[156:159], v[180:183], v[120:123]
	v_mfma_f32_16x16x32_bf16 v[116:119], v[148:151], v[188:191], v[116:119]
	v_mfma_f32_16x16x32_bf16 v[112:115], v[156:159], v[188:191], v[112:115]
	v_mfma_f32_16x16x32_bf16 v[108:111], v[148:151], v[196:199], v[108:111]
	v_mfma_f32_16x16x32_bf16 v[100:103], v[156:159], v[196:199], v[100:103]
	v_mfma_f32_16x16x32_bf16 v[92:95], v[148:151], v[204:207], v[92:95]
	v_mfma_f32_16x16x32_bf16 v[84:87], v[156:159], v[204:207], v[84:87]
	v_mfma_f32_16x16x32_bf16 v[104:107], v[160:163], v[176:179], v[104:107]
	v_mfma_f32_16x16x32_bf16 v[96:99], v[168:171], v[176:179], v[96:99]
	v_mfma_f32_16x16x32_bf16 v[88:91], v[160:163], v[184:187], v[88:91]
	v_mfma_f32_16x16x32_bf16 v[80:83], v[168:171], v[184:187], v[80:83]
	v_mfma_f32_16x16x32_bf16 v[76:79], v[160:163], v[192:195], v[76:79]
	v_mfma_f32_16x16x32_bf16 v[72:75], v[168:171], v[192:195], v[72:75]
	v_mfma_f32_16x16x32_bf16 v[68:71], v[160:163], v[200:203], v[68:71]
	v_mfma_f32_16x16x32_bf16 v[64:67], v[168:171], v[200:203], v[64:67]
	v_mfma_f32_16x16x32_bf16 v[104:107], v[164:167], v[180:183], v[104:107]
	v_mfma_f32_16x16x32_bf16 v[96:99], v[172:175], v[180:183], v[96:99]
	v_mfma_f32_16x16x32_bf16 v[88:91], v[164:167], v[188:191], v[88:91]
	v_mfma_f32_16x16x32_bf16 v[80:83], v[172:175], v[188:191], v[80:83]
	v_mfma_f32_16x16x32_bf16 v[76:79], v[164:167], v[196:199], v[76:79]
	v_mfma_f32_16x16x32_bf16 v[72:75], v[172:175], v[196:199], v[72:75]
	v_mfma_f32_16x16x32_bf16 v[68:71], v[164:167], v[204:207], v[68:71]
	v_mfma_f32_16x16x32_bf16 v[64:67], v[172:175], v[204:207], v[64:67]
	s_barrier
; template <class Epi, class Sched, class Hook = NoHook>
; __device__ __forceinline__ void gemm_phase_w(LAS unsigned char* lds, const Sched& S, const Epi& E, int wave_id, const Hook& HK = Hook()) {
;     ...
;         if constexpr (!SEG2) {
;             for (int tt = 0; tt < nt; tt += 2) {
;                 if constexpr (GATHER) { if (tt == nt - 2) {
;                     if (has_next) { gnxt_00 = S.grow_l(nxt, lds, nbuf, R0) + (unsigned)(C0 * 2); gnxt_01 = S.grow_l(nxt, lds, nbuf, R1) + (unsigned)(C1 * 2); gnxt_10 = S.grow_l(nxt, lds, nbuf, 128 + R0) + (unsigned)(C0 * 2); gnxt_11 = S.grow_l(nxt, lds, nbuf, 128 + R1) + (unsigned)(C1 * 2); }
;                     else { gnxt_00 = gcur_00; gnxt_01 = gcur_01; gnxt_10 = gcur_10; gnxt_11 = gcur_11; } } }
;                 PG_TRIP(tt, false, false, false);
	s_bitset1_b32 s30, 7
	s_add_i32 s0, s30, s68
	s_ashr_i32 s1, s0, 31
	s_add_u32 s0, s6, s0
	s_addc_u32 s1, s7, s1
	s_add_i32 s68, s70, s27
	v_lshl_add_u64 v[208:209], s[0:1], 0, v[128:129]
	s_mov_b32 m0, s68
	s_nop 0
	global_load_lds_dwordx4 v[208:209], off
	v_lshl_add_u64 v[208:209], s[0:1], 0, v[130:131]
	s_add_i32 s0, s30, s31
	s_add_i32 m0, s68, 0x2000
	s_ashr_i32 s1, s0, 31
	s_add_u32 s0, s6, s0
	s_addc_u32 s1, s7, s1
	s_add_i32 s31, s71, s27
	global_load_lds_dwordx4 v[208:209], off
	v_lshl_add_u64 v[208:209], s[0:1], 0, v[128:129]
	s_mov_b32 m0, s31
	s_add_i32 s30, s30, s19
	global_load_lds_dwordx4 v[208:209], off
	s_add_i32 m0, s31, 0x2000
	v_lshl_add_u64 v[208:209], s[0:1], 0, v[130:131]
	s_add_u32 s0, s4, s30
	s_addc_u32 s1, s5, 0
	global_load_lds_dwordx4 v[208:209], off
	v_lshl_add_u64 v[208:209], s[0:1], 0, v[128:129]
	s_mov_b32 m0, s36
	s_nop 0
	global_load_lds_dwordx4 v[208:209], off
	v_lshl_add_u64 v[208:209], s[0:1], 0, v[130:131]
	s_mov_b32 m0, s37
	s_nop 0
	global_load_lds_dwordx4 v[208:209], off
	ds_read_b128 v[176:179], v143 offset:49152
	ds_read_b128 v[180:183], v143 offset:50176
	ds_read_b128 v[184:187], v143 offset:51200
	ds_read_b128 v[188:191], v143 offset:52224
	ds_read_b128 v[192:195], v143 offset:53248
	ds_read_b128 v[196:199], v143 offset:54272
	ds_read_b128 v[200:203], v143 offset:55296
	ds_read_b128 v[204:207], v143 offset:56320
	s_waitcnt vmcnt(8)
	s_waitcnt lgkmcnt(0)
	s_barrier
	s_waitcnt lgkmcnt(0)
	v_mfma_f32_16x16x32_bf16 v[60:63], v[144:147], v[176:179], v[60:63]
	v_mfma_f32_16x16x32_bf16 v[56:59], v[152:155], v[176:179], v[56:59]
	v_mfma_f32_16x16x32_bf16 v[52:55], v[144:147], v[184:187], v[52:55]
	v_mfma_f32_16x16x32_bf16 v[48:51], v[152:155], v[184:187], v[48:51]
	v_mfma_f32_16x16x32_bf16 v[44:47], v[144:147], v[192:195], v[44:47]
	v_mfma_f32_16x16x32_bf16 v[36:39], v[152:155], v[192:195], v[36:39]
	v_mfma_f32_16x16x32_bf16 v[28:31], v[144:147], v[200:203], v[28:31]
	v_mfma_f32_16x16x32_bf16 v[20:23], v[152:155], v[200:203], v[20:23]
	v_mfma_f32_16x16x32_bf16 v[60:63], v[148:151], v[180:183], v[60:63]
	v_mfma_f32_16x16x32_bf16 v[56:59], v[156:159], v[180:183], v[56:59]
	v_mfma_f32_16x16x32_bf16 v[52:55], v[148:151], v[188:191], v[52:55]
	v_mfma_f32_16x16x32_bf16 v[48:51], v[156:159], v[188:191], v[48:51]
	v_mfma_f32_16x16x32_bf16 v[44:47], v[148:151], v[196:199], v[44:47]
	v_mfma_f32_16x16x32_bf16 v[36:39], v[156:159], v[196:199], v[36:39]
	v_mfma_f32_16x16x32_bf16 v[28:31], v[148:151], v[204:207], v[28:31]
	v_mfma_f32_16x16x32_bf16 v[20:23], v[156:159], v[204:207], v[20:23]
	v_mfma_f32_16x16x32_bf16 v[40:43], v[160:163], v[176:179], v[40:43]
	v_mfma_f32_16x16x32_bf16 v[32:35], v[168:171], v[176:179], v[32:35]
	v_mfma_f32_16x16x32_bf16 v[24:27], v[160:163], v[184:187], v[24:27]
	v_mfma_f32_16x16x32_bf16 v[16:19], v[168:171], v[184:187], v[16:19]
	v_mfma_f32_16x16x32_bf16 v[12:15], v[160:163], v[192:195], v[12:15]
	v_mfma_f32_16x16x32_bf16 v[8:11], v[168:171], v[192:195], v[8:11]
	v_mfma_f32_16x16x32_bf16 v[4:7], v[160:163], v[200:203], v[4:7]
	v_mfma_f32_16x16x32_bf16 v[0:3], v[168:171], v[200:203], v[0:3]
	v_mfma_f32_16x16x32_bf16 v[40:43], v[164:167], v[180:183], v[40:43]
	v_mfma_f32_16x16x32_bf16 v[32:35], v[172:175], v[180:183], v[32:35]
	v_mfma_f32_16x16x32_bf16 v[24:27], v[164:167], v[188:191], v[24:27]
	v_mfma_f32_16x16x32_bf16 v[16:19], v[172:175], v[188:191], v[16:19]
	v_mfma_f32_16x16x32_bf16 v[12:15], v[164:167], v[196:199], v[12:15]
	v_mfma_f32_16x16x32_bf16 v[8:11], v[172:175], v[196:199], v[8:11]
	v_mfma_f32_16x16x32_bf16 v[4:7], v[164:167], v[204:207], v[4:7]
	v_mfma_f32_16x16x32_bf16 v[0:3], v[172:175], v[204:207], v[0:3]
	s_barrier
	s_addk_i32 s10, 0x100
	s_add_i32 s18, s18, 2
	s_cmp_gt_u32 s18, 29
	s_cbranch_scc0 .LBB0_261
	s_and_b64 vcc, exec, s[14:15]
	s_cbranch_vccz .LBB0_264
	s_barrier

.LBB0_386:
	s_add_i32 s0, s45, s10
	s_add_u32 s0, s4, s0
	s_addc_u32 s1, s5, 0
	s_add_i32 m0, s23, 0xc000
	s_add_i32 s61, s23, 0xe000
	s_add_i32 s66, s10, 0xfff80080
	s_cmp_eq_u32 s18, 28
	s_cselect_b32 s19, s41, s45
	s_cselect_b32 s60, s40, s44
	v_lshl_add_u64 v[206:207], s[0:1], 0, v[128:129]
	global_load_lds_dwordx4 v[206:207], off
	v_lshl_add_u64 v[206:207], s[0:1], 0, v[130:131]
	s_mov_b32 m0, s61
	s_nop 0
	global_load_lds_dwordx4 v[206:207], off
	ds_read_b128 v[142:145], v139
	ds_read_b128 v[146:149], v139 offset:1024
	ds_read_b128 v[150:153], v139 offset:2048
	ds_read_b128 v[154:157], v139 offset:3072
	ds_read_b128 v[158:161], v140
	ds_read_b128 v[162:165], v140 offset:1024
	ds_read_b128 v[166:169], v140 offset:2048
	ds_read_b128 v[170:173], v140 offset:3072
	ds_read_b128 v[174:177], v141
	ds_read_b128 v[178:181], v141 offset:1024
	ds_read_b128 v[182:185], v141 offset:2048
	ds_read_b128 v[186:189], v141 offset:3072
	ds_read_b128 v[190:193], v141 offset:4096
	ds_read_b128 v[194:197], v141 offset:5120
	ds_read_b128 v[198:201], v141 offset:6144
	ds_read_b128 v[202:205], v141 offset:7168
	s_waitcnt vmcnt(8)
	s_waitcnt lgkmcnt(0)
	s_barrier
	s_waitcnt lgkmcnt(0)
	v_mfma_f32_16x16x32_bf16 v[124:127], v[142:145], v[174:177], v[124:127]
	v_mfma_f32_16x16x32_bf16 v[120:123], v[150:153], v[174:177], v[120:123]
	v_mfma_f32_16x16x32_bf16 v[116:119], v[142:145], v[182:185], v[116:119]
	v_mfma_f32_16x16x32_bf16 v[112:115], v[150:153], v[182:185], v[112:115]
	v_mfma_f32_16x16x32_bf16 v[108:111], v[142:145], v[190:193], v[108:111]
	v_mfma_f32_16x16x32_bf16 v[100:103], v[150:153], v[190:193], v[100:103]
	v_mfma_f32_16x16x32_bf16 v[92:95], v[142:145], v[198:201], v[92:95]
	v_mfma_f32_16x16x32_bf16 v[84:87], v[150:153], v[198:201], v[84:87]
	v_mfma_f32_16x16x32_bf16 v[124:127], v[146:149], v[178:181], v[124:127]
	v_mfma_f32_16x16x32_bf16 v[120:123], v[154:157], v[178:181], v[120:123]
	v_mfma_f32_16x16x32_bf16 v[116:119], v[146:149], v[186:189], v[116:119]
	v_mfma_f32_16x16x32_bf16 v[112:115], v[154:157], v[186:189], v[112:115]
	v_mfma_f32_16x16x32_bf16 v[108:111], v[146:149], v[194:197], v[108:111]
	v_mfma_f32_16x16x32_bf16 v[100:103], v[154:157], v[194:197], v[100:103]
	v_mfma_f32_16x16x32_bf16 v[92:95], v[146:149], v[202:205], v[92:95]
	v_mfma_f32_16x16x32_bf16 v[84:87], v[154:157], v[202:205], v[84:87]
	v_mfma_f32_16x16x32_bf16 v[104:107], v[158:161], v[174:177], v[104:107]
	v_mfma_f32_16x16x32_bf16 v[96:99], v[166:169], v[174:177], v[96:99]
	v_mfma_f32_16x16x32_bf16 v[88:91], v[158:161], v[182:185], v[88:91]
	v_mfma_f32_16x16x32_bf16 v[80:83], v[166:169], v[182:185], v[80:83]
	v_mfma_f32_16x16x32_bf16 v[76:79], v[158:161], v[190:193], v[76:79]
	v_mfma_f32_16x16x32_bf16 v[72:75], v[166:169], v[190:193], v[72:75]
	v_mfma_f32_16x16x32_bf16 v[68:71], v[158:161], v[198:201], v[68:71]
	v_mfma_f32_16x16x32_bf16 v[64:67], v[166:169], v[198:201], v[64:67]
	v_mfma_f32_16x16x32_bf16 v[104:107], v[162:165], v[178:181], v[104:107]
	v_mfma_f32_16x16x32_bf16 v[96:99], v[170:173], v[178:181], v[96:99]
	v_mfma_f32_16x16x32_bf16 v[88:91], v[162:165], v[186:189], v[88:91]
	v_mfma_f32_16x16x32_bf16 v[80:83], v[170:173], v[186:189], v[80:83]
	v_mfma_f32_16x16x32_bf16 v[76:79], v[162:165], v[194:197], v[76:79]
	v_mfma_f32_16x16x32_bf16 v[72:75], v[170:173], v[194:197], v[72:75]
	v_mfma_f32_16x16x32_bf16 v[68:71], v[162:165], v[202:205], v[68:71]
	v_mfma_f32_16x16x32_bf16 v[64:67], v[170:173], v[202:205], v[64:67]
	s_barrier
	s_cselect_b32 s61, 0, s66
	s_add_i32 s0, s61, s60
	s_ashr_i32 s1, s0, 31
	s_add_u32 s0, s6, s0
	s_addc_u32 s1, s7, s1
	s_add_i32 s66, s30, s27
	v_lshl_add_u64 v[206:207], s[0:1], 0, v[128:129]
	s_mov_b32 m0, s66
	s_nop 0
	global_load_lds_dwordx4 v[206:207], off
	s_add_i32 m0, s66, 0x2000
	s_add_i32 s66, s60, 0x80000
	v_lshl_add_u64 v[206:207], s[0:1], 0, v[130:131]
	s_add_i32 s0, s66, s61
	s_ashr_i32 s1, s0, 31
	s_add_u32 s0, s6, s0
	s_addc_u32 s1, s7, s1
	s_add_i32 s67, s31, s27
	global_load_lds_dwordx4 v[206:207], off
	v_lshl_add_u64 v[206:207], s[0:1], 0, v[128:129]
	s_mov_b32 m0, s67
	s_nop 0
	global_load_lds_dwordx4 v[206:207], off
	s_add_i32 m0, s67, 0x2000
	s_add_i32 s67, s61, s19
	v_lshl_add_u64 v[206:207], s[0:1], 0, v[130:131]
	s_add_u32 s0, s4, s67
	s_addc_u32 s1, s5, 0
	global_load_lds_dwordx4 v[206:207], off
	v_lshl_add_u64 v[206:207], s[0:1], 0, v[128:129]
	s_mov_b32 m0, s23
	s_nop 0
	global_load_lds_dwordx4 v[206:207], off
	v_lshl_add_u64 v[206:207], s[0:1], 0, v[130:131]
	s_mov_b32 m0, s24
	s_nop 0
	global_load_lds_dwordx4 v[206:207], off
	ds_read_b128 v[174:177], v141 offset:16384
	ds_read_b128 v[178:181], v141 offset:17408
	ds_read_b128 v[182:185], v141 offset:18432
	ds_read_b128 v[186:189], v141 offset:19456
	ds_read_b128 v[190:193], v141 offset:20480
	ds_read_b128 v[194:197], v141 offset:21504
	ds_read_b128 v[198:201], v141 offset:22528
	ds_read_b128 v[202:205], v141 offset:23552
	s_waitcnt vmcnt(8)
	s_waitcnt lgkmcnt(0)
	s_barrier
	s_waitcnt lgkmcnt(0)
	v_mfma_f32_16x16x32_bf16 v[60:63], v[142:145], v[174:177], v[60:63]
	v_mfma_f32_16x16x32_bf16 v[56:59], v[150:153], v[174:177], v[56:59]
	v_mfma_f32_16x16x32_bf16 v[52:55], v[142:145], v[182:185], v[52:55]
	v_mfma_f32_16x16x32_bf16 v[48:51], v[150:153], v[182:185], v[48:51]
	v_mfma_f32_16x16x32_bf16 v[44:47], v[142:145], v[190:193], v[44:47]
	v_mfma_f32_16x16x32_bf16 v[36:39], v[150:153], v[190:193], v[36:39]
	v_mfma_f32_16x16x32_bf16 v[28:31], v[142:145], v[198:201], v[28:31]
	v_mfma_f32_16x16x32_bf16 v[20:23], v[150:153], v[198:201], v[20:23]
	v_mfma_f32_16x16x32_bf16 v[60:63], v[146:149], v[178:181], v[60:63]
	v_mfma_f32_16x16x32_bf16 v[56:59], v[154:157], v[178:181], v[56:59]
	v_mfma_f32_16x16x32_bf16 v[52:55], v[146:149], v[186:189], v[52:55]
	v_mfma_f32_16x16x32_bf16 v[48:51], v[154:157], v[186:189], v[48:51]
	v_mfma_f32_16x16x32_bf16 v[44:47], v[146:149], v[194:197], v[44:47]
	v_mfma_f32_16x16x32_bf16 v[36:39], v[154:157], v[194:197], v[36:39]
	v_mfma_f32_16x16x32_bf16 v[28:31], v[146:149], v[202:205], v[28:31]
	v_mfma_f32_16x16x32_bf16 v[20:23], v[154:157], v[202:205], v[20:23]
	v_mfma_f32_16x16x32_bf16 v[40:43], v[158:161], v[174:177], v[40:43]
	v_mfma_f32_16x16x32_bf16 v[32:35], v[166:169], v[174:177], v[32:35]
	v_mfma_f32_16x16x32_bf16 v[24:27], v[158:161], v[182:185], v[24:27]
	v_mfma_f32_16x16x32_bf16 v[16:19], v[166:169], v[182:185], v[16:19]
	v_mfma_f32_16x16x32_bf16 v[12:15], v[158:161], v[190:193], v[12:15]
	v_mfma_f32_16x16x32_bf16 v[8:11], v[166:169], v[190:193], v[8:11]
	v_mfma_f32_16x16x32_bf16 v[4:7], v[158:161], v[198:201], v[4:7]
	v_mfma_f32_16x16x32_bf16 v[0:3], v[166:169], v[198:201], v[0:3]
	v_mfma_f32_16x16x32_bf16 v[40:43], v[162:165], v[178:181], v[40:43]
	v_mfma_f32_16x16x32_bf16 v[32:35], v[170:173], v[178:181], v[32:35]
	v_mfma_f32_16x16x32_bf16 v[24:27], v[162:165], v[186:189], v[24:27]
	v_mfma_f32_16x16x32_bf16 v[16:19], v[170:173], v[186:189], v[16:19]
	v_mfma_f32_16x16x32_bf16 v[12:15], v[162:165], v[194:197], v[12:15]
	v_mfma_f32_16x16x32_bf16 v[8:11], v[170:173], v[194:197], v[8:11]
	v_mfma_f32_16x16x32_bf16 v[4:7], v[162:165], v[202:205], v[4:7]
	v_mfma_f32_16x16x32_bf16 v[0:3], v[170:173], v[202:205], v[0:3]
	s_barrier
	s_add_i32 s68, 0, 0x18000
	s_add_i32 s69, 0, 0x1c000
	s_add_i32 s67, s67, 0x80000
	s_add_u32 s0, s4, s67
	s_addc_u32 s1, s5, 0
	s_mov_b32 m0, s25
	v_lshl_add_u64 v[206:207], s[0:1], 0, v[128:129]
	global_load_lds_dwordx4 v[206:207], off
	v_lshl_add_u64 v[206:207], s[0:1], 0, v[130:131]
	s_mov_b32 m0, s33
	s_nop 0
	global_load_lds_dwordx4 v[206:207], off
	v_add_u32_e32 v154, s68, v138
	v_add_u32_e32 v170, s69, v138
	ds_read_b128 v[142:145], v154
	ds_read_b128 v[146:149], v154 offset:1024
	ds_read_b128 v[150:153], v154 offset:2048
	ds_read_b128 v[154:157], v154 offset:3072
	ds_read_b128 v[158:161], v170
	ds_read_b128 v[162:165], v170 offset:1024
	ds_read_b128 v[166:169], v170 offset:2048
	ds_read_b128 v[170:173], v170 offset:3072
	ds_read_b128 v[174:177], v141 offset:32768
	ds_read_b128 v[178:181], v141 offset:33792
	ds_read_b128 v[182:185], v141 offset:34816
	ds_read_b128 v[186:189], v141 offset:35840
	ds_read_b128 v[190:193], v141 offset:36864
	ds_read_b128 v[194:197], v141 offset:37888
	ds_read_b128 v[198:201], v141 offset:38912
	ds_read_b128 v[202:205], v141 offset:39936
	s_waitcnt vmcnt(8)
	s_waitcnt lgkmcnt(0)
	s_barrier
	s_waitcnt lgkmcnt(0)
	v_mfma_f32_16x16x32_bf16 v[124:127], v[142:145], v[174:177], v[124:127]
	v_mfma_f32_16x16x32_bf16 v[120:123], v[150:153], v[174:177], v[120:123]
	v_mfma_f32_16x16x32_bf16 v[116:119], v[142:145], v[182:185], v[116:119]
	v_mfma_f32_16x16x32_bf16 v[112:115], v[150:153], v[182:185], v[112:115]
	v_mfma_f32_16x16x32_bf16 v[108:111], v[142:145], v[190:193], v[108:111]
	v_mfma_f32_16x16x32_bf16 v[100:103], v[150:153], v[190:193], v[100:103]
	v_mfma_f32_16x16x32_bf16 v[92:95], v[142:145], v[198:201], v[92:95]
	v_mfma_f32_16x16x32_bf16 v[84:87], v[150:153], v[198:201], v[84:87]
	v_mfma_f32_16x16x32_bf16 v[124:127], v[146:149], v[178:181], v[124:127]
	v_mfma_f32_16x16x32_bf16 v[120:123], v[154:157], v[178:181], v[120:123]
	v_mfma_f32_16x16x32_bf16 v[116:119], v[146:149], v[186:189], v[116:119]
	v_mfma_f32_16x16x32_bf16 v[112:115], v[154:157], v[186:189], v[112:115]
	v_mfma_f32_16x16x32_bf16 v[108:111], v[146:149], v[194:197], v[108:111]
	v_mfma_f32_16x16x32_bf16 v[100:103], v[154:157], v[194:197], v[100:103]
	v_mfma_f32_16x16x32_bf16 v[92:95], v[146:149], v[202:205], v[92:95]
	v_mfma_f32_16x16x32_bf16 v[84:87], v[154:157], v[202:205], v[84:87]
	v_mfma_f32_16x16x32_bf16 v[104:107], v[158:161], v[174:177], v[104:107]
	v_mfma_f32_16x16x32_bf16 v[96:99], v[166:169], v[174:177], v[96:99]
	v_mfma_f32_16x16x32_bf16 v[88:91], v[158:161], v[182:185], v[88:91]
	v_mfma_f32_16x16x32_bf16 v[80:83], v[166:169], v[182:185], v[80:83]
	v_mfma_f32_16x16x32_bf16 v[76:79], v[158:161], v[190:193], v[76:79]
	v_mfma_f32_16x16x32_bf16 v[72:75], v[166:169], v[190:193], v[72:75]
	v_mfma_f32_16x16x32_bf16 v[68:71], v[158:161], v[198:201], v[68:71]
	v_mfma_f32_16x16x32_bf16 v[64:67], v[166:169], v[198:201], v[64:67]
	v_mfma_f32_16x16x32_bf16 v[104:107], v[162:165], v[178:181], v[104:107]
	v_mfma_f32_16x16x32_bf16 v[96:99], v[170:173], v[178:181], v[96:99]
	v_mfma_f32_16x16x32_bf16 v[88:91], v[162:165], v[186:189], v[88:91]
	v_mfma_f32_16x16x32_bf16 v[80:83], v[170:173], v[186:189], v[80:83]
	v_mfma_f32_16x16x32_bf16 v[76:79], v[162:165], v[194:197], v[76:79]
	v_mfma_f32_16x16x32_bf16 v[72:75], v[170:173], v[194:197], v[72:75]
	v_mfma_f32_16x16x32_bf16 v[68:71], v[162:165], v[202:205], v[68:71]
	v_mfma_f32_16x16x32_bf16 v[64:67], v[170:173], v[202:205], v[64:67]
	s_barrier
; template <class Epi, class Sched, class Hook = NoHook>
; __device__ __forceinline__ void gemm_phase_w(LAS unsigned char* lds, const Sched& S, const Epi& E, int wave_id, const Hook& HK = Hook()) {
;     ...
;         if constexpr (!SEG2) {
;             for (int tt = 0; tt < nt; tt += 2) {
;                 if constexpr (GATHER) { if (tt == nt - 2) {
;                     if (has_next) { gnxt_00 = S.grow_l(nxt, lds, nbuf, R0) + (unsigned)(C0 * 2); gnxt_01 = S.grow_l(nxt, lds, nbuf, R1) + (unsigned)(C1 * 2); gnxt_10 = S.grow_l(nxt, lds, nbuf, 128 + R0) + (unsigned)(C0 * 2); gnxt_11 = S.grow_l(nxt, lds, nbuf, 128 + R1) + (unsigned)(C1 * 2); }
;                     else { gnxt_00 = gcur_00; gnxt_01 = gcur_01; gnxt_10 = gcur_10; gnxt_11 = gcur_11; } } }
;                 PG_TRIP(tt, false, false, false);
	s_bitset1_b32 s61, 7
	s_add_i32 s0, s61, s60
	s_ashr_i32 s1, s0, 31
	s_add_u32 s0, s6, s0
	s_addc_u32 s1, s7, s1
	s_add_i32 s60, s68, s27
	v_lshl_add_u64 v[206:207], s[0:1], 0, v[128:129]
	s_mov_b32 m0, s60
	s_nop 0
	global_load_lds_dwordx4 v[206:207], off
	v_lshl_add_u64 v[206:207], s[0:1], 0, v[130:131]
	s_add_i32 s0, s61, s66
	s_add_i32 m0, s60, 0x2000
	s_ashr_i32 s1, s0, 31
	s_add_u32 s0, s6, s0
	s_addc_u32 s1, s7, s1
	s_add_i32 s60, s69, s27
	global_load_lds_dwordx4 v[206:207], off
	v_lshl_add_u64 v[206:207], s[0:1], 0, v[128:129]
	s_mov_b32 m0, s60
	s_add_i32 s61, s61, s19
	global_load_lds_dwordx4 v[206:207], off
	s_add_i32 m0, s60, 0x2000
	v_lshl_add_u64 v[206:207], s[0:1], 0, v[130:131]
	s_add_u32 s0, s4, s61
	s_addc_u32 s1, s5, 0
	global_load_lds_dwordx4 v[206:207], off
	v_lshl_add_u64 v[206:207], s[0:1], 0, v[128:129]
	s_mov_b32 m0, s34
	s_nop 0
	global_load_lds_dwordx4 v[206:207], off
	v_lshl_add_u64 v[206:207], s[0:1], 0, v[130:131]
	s_mov_b32 m0, s35
	s_nop 0
	global_load_lds_dwordx4 v[206:207], off
	ds_read_b128 v[174:177], v141 offset:49152
	ds_read_b128 v[178:181], v141 offset:50176
	ds_read_b128 v[182:185], v141 offset:51200
	ds_read_b128 v[186:189], v141 offset:52224
	ds_read_b128 v[190:193], v141 offset:53248
	ds_read_b128 v[194:197], v141 offset:54272
	ds_read_b128 v[198:201], v141 offset:55296
	ds_read_b128 v[202:205], v141 offset:56320
	s_waitcnt vmcnt(8)
	s_waitcnt lgkmcnt(0)
	s_barrier
	s_waitcnt lgkmcnt(0)
	v_mfma_f32_16x16x32_bf16 v[60:63], v[142:145], v[174:177], v[60:63]
	v_mfma_f32_16x16x32_bf16 v[56:59], v[150:153], v[174:177], v[56:59]
	v_mfma_f32_16x16x32_bf16 v[52:55], v[142:145], v[182:185], v[52:55]
	v_mfma_f32_16x16x32_bf16 v[48:51], v[150:153], v[182:185], v[48:51]
	v_mfma_f32_16x16x32_bf16 v[44:47], v[142:145], v[190:193], v[44:47]
	v_mfma_f32_16x16x32_bf16 v[36:39], v[150:153], v[190:193], v[36:39]
	v_mfma_f32_16x16x32_bf16 v[28:31], v[142:145], v[198:201], v[28:31]
	v_mfma_f32_16x16x32_bf16 v[20:23], v[150:153], v[198:201], v[20:23]
	v_mfma_f32_16x16x32_bf16 v[60:63], v[146:149], v[178:181], v[60:63]
	v_mfma_f32_16x16x32_bf16 v[56:59], v[154:157], v[178:181], v[56:59]
	v_mfma_f32_16x16x32_bf16 v[52:55], v[146:149], v[186:189], v[52:55]
	v_mfma_f32_16x16x32_bf16 v[48:51], v[154:157], v[186:189], v[48:51]
	v_mfma_f32_16x16x32_bf16 v[44:47], v[146:149], v[194:197], v[44:47]
	v_mfma_f32_16x16x32_bf16 v[36:39], v[154:157], v[194:197], v[36:39]
	v_mfma_f32_16x16x32_bf16 v[28:31], v[146:149], v[202:205], v[28:31]
	v_mfma_f32_16x16x32_bf16 v[20:23], v[154:157], v[202:205], v[20:23]
	v_mfma_f32_16x16x32_bf16 v[40:43], v[158:161], v[174:177], v[40:43]
	v_mfma_f32_16x16x32_bf16 v[32:35], v[166:169], v[174:177], v[32:35]
	v_mfma_f32_16x16x32_bf16 v[24:27], v[158:161], v[182:185], v[24:27]
	v_mfma_f32_16x16x32_bf16 v[16:19], v[166:169], v[182:185], v[16:19]
	v_mfma_f32_16x16x32_bf16 v[12:15], v[158:161], v[190:193], v[12:15]
	v_mfma_f32_16x16x32_bf16 v[8:11], v[166:169], v[190:193], v[8:11]
	v_mfma_f32_16x16x32_bf16 v[4:7], v[158:161], v[198:201], v[4:7]
	v_mfma_f32_16x16x32_bf16 v[0:3], v[166:169], v[198:201], v[0:3]
	v_mfma_f32_16x16x32_bf16 v[40:43], v[162:165], v[178:181], v[40:43]
	v_mfma_f32_16x16x32_bf16 v[32:35], v[170:173], v[178:181], v[32:35]
	v_mfma_f32_16x16x32_bf16 v[24:27], v[162:165], v[186:189], v[24:27]
	v_mfma_f32_16x16x32_bf16 v[16:19], v[170:173], v[186:189], v[16:19]
	v_mfma_f32_16x16x32_bf16 v[12:15], v[162:165], v[194:197], v[12:15]
	v_mfma_f32_16x16x32_bf16 v[8:11], v[170:173], v[194:197], v[8:11]
	v_mfma_f32_16x16x32_bf16 v[4:7], v[162:165], v[202:205], v[4:7]
	v_mfma_f32_16x16x32_bf16 v[0:3], v[170:173], v[202:205], v[0:3]
	s_barrier
	s_addk_i32 s10, 0x100
	s_add_i32 s18, s18, 2
	s_cmp_gt_u32 s18, 29
	s_cbranch_scc0 .LBB0_386
	s_and_b64 vcc, exec, s[14:15]
	s_cbranch_vccz .LBB0_389
	s_barrier

.LBB0_654:
	s_add_i32 s40, s39, s18
	s_add_u32 s42, s4, s40
	s_addc_u32 s43, s5, 0
	s_add_i32 m0, s23, 0xc000
	s_add_i32 s44, s23, 0xe000
	s_add_i32 s45, s18, 0xfff80080
	s_cmp_eq_u32 s19, 28
	s_cselect_b32 s40, s35, s39
	s_cselect_b32 s41, s34, s38
	v_lshl_add_u64 v[204:205], s[42:43], 0, v[144:145]
	global_load_lds_dwordx4 v[204:205], off
	v_lshl_add_u64 v[204:205], s[42:43], 0, v[146:147]
	s_mov_b32 m0, s44
	s_nop 0
	global_load_lds_dwordx4 v[204:205], off
	ds_read_b128 v[116:119], v157
	ds_read_b128 v[120:123], v157 offset:1024
	ds_read_b128 v[128:131], v157 offset:2048
	ds_read_b128 v[132:135], v157 offset:3072
	ds_read_b128 v[150:153], v158
	ds_read_b128 v[160:163], v158 offset:1024
	ds_read_b128 v[164:167], v158 offset:2048
	ds_read_b128 v[168:171], v158 offset:3072
	ds_read_b128 v[172:175], v159
	ds_read_b128 v[176:179], v159 offset:1024
	ds_read_b128 v[180:183], v159 offset:2048
	ds_read_b128 v[184:187], v159 offset:3072
	ds_read_b128 v[188:191], v159 offset:4096
	ds_read_b128 v[192:195], v159 offset:5120
	ds_read_b128 v[196:199], v159 offset:6144
	ds_read_b128 v[200:203], v159 offset:7168
	s_waitcnt vmcnt(8)
	s_waitcnt lgkmcnt(0)
	s_barrier
	s_waitcnt lgkmcnt(0)
	v_mfma_f32_16x16x32_bf16 v[140:143], v[116:119], v[172:175], v[140:143]
	v_mfma_f32_16x16x32_bf16 v[136:139], v[128:131], v[172:175], v[136:139]
	v_mfma_f32_16x16x32_bf16 v[112:115], v[116:119], v[180:183], v[112:115]
	v_mfma_f32_16x16x32_bf16 v[104:107], v[128:131], v[180:183], v[104:107]
	v_mfma_f32_16x16x32_bf16 v[96:99], v[116:119], v[188:191], v[96:99]
	v_mfma_f32_16x16x32_bf16 v[88:91], v[128:131], v[188:191], v[88:91]
	v_mfma_f32_16x16x32_bf16 v[80:83], v[116:119], v[196:199], v[80:83]
	v_mfma_f32_16x16x32_bf16 v[72:75], v[128:131], v[196:199], v[72:75]
	v_mfma_f32_16x16x32_bf16 v[140:143], v[120:123], v[176:179], v[140:143]
	v_mfma_f32_16x16x32_bf16 v[136:139], v[132:135], v[176:179], v[136:139]
	v_mfma_f32_16x16x32_bf16 v[112:115], v[120:123], v[184:187], v[112:115]
	v_mfma_f32_16x16x32_bf16 v[104:107], v[132:135], v[184:187], v[104:107]
	v_mfma_f32_16x16x32_bf16 v[96:99], v[120:123], v[192:195], v[96:99]
	v_mfma_f32_16x16x32_bf16 v[88:91], v[132:135], v[192:195], v[88:91]
	v_mfma_f32_16x16x32_bf16 v[80:83], v[120:123], v[200:203], v[80:83]
	v_mfma_f32_16x16x32_bf16 v[72:75], v[132:135], v[200:203], v[72:75]
	v_mfma_f32_16x16x32_bf16 v[124:127], v[150:153], v[172:175], v[124:127]
	v_mfma_f32_16x16x32_bf16 v[108:111], v[164:167], v[172:175], v[108:111]
	v_mfma_f32_16x16x32_bf16 v[100:103], v[150:153], v[180:183], v[100:103]
	v_mfma_f32_16x16x32_bf16 v[92:95], v[164:167], v[180:183], v[92:95]
	v_mfma_f32_16x16x32_bf16 v[84:87], v[150:153], v[188:191], v[84:87]
	v_mfma_f32_16x16x32_bf16 v[76:79], v[164:167], v[188:191], v[76:79]
	v_mfma_f32_16x16x32_bf16 v[68:71], v[150:153], v[196:199], v[68:71]
	v_mfma_f32_16x16x32_bf16 v[64:67], v[164:167], v[196:199], v[64:67]
	v_mfma_f32_16x16x32_bf16 v[124:127], v[160:163], v[176:179], v[124:127]
	v_mfma_f32_16x16x32_bf16 v[108:111], v[168:171], v[176:179], v[108:111]
	v_mfma_f32_16x16x32_bf16 v[100:103], v[160:163], v[184:187], v[100:103]
	v_mfma_f32_16x16x32_bf16 v[92:95], v[168:171], v[184:187], v[92:95]
	v_mfma_f32_16x16x32_bf16 v[84:87], v[160:163], v[192:195], v[84:87]
	v_mfma_f32_16x16x32_bf16 v[76:79], v[168:171], v[192:195], v[76:79]
	v_mfma_f32_16x16x32_bf16 v[68:71], v[160:163], v[200:203], v[68:71]
	v_mfma_f32_16x16x32_bf16 v[64:67], v[168:171], v[200:203], v[64:67]
	s_barrier
	s_cselect_b32 s44, 0, s45
	s_add_i32 s42, s44, s41
	s_ashr_i32 s43, s42, 31
	s_add_u32 s42, s20, s42
	s_addc_u32 s43, s21, s43
	s_add_i32 s45, s29, s22
	v_lshl_add_u64 v[204:205], s[42:43], 0, v[144:145]
	s_mov_b32 m0, s45
	s_nop 0
	global_load_lds_dwordx4 v[204:205], off
	s_add_i32 m0, s45, 0x2000
	s_add_i32 s45, s41, 0x80000
	v_lshl_add_u64 v[204:205], s[42:43], 0, v[146:147]
	s_add_i32 s42, s45, s44
	s_ashr_i32 s43, s42, 31
	s_add_u32 s42, s20, s42
	s_addc_u32 s43, s21, s43
	s_add_i32 s58, s30, s22
	global_load_lds_dwordx4 v[204:205], off
	v_lshl_add_u64 v[204:205], s[42:43], 0, v[144:145]
	s_mov_b32 m0, s58
	s_nop 0
	global_load_lds_dwordx4 v[204:205], off
	s_add_i32 m0, s58, 0x2000
	s_add_i32 s58, s44, s40
	v_lshl_add_u64 v[204:205], s[42:43], 0, v[146:147]
	s_add_u32 s42, s4, s58
	s_addc_u32 s43, s5, 0
	global_load_lds_dwordx4 v[204:205], off
	v_lshl_add_u64 v[204:205], s[42:43], 0, v[144:145]
	s_mov_b32 m0, s23
	s_nop 0
	global_load_lds_dwordx4 v[204:205], off
	v_lshl_add_u64 v[204:205], s[42:43], 0, v[146:147]
	s_mov_b32 m0, s24
	s_nop 0
	global_load_lds_dwordx4 v[204:205], off
	ds_read_b128 v[172:175], v159 offset:16384
	ds_read_b128 v[176:179], v159 offset:17408
	ds_read_b128 v[180:183], v159 offset:18432
	ds_read_b128 v[184:187], v159 offset:19456
	ds_read_b128 v[188:191], v159 offset:20480
	ds_read_b128 v[192:195], v159 offset:21504
	ds_read_b128 v[196:199], v159 offset:22528
	ds_read_b128 v[200:203], v159 offset:23552
	s_waitcnt vmcnt(8)
	s_waitcnt lgkmcnt(0)
	s_barrier
	s_waitcnt lgkmcnt(0)
	v_mfma_f32_16x16x32_bf16 v[60:63], v[116:119], v[172:175], v[60:63]
	v_mfma_f32_16x16x32_bf16 v[56:59], v[128:131], v[172:175], v[56:59]
	v_mfma_f32_16x16x32_bf16 v[48:51], v[116:119], v[180:183], v[48:51]
	v_mfma_f32_16x16x32_bf16 v[40:43], v[128:131], v[180:183], v[40:43]
	v_mfma_f32_16x16x32_bf16 v[32:35], v[116:119], v[188:191], v[32:35]
	v_mfma_f32_16x16x32_bf16 v[24:27], v[128:131], v[188:191], v[24:27]
	v_mfma_f32_16x16x32_bf16 v[16:19], v[116:119], v[196:199], v[16:19]
	v_mfma_f32_16x16x32_bf16 v[8:11], v[128:131], v[196:199], v[8:11]
	v_mfma_f32_16x16x32_bf16 v[60:63], v[120:123], v[176:179], v[60:63]
	v_mfma_f32_16x16x32_bf16 v[56:59], v[132:135], v[176:179], v[56:59]
	v_mfma_f32_16x16x32_bf16 v[48:51], v[120:123], v[184:187], v[48:51]
	v_mfma_f32_16x16x32_bf16 v[40:43], v[132:135], v[184:187], v[40:43]
	v_mfma_f32_16x16x32_bf16 v[32:35], v[120:123], v[192:195], v[32:35]
	v_mfma_f32_16x16x32_bf16 v[24:27], v[132:135], v[192:195], v[24:27]
	v_mfma_f32_16x16x32_bf16 v[16:19], v[120:123], v[200:203], v[16:19]
	v_mfma_f32_16x16x32_bf16 v[8:11], v[132:135], v[200:203], v[8:11]
	v_mfma_f32_16x16x32_bf16 v[52:55], v[150:153], v[172:175], v[52:55]
	v_mfma_f32_16x16x32_bf16 v[44:47], v[164:167], v[172:175], v[44:47]
	v_mfma_f32_16x16x32_bf16 v[36:39], v[150:153], v[180:183], v[36:39]
	v_mfma_f32_16x16x32_bf16 v[28:31], v[164:167], v[180:183], v[28:31]
	v_mfma_f32_16x16x32_bf16 v[20:23], v[150:153], v[188:191], v[20:23]
	v_mfma_f32_16x16x32_bf16 v[12:15], v[164:167], v[188:191], v[12:15]
	v_mfma_f32_16x16x32_bf16 v[4:7], v[150:153], v[196:199], v[4:7]
	v_mfma_f32_16x16x32_bf16 v[0:3], v[164:167], v[196:199], v[0:3]
	v_mfma_f32_16x16x32_bf16 v[52:55], v[160:163], v[176:179], v[52:55]
	v_mfma_f32_16x16x32_bf16 v[44:47], v[168:171], v[176:179], v[44:47]
	v_mfma_f32_16x16x32_bf16 v[36:39], v[160:163], v[184:187], v[36:39]
	v_mfma_f32_16x16x32_bf16 v[28:31], v[168:171], v[184:187], v[28:31]
	v_mfma_f32_16x16x32_bf16 v[20:23], v[160:163], v[192:195], v[20:23]
	v_mfma_f32_16x16x32_bf16 v[12:15], v[168:171], v[192:195], v[12:15]
	v_mfma_f32_16x16x32_bf16 v[4:7], v[160:163], v[200:203], v[4:7]
	v_mfma_f32_16x16x32_bf16 v[0:3], v[168:171], v[200:203], v[0:3]
	s_barrier
	s_add_i32 s59, 0, 0x18000
	s_add_i32 s60, 0, 0x1c000
	s_add_i32 s58, s58, 0x80000
	s_add_u32 s42, s4, s58
	s_addc_u32 s43, s5, 0
	s_mov_b32 m0, s25
	v_lshl_add_u64 v[204:205], s[42:43], 0, v[144:145]
	global_load_lds_dwordx4 v[204:205], off
	v_lshl_add_u64 v[204:205], s[42:43], 0, v[146:147]
	s_mov_b32 m0, s26
	s_nop 0
	global_load_lds_dwordx4 v[204:205], off
	v_add_u32_e32 v132, s59, v155
	v_add_u32_e32 v168, s60, v155
	ds_read_b128 v[116:119], v132
	ds_read_b128 v[120:123], v132 offset:1024
	ds_read_b128 v[128:131], v132 offset:2048
	ds_read_b128 v[132:135], v132 offset:3072
	ds_read_b128 v[150:153], v168
	ds_read_b128 v[160:163], v168 offset:1024
	ds_read_b128 v[164:167], v168 offset:2048
	ds_read_b128 v[168:171], v168 offset:3072
	ds_read_b128 v[172:175], v159 offset:32768
	ds_read_b128 v[176:179], v159 offset:33792
	ds_read_b128 v[180:183], v159 offset:34816
	ds_read_b128 v[184:187], v159 offset:35840
	ds_read_b128 v[188:191], v159 offset:36864
	ds_read_b128 v[192:195], v159 offset:37888
	ds_read_b128 v[196:199], v159 offset:38912
	ds_read_b128 v[200:203], v159 offset:39936
	s_waitcnt vmcnt(8)
	s_waitcnt lgkmcnt(0)
	s_barrier
	s_waitcnt lgkmcnt(0)
	v_mfma_f32_16x16x32_bf16 v[140:143], v[116:119], v[172:175], v[140:143]
	v_mfma_f32_16x16x32_bf16 v[136:139], v[128:131], v[172:175], v[136:139]
	v_mfma_f32_16x16x32_bf16 v[112:115], v[116:119], v[180:183], v[112:115]
	v_mfma_f32_16x16x32_bf16 v[104:107], v[128:131], v[180:183], v[104:107]
	v_mfma_f32_16x16x32_bf16 v[96:99], v[116:119], v[188:191], v[96:99]
	v_mfma_f32_16x16x32_bf16 v[88:91], v[128:131], v[188:191], v[88:91]
	v_mfma_f32_16x16x32_bf16 v[80:83], v[116:119], v[196:199], v[80:83]
	v_mfma_f32_16x16x32_bf16 v[72:75], v[128:131], v[196:199], v[72:75]
	v_mfma_f32_16x16x32_bf16 v[140:143], v[120:123], v[176:179], v[140:143]
	v_mfma_f32_16x16x32_bf16 v[136:139], v[132:135], v[176:179], v[136:139]
	v_mfma_f32_16x16x32_bf16 v[112:115], v[120:123], v[184:187], v[112:115]
	v_mfma_f32_16x16x32_bf16 v[104:107], v[132:135], v[184:187], v[104:107]
	v_mfma_f32_16x16x32_bf16 v[96:99], v[120:123], v[192:195], v[96:99]
	v_mfma_f32_16x16x32_bf16 v[88:91], v[132:135], v[192:195], v[88:91]
	v_mfma_f32_16x16x32_bf16 v[80:83], v[120:123], v[200:203], v[80:83]
	v_mfma_f32_16x16x32_bf16 v[72:75], v[132:135], v[200:203], v[72:75]
	v_mfma_f32_16x16x32_bf16 v[124:127], v[150:153], v[172:175], v[124:127]
	v_mfma_f32_16x16x32_bf16 v[108:111], v[164:167], v[172:175], v[108:111]
	v_mfma_f32_16x16x32_bf16 v[100:103], v[150:153], v[180:183], v[100:103]
	v_mfma_f32_16x16x32_bf16 v[92:95], v[164:167], v[180:183], v[92:95]
	v_mfma_f32_16x16x32_bf16 v[84:87], v[150:153], v[188:191], v[84:87]
	v_mfma_f32_16x16x32_bf16 v[76:79], v[164:167], v[188:191], v[76:79]
	v_mfma_f32_16x16x32_bf16 v[68:71], v[150:153], v[196:199], v[68:71]
	v_mfma_f32_16x16x32_bf16 v[64:67], v[164:167], v[196:199], v[64:67]
	v_mfma_f32_16x16x32_bf16 v[124:127], v[160:163], v[176:179], v[124:127]
	v_mfma_f32_16x16x32_bf16 v[108:111], v[168:171], v[176:179], v[108:111]
	v_mfma_f32_16x16x32_bf16 v[100:103], v[160:163], v[184:187], v[100:103]
	v_mfma_f32_16x16x32_bf16 v[92:95], v[168:171], v[184:187], v[92:95]
	v_mfma_f32_16x16x32_bf16 v[84:87], v[160:163], v[192:195], v[84:87]
	v_mfma_f32_16x16x32_bf16 v[76:79], v[168:171], v[192:195], v[76:79]
	v_mfma_f32_16x16x32_bf16 v[68:71], v[160:163], v[200:203], v[68:71]
	v_mfma_f32_16x16x32_bf16 v[64:67], v[168:171], v[200:203], v[64:67]
	s_barrier
; template <class Epi, class Sched, class Hook = NoHook>
; __device__ __forceinline__ void gemm_phase_w(LAS unsigned char* lds, const Sched& S, const Epi& E, int wave_id, const Hook& HK = Hook()) {
;     ...
;         if constexpr (!SEG2) {
;             for (int tt = 0; tt < nt; tt += 2) {
	s_bitset1_b32 s44, 7
	s_add_i32 s41, s44, s41
	s_ashr_i32 s43, s41, 31
	s_add_u32 s42, s20, s41
	s_addc_u32 s43, s21, s43
	s_add_i32 s41, s59, s22
	v_lshl_add_u64 v[204:205], s[42:43], 0, v[144:145]
	s_mov_b32 m0, s41
	s_nop 0
	global_load_lds_dwordx4 v[204:205], off
	s_add_i32 m0, s41, 0x2000
	s_add_i32 s41, s44, s45
	v_lshl_add_u64 v[204:205], s[42:43], 0, v[146:147]
	s_ashr_i32 s43, s41, 31
	s_add_u32 s42, s20, s41
	s_addc_u32 s43, s21, s43
	s_add_i32 s41, s60, s22
	global_load_lds_dwordx4 v[204:205], off
	v_lshl_add_u64 v[204:205], s[42:43], 0, v[144:145]
	s_mov_b32 m0, s41
	s_add_i32 s44, s44, s40
	global_load_lds_dwordx4 v[204:205], off
	s_add_i32 m0, s41, 0x2000
	s_add_u32 s40, s4, s44
	v_lshl_add_u64 v[204:205], s[42:43], 0, v[146:147]
	s_addc_u32 s41, s5, 0
	global_load_lds_dwordx4 v[204:205], off
	v_lshl_add_u64 v[204:205], s[40:41], 0, v[144:145]
	s_mov_b32 m0, s28
	s_nop 0
	global_load_lds_dwordx4 v[204:205], off
	v_lshl_add_u64 v[204:205], s[40:41], 0, v[146:147]
	s_mov_b32 m0, s6
	s_nop 0
	global_load_lds_dwordx4 v[204:205], off
	ds_read_b128 v[172:175], v159 offset:49152
	ds_read_b128 v[176:179], v159 offset:50176
	ds_read_b128 v[180:183], v159 offset:51200
	ds_read_b128 v[184:187], v159 offset:52224
	ds_read_b128 v[188:191], v159 offset:53248
	ds_read_b128 v[192:195], v159 offset:54272
	ds_read_b128 v[196:199], v159 offset:55296
	ds_read_b128 v[200:203], v159 offset:56320
	s_waitcnt vmcnt(8)
	s_waitcnt lgkmcnt(0)
	s_barrier
	s_waitcnt lgkmcnt(0)
	v_mfma_f32_16x16x32_bf16 v[60:63], v[116:119], v[172:175], v[60:63]
	v_mfma_f32_16x16x32_bf16 v[56:59], v[128:131], v[172:175], v[56:59]
	v_mfma_f32_16x16x32_bf16 v[48:51], v[116:119], v[180:183], v[48:51]
	v_mfma_f32_16x16x32_bf16 v[40:43], v[128:131], v[180:183], v[40:43]
	v_mfma_f32_16x16x32_bf16 v[32:35], v[116:119], v[188:191], v[32:35]
	v_mfma_f32_16x16x32_bf16 v[24:27], v[128:131], v[188:191], v[24:27]
	v_mfma_f32_16x16x32_bf16 v[16:19], v[116:119], v[196:199], v[16:19]
	v_mfma_f32_16x16x32_bf16 v[8:11], v[128:131], v[196:199], v[8:11]
	v_mfma_f32_16x16x32_bf16 v[60:63], v[120:123], v[176:179], v[60:63]
	v_mfma_f32_16x16x32_bf16 v[56:59], v[132:135], v[176:179], v[56:59]
	v_mfma_f32_16x16x32_bf16 v[48:51], v[120:123], v[184:187], v[48:51]
	v_mfma_f32_16x16x32_bf16 v[40:43], v[132:135], v[184:187], v[40:43]
	v_mfma_f32_16x16x32_bf16 v[32:35], v[120:123], v[192:195], v[32:35]
	v_mfma_f32_16x16x32_bf16 v[24:27], v[132:135], v[192:195], v[24:27]
	v_mfma_f32_16x16x32_bf16 v[16:19], v[120:123], v[200:203], v[16:19]
	v_mfma_f32_16x16x32_bf16 v[8:11], v[132:135], v[200:203], v[8:11]
	v_mfma_f32_16x16x32_bf16 v[52:55], v[150:153], v[172:175], v[52:55]
	v_mfma_f32_16x16x32_bf16 v[44:47], v[164:167], v[172:175], v[44:47]
	v_mfma_f32_16x16x32_bf16 v[36:39], v[150:153], v[180:183], v[36:39]
	v_mfma_f32_16x16x32_bf16 v[28:31], v[164:167], v[180:183], v[28:31]
	v_mfma_f32_16x16x32_bf16 v[20:23], v[150:153], v[188:191], v[20:23]
	v_mfma_f32_16x16x32_bf16 v[12:15], v[164:167], v[188:191], v[12:15]
	v_mfma_f32_16x16x32_bf16 v[4:7], v[150:153], v[196:199], v[4:7]
	v_mfma_f32_16x16x32_bf16 v[0:3], v[164:167], v[196:199], v[0:3]
	v_mfma_f32_16x16x32_bf16 v[52:55], v[160:163], v[176:179], v[52:55]
	v_mfma_f32_16x16x32_bf16 v[44:47], v[168:171], v[176:179], v[44:47]
	v_mfma_f32_16x16x32_bf16 v[36:39], v[160:163], v[184:187], v[36:39]
	v_mfma_f32_16x16x32_bf16 v[28:31], v[168:171], v[184:187], v[28:31]
	v_mfma_f32_16x16x32_bf16 v[20:23], v[160:163], v[192:195], v[20:23]
	v_mfma_f32_16x16x32_bf16 v[12:15], v[168:171], v[192:195], v[12:15]
	v_mfma_f32_16x16x32_bf16 v[4:7], v[160:163], v[200:203], v[4:7]
	v_mfma_f32_16x16x32_bf16 v[0:3], v[168:171], v[200:203], v[0:3]
	s_barrier
	s_addk_i32 s18, 0x100
	s_add_i32 s19, s19, 2
	s_cmp_gt_u32 s19, 29
	s_cbranch_scc0 .LBB0_654
	s_and_b64 vcc, exec, s[14:15]
	s_cbranch_vccz .LBB0_657
	s_barrier

.LBB0_1194:
	s_add_i32 s22, s68, s12
	s_add_u32 s36, s28, s22
	s_addc_u32 s37, s29, 0
	s_add_i32 m0, s26, 0xc000
	s_add_i32 s71, s26, 0xe000
	s_add_i32 s72, s12, 0xfffc0080
	s_cmp_eq_u32 s19, 12
	s_cselect_b32 s22, s63, s68
	s_cselect_b32 s23, s66, s69
	v_lshl_add_u64 v[224:225], s[36:37], 0, v[130:131]
	global_load_lds_dwordx4 v[224:225], off
	v_lshl_add_u64 v[224:225], s[36:37], 0, v[132:133]
	s_mov_b32 m0, s71
	s_nop 0
	global_load_lds_dwordx4 v[224:225], off
	ds_read_b128 v[160:163], v156
	ds_read_b128 v[164:167], v156 offset:1024
	ds_read_b128 v[168:171], v156 offset:2048
	ds_read_b128 v[172:175], v156 offset:3072
	ds_read_b128 v[176:179], v157
	ds_read_b128 v[180:183], v157 offset:1024
	ds_read_b128 v[184:187], v157 offset:2048
	ds_read_b128 v[188:191], v157 offset:3072
	ds_read_b128 v[192:195], v158
	ds_read_b128 v[196:199], v158 offset:1024
	ds_read_b128 v[200:203], v158 offset:2048
	ds_read_b128 v[204:207], v158 offset:3072
	ds_read_b128 v[208:211], v158 offset:4096
	ds_read_b128 v[212:215], v158 offset:5120
	ds_read_b128 v[216:219], v158 offset:6144
	ds_read_b128 v[220:223], v158 offset:7168
	s_waitcnt vmcnt(8)
	s_waitcnt lgkmcnt(0)
	s_barrier
	s_waitcnt lgkmcnt(0)
	v_mfma_f32_16x16x32_bf16 v[124:127], v[160:163], v[192:195], v[124:127]
	v_mfma_f32_16x16x32_bf16 v[120:123], v[168:171], v[192:195], v[120:123]
	v_mfma_f32_16x16x32_bf16 v[108:111], v[160:163], v[200:203], v[108:111]
	v_mfma_f32_16x16x32_bf16 v[104:107], v[168:171], v[200:203], v[104:107]
	v_mfma_f32_16x16x32_bf16 v[92:95], v[160:163], v[208:211], v[92:95]
	v_mfma_f32_16x16x32_bf16 v[88:91], v[168:171], v[208:211], v[88:91]
	v_mfma_f32_16x16x32_bf16 v[76:79], v[160:163], v[216:219], v[76:79]
	v_mfma_f32_16x16x32_bf16 v[72:75], v[168:171], v[216:219], v[72:75]
	v_mfma_f32_16x16x32_bf16 v[124:127], v[164:167], v[196:199], v[124:127]
	v_mfma_f32_16x16x32_bf16 v[120:123], v[172:175], v[196:199], v[120:123]
	v_mfma_f32_16x16x32_bf16 v[108:111], v[164:167], v[204:207], v[108:111]
	v_mfma_f32_16x16x32_bf16 v[104:107], v[172:175], v[204:207], v[104:107]
	v_mfma_f32_16x16x32_bf16 v[92:95], v[164:167], v[212:215], v[92:95]
	v_mfma_f32_16x16x32_bf16 v[88:91], v[172:175], v[212:215], v[88:91]
	v_mfma_f32_16x16x32_bf16 v[76:79], v[164:167], v[220:223], v[76:79]
	v_mfma_f32_16x16x32_bf16 v[72:75], v[172:175], v[220:223], v[72:75]
	v_mfma_f32_16x16x32_bf16 v[116:119], v[176:179], v[192:195], v[116:119]
	v_mfma_f32_16x16x32_bf16 v[112:115], v[184:187], v[192:195], v[112:115]
	v_mfma_f32_16x16x32_bf16 v[100:103], v[176:179], v[200:203], v[100:103]
	v_mfma_f32_16x16x32_bf16 v[96:99], v[184:187], v[200:203], v[96:99]
	v_mfma_f32_16x16x32_bf16 v[84:87], v[176:179], v[208:211], v[84:87]
	v_mfma_f32_16x16x32_bf16 v[80:83], v[184:187], v[208:211], v[80:83]
	v_mfma_f32_16x16x32_bf16 v[68:71], v[176:179], v[216:219], v[68:71]
	v_mfma_f32_16x16x32_bf16 v[64:67], v[184:187], v[216:219], v[64:67]
	v_mfma_f32_16x16x32_bf16 v[116:119], v[180:183], v[196:199], v[116:119]
	v_mfma_f32_16x16x32_bf16 v[112:115], v[188:191], v[196:199], v[112:115]
	v_mfma_f32_16x16x32_bf16 v[100:103], v[180:183], v[204:207], v[100:103]
	v_mfma_f32_16x16x32_bf16 v[96:99], v[188:191], v[204:207], v[96:99]
	v_mfma_f32_16x16x32_bf16 v[84:87], v[180:183], v[212:215], v[84:87]
	v_mfma_f32_16x16x32_bf16 v[80:83], v[188:191], v[212:215], v[80:83]
	v_mfma_f32_16x16x32_bf16 v[68:71], v[180:183], v[220:223], v[68:71]
	v_mfma_f32_16x16x32_bf16 v[64:67], v[188:191], v[220:223], v[64:67]
	s_barrier
	s_cselect_b32 s71, 0, s72
	s_add_i32 s36, s71, s23
	s_ashr_i32 s37, s36, 31
	s_add_u32 s36, s10, s36
	s_addc_u32 s37, s11, s37
	s_add_i32 s72, s49, s34
	v_lshl_add_u64 v[224:225], s[36:37], 0, v[130:131]
	s_mov_b32 m0, s72
	s_nop 0
	global_load_lds_dwordx4 v[224:225], off
	s_add_i32 m0, s72, 0x2000
	s_add_i32 s72, s23, 0x40000
	v_lshl_add_u64 v[224:225], s[36:37], 0, v[132:133]
	s_add_i32 s36, s72, s71
	s_ashr_i32 s37, s36, 31
	s_add_u32 s36, s10, s36
	s_addc_u32 s37, s11, s37
	s_add_i32 s73, s58, s34
	global_load_lds_dwordx4 v[224:225], off
	v_lshl_add_u64 v[224:225], s[36:37], 0, v[130:131]
	s_mov_b32 m0, s73
	s_nop 0
	global_load_lds_dwordx4 v[224:225], off
	s_add_i32 m0, s73, 0x2000
	s_add_i32 s73, s71, s22
	v_lshl_add_u64 v[224:225], s[36:37], 0, v[132:133]
	s_add_u32 s36, s28, s73
	s_addc_u32 s37, s29, 0
	global_load_lds_dwordx4 v[224:225], off
	v_lshl_add_u64 v[224:225], s[36:37], 0, v[130:131]
	s_mov_b32 m0, s26
	s_nop 0
	global_load_lds_dwordx4 v[224:225], off
	v_lshl_add_u64 v[224:225], s[36:37], 0, v[132:133]
	s_mov_b32 m0, s27
	s_nop 0
	global_load_lds_dwordx4 v[224:225], off
	ds_read_b128 v[192:195], v158 offset:16384
	ds_read_b128 v[196:199], v158 offset:17408
	ds_read_b128 v[200:203], v158 offset:18432
	ds_read_b128 v[204:207], v158 offset:19456
	ds_read_b128 v[208:211], v158 offset:20480
	ds_read_b128 v[212:215], v158 offset:21504
	ds_read_b128 v[216:219], v158 offset:22528
	ds_read_b128 v[220:223], v158 offset:23552
	s_waitcnt vmcnt(8)
	s_waitcnt lgkmcnt(0)
	s_barrier
	s_waitcnt lgkmcnt(0)
	v_mfma_f32_16x16x32_bf16 v[60:63], v[160:163], v[192:195], v[60:63]
	v_mfma_f32_16x16x32_bf16 v[56:59], v[168:171], v[192:195], v[56:59]
	v_mfma_f32_16x16x32_bf16 v[44:47], v[160:163], v[200:203], v[44:47]
	v_mfma_f32_16x16x32_bf16 v[40:43], v[168:171], v[200:203], v[40:43]
	v_mfma_f32_16x16x32_bf16 v[28:31], v[160:163], v[208:211], v[28:31]
	v_mfma_f32_16x16x32_bf16 v[24:27], v[168:171], v[208:211], v[24:27]
	v_mfma_f32_16x16x32_bf16 v[12:15], v[160:163], v[216:219], v[12:15]
	v_mfma_f32_16x16x32_bf16 v[8:11], v[168:171], v[216:219], v[8:11]
	v_mfma_f32_16x16x32_bf16 v[60:63], v[164:167], v[196:199], v[60:63]
	v_mfma_f32_16x16x32_bf16 v[56:59], v[172:175], v[196:199], v[56:59]
	v_mfma_f32_16x16x32_bf16 v[44:47], v[164:167], v[204:207], v[44:47]
	v_mfma_f32_16x16x32_bf16 v[40:43], v[172:175], v[204:207], v[40:43]
	v_mfma_f32_16x16x32_bf16 v[28:31], v[164:167], v[212:215], v[28:31]
	v_mfma_f32_16x16x32_bf16 v[24:27], v[172:175], v[212:215], v[24:27]
	v_mfma_f32_16x16x32_bf16 v[12:15], v[164:167], v[220:223], v[12:15]
	v_mfma_f32_16x16x32_bf16 v[8:11], v[172:175], v[220:223], v[8:11]
	v_mfma_f32_16x16x32_bf16 v[52:55], v[176:179], v[192:195], v[52:55]
	v_mfma_f32_16x16x32_bf16 v[48:51], v[184:187], v[192:195], v[48:51]
	v_mfma_f32_16x16x32_bf16 v[36:39], v[176:179], v[200:203], v[36:39]
	v_mfma_f32_16x16x32_bf16 v[32:35], v[184:187], v[200:203], v[32:35]
	v_mfma_f32_16x16x32_bf16 v[20:23], v[176:179], v[208:211], v[20:23]
	v_mfma_f32_16x16x32_bf16 v[16:19], v[184:187], v[208:211], v[16:19]
	v_mfma_f32_16x16x32_bf16 v[4:7], v[176:179], v[216:219], v[4:7]
	v_mfma_f32_16x16x32_bf16 v[0:3], v[184:187], v[216:219], v[0:3]
	v_mfma_f32_16x16x32_bf16 v[52:55], v[180:183], v[196:199], v[52:55]
	v_mfma_f32_16x16x32_bf16 v[48:51], v[188:191], v[196:199], v[48:51]
	v_mfma_f32_16x16x32_bf16 v[36:39], v[180:183], v[204:207], v[36:39]
	v_mfma_f32_16x16x32_bf16 v[32:35], v[188:191], v[204:207], v[32:35]
	v_mfma_f32_16x16x32_bf16 v[20:23], v[180:183], v[212:215], v[20:23]
	v_mfma_f32_16x16x32_bf16 v[16:19], v[188:191], v[212:215], v[16:19]
	v_mfma_f32_16x16x32_bf16 v[4:7], v[180:183], v[220:223], v[4:7]
	v_mfma_f32_16x16x32_bf16 v[0:3], v[188:191], v[220:223], v[0:3]
	s_barrier
	s_add_i32 s74, 0, 0x18000
	s_add_i32 s75, 0, 0x1c000
	s_add_i32 s73, s73, 0x40000
	s_add_u32 s36, s28, s73
	s_addc_u32 s37, s29, 0
	s_mov_b32 m0, s33
	v_lshl_add_u64 v[224:225], s[36:37], 0, v[130:131]
	global_load_lds_dwordx4 v[224:225], off
	v_lshl_add_u64 v[224:225], s[36:37], 0, v[132:133]
	s_mov_b32 m0, s41
	s_nop 0
	global_load_lds_dwordx4 v[224:225], off
	v_add_u32_e32 v159, s74, v140
	ds_read_b128 v[160:163], v159
	ds_read_b128 v[164:167], v159 offset:1024
	ds_read_b128 v[168:171], v159 offset:2048
	ds_read_b128 v[172:175], v159 offset:3072
	v_add_u32_e32 v159, s75, v140
	ds_read_b128 v[176:179], v159
	ds_read_b128 v[180:183], v159 offset:1024
	ds_read_b128 v[184:187], v159 offset:2048
	ds_read_b128 v[188:191], v159 offset:3072
	ds_read_b128 v[192:195], v158 offset:32768
	ds_read_b128 v[196:199], v158 offset:33792
	ds_read_b128 v[200:203], v158 offset:34816
	ds_read_b128 v[204:207], v158 offset:35840
	ds_read_b128 v[208:211], v158 offset:36864
	ds_read_b128 v[212:215], v158 offset:37888
	ds_read_b128 v[216:219], v158 offset:38912
	ds_read_b128 v[220:223], v158 offset:39936
	s_waitcnt vmcnt(8)
	s_waitcnt lgkmcnt(0)
	s_barrier
	s_waitcnt lgkmcnt(0)
	v_mfma_f32_16x16x32_bf16 v[124:127], v[160:163], v[192:195], v[124:127]
	v_mfma_f32_16x16x32_bf16 v[120:123], v[168:171], v[192:195], v[120:123]
	v_mfma_f32_16x16x32_bf16 v[108:111], v[160:163], v[200:203], v[108:111]
	v_mfma_f32_16x16x32_bf16 v[104:107], v[168:171], v[200:203], v[104:107]
	v_mfma_f32_16x16x32_bf16 v[92:95], v[160:163], v[208:211], v[92:95]
	v_mfma_f32_16x16x32_bf16 v[88:91], v[168:171], v[208:211], v[88:91]
	v_mfma_f32_16x16x32_bf16 v[76:79], v[160:163], v[216:219], v[76:79]
	v_mfma_f32_16x16x32_bf16 v[72:75], v[168:171], v[216:219], v[72:75]
	v_mfma_f32_16x16x32_bf16 v[124:127], v[164:167], v[196:199], v[124:127]
	v_mfma_f32_16x16x32_bf16 v[120:123], v[172:175], v[196:199], v[120:123]
	v_mfma_f32_16x16x32_bf16 v[108:111], v[164:167], v[204:207], v[108:111]
	v_mfma_f32_16x16x32_bf16 v[104:107], v[172:175], v[204:207], v[104:107]
	v_mfma_f32_16x16x32_bf16 v[92:95], v[164:167], v[212:215], v[92:95]
	v_mfma_f32_16x16x32_bf16 v[88:91], v[172:175], v[212:215], v[88:91]
	v_mfma_f32_16x16x32_bf16 v[76:79], v[164:167], v[220:223], v[76:79]
	v_mfma_f32_16x16x32_bf16 v[72:75], v[172:175], v[220:223], v[72:75]
	v_mfma_f32_16x16x32_bf16 v[116:119], v[176:179], v[192:195], v[116:119]
	v_mfma_f32_16x16x32_bf16 v[112:115], v[184:187], v[192:195], v[112:115]
	v_mfma_f32_16x16x32_bf16 v[100:103], v[176:179], v[200:203], v[100:103]
	v_mfma_f32_16x16x32_bf16 v[96:99], v[184:187], v[200:203], v[96:99]
	v_mfma_f32_16x16x32_bf16 v[84:87], v[176:179], v[208:211], v[84:87]
	v_mfma_f32_16x16x32_bf16 v[80:83], v[184:187], v[208:211], v[80:83]
	v_mfma_f32_16x16x32_bf16 v[68:71], v[176:179], v[216:219], v[68:71]
	v_mfma_f32_16x16x32_bf16 v[64:67], v[184:187], v[216:219], v[64:67]
	v_mfma_f32_16x16x32_bf16 v[116:119], v[180:183], v[196:199], v[116:119]
	v_mfma_f32_16x16x32_bf16 v[112:115], v[188:191], v[196:199], v[112:115]
	v_mfma_f32_16x16x32_bf16 v[100:103], v[180:183], v[204:207], v[100:103]
	v_mfma_f32_16x16x32_bf16 v[96:99], v[188:191], v[204:207], v[96:99]
	v_mfma_f32_16x16x32_bf16 v[84:87], v[180:183], v[212:215], v[84:87]
	v_mfma_f32_16x16x32_bf16 v[80:83], v[188:191], v[212:215], v[80:83]
	v_mfma_f32_16x16x32_bf16 v[68:71], v[180:183], v[220:223], v[68:71]
	v_mfma_f32_16x16x32_bf16 v[64:67], v[188:191], v[220:223], v[64:67]
	s_barrier
; template <class Epi, class Sched, class Hook = NoHook>
; __device__ __forceinline__ void gemm_phase_w(LAS unsigned char* lds, const Sched& S, const Epi& E, int wave_id, const Hook& HK = Hook()) {
;     ...
;         if constexpr (!SEG2) {
;             for (int tt = 0; tt < nt; tt += 2) {
	s_bitset1_b32 s71, 7
	s_add_i32 s23, s71, s23
	s_ashr_i32 s37, s23, 31
	s_add_u32 s36, s10, s23
	s_addc_u32 s37, s11, s37
	s_add_i32 s23, s74, s34
	v_lshl_add_u64 v[224:225], s[36:37], 0, v[130:131]
	s_mov_b32 m0, s23
	s_nop 0
	global_load_lds_dwordx4 v[224:225], off
	s_add_i32 m0, s23, 0x2000
	s_add_i32 s23, s71, s72
	v_lshl_add_u64 v[224:225], s[36:37], 0, v[132:133]
	s_ashr_i32 s37, s23, 31
	s_add_u32 s36, s10, s23
	s_addc_u32 s37, s11, s37
	s_add_i32 s23, s75, s34
	global_load_lds_dwordx4 v[224:225], off
	v_lshl_add_u64 v[224:225], s[36:37], 0, v[130:131]
	s_mov_b32 m0, s23
	s_add_i32 s71, s71, s22
	global_load_lds_dwordx4 v[224:225], off
	s_add_i32 m0, s23, 0x2000
	s_add_u32 s22, s28, s71
	v_lshl_add_u64 v[224:225], s[36:37], 0, v[132:133]
	s_addc_u32 s23, s29, 0
	global_load_lds_dwordx4 v[224:225], off
	v_lshl_add_u64 v[224:225], s[22:23], 0, v[130:131]
	s_mov_b32 m0, s42
	s_nop 0
	global_load_lds_dwordx4 v[224:225], off
	v_lshl_add_u64 v[224:225], s[22:23], 0, v[132:133]
	s_mov_b32 m0, s43
	s_nop 0
	global_load_lds_dwordx4 v[224:225], off
	ds_read_b128 v[192:195], v158 offset:49152
	ds_read_b128 v[196:199], v158 offset:50176
	ds_read_b128 v[200:203], v158 offset:51200
	ds_read_b128 v[204:207], v158 offset:52224
	ds_read_b128 v[208:211], v158 offset:53248
	ds_read_b128 v[212:215], v158 offset:54272
	ds_read_b128 v[216:219], v158 offset:55296
	ds_read_b128 v[220:223], v158 offset:56320
	s_waitcnt vmcnt(8)
	s_waitcnt lgkmcnt(0)
	s_barrier
	s_waitcnt lgkmcnt(0)
	v_mfma_f32_16x16x32_bf16 v[60:63], v[160:163], v[192:195], v[60:63]
	v_mfma_f32_16x16x32_bf16 v[56:59], v[168:171], v[192:195], v[56:59]
	v_mfma_f32_16x16x32_bf16 v[44:47], v[160:163], v[200:203], v[44:47]
	v_mfma_f32_16x16x32_bf16 v[40:43], v[168:171], v[200:203], v[40:43]
	v_mfma_f32_16x16x32_bf16 v[28:31], v[160:163], v[208:211], v[28:31]
	v_mfma_f32_16x16x32_bf16 v[24:27], v[168:171], v[208:211], v[24:27]
	v_mfma_f32_16x16x32_bf16 v[12:15], v[160:163], v[216:219], v[12:15]
	v_mfma_f32_16x16x32_bf16 v[8:11], v[168:171], v[216:219], v[8:11]
	v_mfma_f32_16x16x32_bf16 v[60:63], v[164:167], v[196:199], v[60:63]
	v_mfma_f32_16x16x32_bf16 v[56:59], v[172:175], v[196:199], v[56:59]
	v_mfma_f32_16x16x32_bf16 v[44:47], v[164:167], v[204:207], v[44:47]
	v_mfma_f32_16x16x32_bf16 v[40:43], v[172:175], v[204:207], v[40:43]
	v_mfma_f32_16x16x32_bf16 v[28:31], v[164:167], v[212:215], v[28:31]
	v_mfma_f32_16x16x32_bf16 v[24:27], v[172:175], v[212:215], v[24:27]
	v_mfma_f32_16x16x32_bf16 v[12:15], v[164:167], v[220:223], v[12:15]
	v_mfma_f32_16x16x32_bf16 v[8:11], v[172:175], v[220:223], v[8:11]
	v_mfma_f32_16x16x32_bf16 v[52:55], v[176:179], v[192:195], v[52:55]
	v_mfma_f32_16x16x32_bf16 v[48:51], v[184:187], v[192:195], v[48:51]
	v_mfma_f32_16x16x32_bf16 v[36:39], v[176:179], v[200:203], v[36:39]
	v_mfma_f32_16x16x32_bf16 v[32:35], v[184:187], v[200:203], v[32:35]
	v_mfma_f32_16x16x32_bf16 v[20:23], v[176:179], v[208:211], v[20:23]
	v_mfma_f32_16x16x32_bf16 v[16:19], v[184:187], v[208:211], v[16:19]
	v_mfma_f32_16x16x32_bf16 v[4:7], v[176:179], v[216:219], v[4:7]
	v_mfma_f32_16x16x32_bf16 v[0:3], v[184:187], v[216:219], v[0:3]
	v_mfma_f32_16x16x32_bf16 v[52:55], v[180:183], v[196:199], v[52:55]
	v_mfma_f32_16x16x32_bf16 v[48:51], v[188:191], v[196:199], v[48:51]
	v_mfma_f32_16x16x32_bf16 v[36:39], v[180:183], v[204:207], v[36:39]
	v_mfma_f32_16x16x32_bf16 v[32:35], v[188:191], v[204:207], v[32:35]
	v_mfma_f32_16x16x32_bf16 v[20:23], v[180:183], v[212:215], v[20:23]
	v_mfma_f32_16x16x32_bf16 v[16:19], v[188:191], v[212:215], v[16:19]
	v_mfma_f32_16x16x32_bf16 v[4:7], v[180:183], v[220:223], v[4:7]
	v_mfma_f32_16x16x32_bf16 v[0:3], v[188:191], v[220:223], v[0:3]
	s_barrier
	s_addk_i32 s12, 0x100
	s_add_i32 s19, s19, 2
	s_cmp_gt_u32 s19, 13
	s_cbranch_scc0 .LBB0_1194
	s_and_b64 vcc, exec, s[0:1]
	s_cbranch_vccz .LBB0_1197
	s_barrier

.LBB0_1442:
	s_add_i32 s22, s61, s12
	s_add_u32 s66, s28, s22
	s_addc_u32 s67, s29, 0
	s_add_i32 m0, s33, 0xc000
	s_add_i32 s68, s33, 0xe000
	s_add_i32 s69, s12, 0xfffc0080
	s_cmp_eq_u32 s19, 12
	s_cselect_b32 s22, s58, s61
	s_cselect_b32 s23, s59, s62
	v_lshl_add_u64 v[220:221], s[66:67], 0, v[130:131]
	global_load_lds_dwordx4 v[220:221], off
	v_lshl_add_u64 v[220:221], s[66:67], 0, v[132:133]
	s_mov_b32 m0, s68
	s_nop 0
	global_load_lds_dwordx4 v[220:221], off
	ds_read_b128 v[156:159], v153
	ds_read_b128 v[160:163], v153 offset:1024
	ds_read_b128 v[164:167], v153 offset:2048
	ds_read_b128 v[168:171], v153 offset:3072
	ds_read_b128 v[172:175], v154
	ds_read_b128 v[176:179], v154 offset:1024
	ds_read_b128 v[180:183], v154 offset:2048
	ds_read_b128 v[184:187], v154 offset:3072
	ds_read_b128 v[188:191], v155
	ds_read_b128 v[192:195], v155 offset:1024
	ds_read_b128 v[196:199], v155 offset:2048
	ds_read_b128 v[200:203], v155 offset:3072
	ds_read_b128 v[204:207], v155 offset:4096
	ds_read_b128 v[208:211], v155 offset:5120
	ds_read_b128 v[212:215], v155 offset:6144
	ds_read_b128 v[216:219], v155 offset:7168
	s_waitcnt vmcnt(8)
	s_waitcnt lgkmcnt(0)
	s_barrier
	s_waitcnt lgkmcnt(0)
	v_mfma_f32_16x16x32_bf16 v[124:127], v[156:159], v[188:191], v[124:127]
	v_mfma_f32_16x16x32_bf16 v[120:123], v[164:167], v[188:191], v[120:123]
	v_mfma_f32_16x16x32_bf16 v[108:111], v[156:159], v[196:199], v[108:111]
	v_mfma_f32_16x16x32_bf16 v[104:107], v[164:167], v[196:199], v[104:107]
	v_mfma_f32_16x16x32_bf16 v[92:95], v[156:159], v[204:207], v[92:95]
	v_mfma_f32_16x16x32_bf16 v[88:91], v[164:167], v[204:207], v[88:91]
	v_mfma_f32_16x16x32_bf16 v[76:79], v[156:159], v[212:215], v[76:79]
	v_mfma_f32_16x16x32_bf16 v[72:75], v[164:167], v[212:215], v[72:75]
	v_mfma_f32_16x16x32_bf16 v[124:127], v[160:163], v[192:195], v[124:127]
	v_mfma_f32_16x16x32_bf16 v[120:123], v[168:171], v[192:195], v[120:123]
	v_mfma_f32_16x16x32_bf16 v[108:111], v[160:163], v[200:203], v[108:111]
	v_mfma_f32_16x16x32_bf16 v[104:107], v[168:171], v[200:203], v[104:107]
	v_mfma_f32_16x16x32_bf16 v[92:95], v[160:163], v[208:211], v[92:95]
	v_mfma_f32_16x16x32_bf16 v[88:91], v[168:171], v[208:211], v[88:91]
	v_mfma_f32_16x16x32_bf16 v[76:79], v[160:163], v[216:219], v[76:79]
	v_mfma_f32_16x16x32_bf16 v[72:75], v[168:171], v[216:219], v[72:75]
	v_mfma_f32_16x16x32_bf16 v[116:119], v[172:175], v[188:191], v[116:119]
	v_mfma_f32_16x16x32_bf16 v[112:115], v[180:183], v[188:191], v[112:115]
	v_mfma_f32_16x16x32_bf16 v[100:103], v[172:175], v[196:199], v[100:103]
	v_mfma_f32_16x16x32_bf16 v[96:99], v[180:183], v[196:199], v[96:99]
	v_mfma_f32_16x16x32_bf16 v[84:87], v[172:175], v[204:207], v[84:87]
	v_mfma_f32_16x16x32_bf16 v[80:83], v[180:183], v[204:207], v[80:83]
	v_mfma_f32_16x16x32_bf16 v[68:71], v[172:175], v[212:215], v[68:71]
	v_mfma_f32_16x16x32_bf16 v[64:67], v[180:183], v[212:215], v[64:67]
	v_mfma_f32_16x16x32_bf16 v[116:119], v[176:179], v[192:195], v[116:119]
	v_mfma_f32_16x16x32_bf16 v[112:115], v[184:187], v[192:195], v[112:115]
	v_mfma_f32_16x16x32_bf16 v[100:103], v[176:179], v[200:203], v[100:103]
	v_mfma_f32_16x16x32_bf16 v[96:99], v[184:187], v[200:203], v[96:99]
	v_mfma_f32_16x16x32_bf16 v[84:87], v[176:179], v[208:211], v[84:87]
	v_mfma_f32_16x16x32_bf16 v[80:83], v[184:187], v[208:211], v[80:83]
	v_mfma_f32_16x16x32_bf16 v[68:71], v[176:179], v[216:219], v[68:71]
	v_mfma_f32_16x16x32_bf16 v[64:67], v[184:187], v[216:219], v[64:67]
	s_barrier
	s_cselect_b32 s68, 0, s69
	s_add_i32 s66, s68, s23
	s_ashr_i32 s67, s66, 31
	s_add_u32 s66, s10, s66
	s_addc_u32 s67, s11, s67
	s_add_i32 s69, s37, s34
	v_lshl_add_u64 v[220:221], s[66:67], 0, v[130:131]
	s_mov_b32 m0, s69
	s_nop 0
	global_load_lds_dwordx4 v[220:221], off
	s_add_i32 m0, s69, 0x2000
	s_add_i32 s69, s23, 0x40000
	v_lshl_add_u64 v[220:221], s[66:67], 0, v[132:133]
	s_add_i32 s66, s69, s68
	s_ashr_i32 s67, s66, 31
	s_add_u32 s66, s10, s66
	s_addc_u32 s67, s11, s67
	s_add_i32 s70, s38, s34
	global_load_lds_dwordx4 v[220:221], off
	v_lshl_add_u64 v[220:221], s[66:67], 0, v[130:131]
	s_mov_b32 m0, s70
	s_nop 0
	global_load_lds_dwordx4 v[220:221], off
	s_add_i32 m0, s70, 0x2000
	s_add_i32 s70, s68, s22
	v_lshl_add_u64 v[220:221], s[66:67], 0, v[132:133]
	s_add_u32 s66, s28, s70
	s_addc_u32 s67, s29, 0
	global_load_lds_dwordx4 v[220:221], off
	v_lshl_add_u64 v[220:221], s[66:67], 0, v[130:131]
	s_mov_b32 m0, s33
	s_nop 0
	global_load_lds_dwordx4 v[220:221], off
	v_lshl_add_u64 v[220:221], s[66:67], 0, v[132:133]
	s_mov_b32 m0, s40
	s_nop 0
	global_load_lds_dwordx4 v[220:221], off
	ds_read_b128 v[188:191], v155 offset:16384
	ds_read_b128 v[192:195], v155 offset:17408
	ds_read_b128 v[196:199], v155 offset:18432
	ds_read_b128 v[200:203], v155 offset:19456
	ds_read_b128 v[204:207], v155 offset:20480
	ds_read_b128 v[208:211], v155 offset:21504
	ds_read_b128 v[212:215], v155 offset:22528
	ds_read_b128 v[216:219], v155 offset:23552
	s_waitcnt vmcnt(8)
	s_waitcnt lgkmcnt(0)
	s_barrier
	s_waitcnt lgkmcnt(0)
	v_mfma_f32_16x16x32_bf16 v[60:63], v[156:159], v[188:191], v[60:63]
	v_mfma_f32_16x16x32_bf16 v[56:59], v[164:167], v[188:191], v[56:59]
	v_mfma_f32_16x16x32_bf16 v[44:47], v[156:159], v[196:199], v[44:47]
	v_mfma_f32_16x16x32_bf16 v[40:43], v[164:167], v[196:199], v[40:43]
	v_mfma_f32_16x16x32_bf16 v[28:31], v[156:159], v[204:207], v[28:31]
	v_mfma_f32_16x16x32_bf16 v[24:27], v[164:167], v[204:207], v[24:27]
	v_mfma_f32_16x16x32_bf16 v[12:15], v[156:159], v[212:215], v[12:15]
	v_mfma_f32_16x16x32_bf16 v[8:11], v[164:167], v[212:215], v[8:11]
	v_mfma_f32_16x16x32_bf16 v[60:63], v[160:163], v[192:195], v[60:63]
	v_mfma_f32_16x16x32_bf16 v[56:59], v[168:171], v[192:195], v[56:59]
	v_mfma_f32_16x16x32_bf16 v[44:47], v[160:163], v[200:203], v[44:47]
	v_mfma_f32_16x16x32_bf16 v[40:43], v[168:171], v[200:203], v[40:43]
	v_mfma_f32_16x16x32_bf16 v[28:31], v[160:163], v[208:211], v[28:31]
	v_mfma_f32_16x16x32_bf16 v[24:27], v[168:171], v[208:211], v[24:27]
	v_mfma_f32_16x16x32_bf16 v[12:15], v[160:163], v[216:219], v[12:15]
	v_mfma_f32_16x16x32_bf16 v[8:11], v[168:171], v[216:219], v[8:11]
	v_mfma_f32_16x16x32_bf16 v[52:55], v[172:175], v[188:191], v[52:55]
	v_mfma_f32_16x16x32_bf16 v[48:51], v[180:183], v[188:191], v[48:51]
	v_mfma_f32_16x16x32_bf16 v[36:39], v[172:175], v[196:199], v[36:39]
	v_mfma_f32_16x16x32_bf16 v[32:35], v[180:183], v[196:199], v[32:35]
	v_mfma_f32_16x16x32_bf16 v[20:23], v[172:175], v[204:207], v[20:23]
	v_mfma_f32_16x16x32_bf16 v[16:19], v[180:183], v[204:207], v[16:19]
	v_mfma_f32_16x16x32_bf16 v[4:7], v[172:175], v[212:215], v[4:7]
	v_mfma_f32_16x16x32_bf16 v[0:3], v[180:183], v[212:215], v[0:3]
	v_mfma_f32_16x16x32_bf16 v[52:55], v[176:179], v[192:195], v[52:55]
	v_mfma_f32_16x16x32_bf16 v[48:51], v[184:187], v[192:195], v[48:51]
	v_mfma_f32_16x16x32_bf16 v[36:39], v[176:179], v[200:203], v[36:39]
	v_mfma_f32_16x16x32_bf16 v[32:35], v[184:187], v[200:203], v[32:35]
	v_mfma_f32_16x16x32_bf16 v[20:23], v[176:179], v[208:211], v[20:23]
	v_mfma_f32_16x16x32_bf16 v[16:19], v[184:187], v[208:211], v[16:19]
	v_mfma_f32_16x16x32_bf16 v[4:7], v[176:179], v[216:219], v[4:7]
	v_mfma_f32_16x16x32_bf16 v[0:3], v[184:187], v[216:219], v[0:3]
	s_barrier
	s_add_i32 s71, 0, 0x18000
	s_add_i32 s72, 0, 0x1c000
	s_add_i32 s70, s70, 0x40000
	s_add_u32 s66, s28, s70
	s_addc_u32 s67, s29, 0
	s_mov_b32 m0, s41
	v_lshl_add_u64 v[220:221], s[66:67], 0, v[130:131]
	global_load_lds_dwordx4 v[220:221], off
	v_lshl_add_u64 v[220:221], s[66:67], 0, v[132:133]
	s_mov_b32 m0, s42
	s_nop 0
	global_load_lds_dwordx4 v[220:221], off
	v_add_u32_e32 v168, s71, v137
	v_add_u32_e32 v184, s72, v137
	ds_read_b128 v[156:159], v168
	ds_read_b128 v[160:163], v168 offset:1024
	ds_read_b128 v[164:167], v168 offset:2048
	ds_read_b128 v[168:171], v168 offset:3072
	ds_read_b128 v[172:175], v184
	ds_read_b128 v[176:179], v184 offset:1024
	ds_read_b128 v[180:183], v184 offset:2048
	ds_read_b128 v[184:187], v184 offset:3072
	ds_read_b128 v[188:191], v155 offset:32768
	ds_read_b128 v[192:195], v155 offset:33792
	ds_read_b128 v[196:199], v155 offset:34816
	ds_read_b128 v[200:203], v155 offset:35840
	ds_read_b128 v[204:207], v155 offset:36864
	ds_read_b128 v[208:211], v155 offset:37888
	ds_read_b128 v[212:215], v155 offset:38912
	ds_read_b128 v[216:219], v155 offset:39936
	s_waitcnt vmcnt(8)
	s_waitcnt lgkmcnt(0)
	s_barrier
	s_waitcnt lgkmcnt(0)
	v_mfma_f32_16x16x32_bf16 v[124:127], v[156:159], v[188:191], v[124:127]
	v_mfma_f32_16x16x32_bf16 v[120:123], v[164:167], v[188:191], v[120:123]
	v_mfma_f32_16x16x32_bf16 v[108:111], v[156:159], v[196:199], v[108:111]
	v_mfma_f32_16x16x32_bf16 v[104:107], v[164:167], v[196:199], v[104:107]
	v_mfma_f32_16x16x32_bf16 v[92:95], v[156:159], v[204:207], v[92:95]
	v_mfma_f32_16x16x32_bf16 v[88:91], v[164:167], v[204:207], v[88:91]
	v_mfma_f32_16x16x32_bf16 v[76:79], v[156:159], v[212:215], v[76:79]
	v_mfma_f32_16x16x32_bf16 v[72:75], v[164:167], v[212:215], v[72:75]
	v_mfma_f32_16x16x32_bf16 v[124:127], v[160:163], v[192:195], v[124:127]
	v_mfma_f32_16x16x32_bf16 v[120:123], v[168:171], v[192:195], v[120:123]
	v_mfma_f32_16x16x32_bf16 v[108:111], v[160:163], v[200:203], v[108:111]
	v_mfma_f32_16x16x32_bf16 v[104:107], v[168:171], v[200:203], v[104:107]
	v_mfma_f32_16x16x32_bf16 v[92:95], v[160:163], v[208:211], v[92:95]
	v_mfma_f32_16x16x32_bf16 v[88:91], v[168:171], v[208:211], v[88:91]
	v_mfma_f32_16x16x32_bf16 v[76:79], v[160:163], v[216:219], v[76:79]
	v_mfma_f32_16x16x32_bf16 v[72:75], v[168:171], v[216:219], v[72:75]
	v_mfma_f32_16x16x32_bf16 v[116:119], v[172:175], v[188:191], v[116:119]
	v_mfma_f32_16x16x32_bf16 v[112:115], v[180:183], v[188:191], v[112:115]
	v_mfma_f32_16x16x32_bf16 v[100:103], v[172:175], v[196:199], v[100:103]
	v_mfma_f32_16x16x32_bf16 v[96:99], v[180:183], v[196:199], v[96:99]
	v_mfma_f32_16x16x32_bf16 v[84:87], v[172:175], v[204:207], v[84:87]
	v_mfma_f32_16x16x32_bf16 v[80:83], v[180:183], v[204:207], v[80:83]
	v_mfma_f32_16x16x32_bf16 v[68:71], v[172:175], v[212:215], v[68:71]
	v_mfma_f32_16x16x32_bf16 v[64:67], v[180:183], v[212:215], v[64:67]
	v_mfma_f32_16x16x32_bf16 v[116:119], v[176:179], v[192:195], v[116:119]
	v_mfma_f32_16x16x32_bf16 v[112:115], v[184:187], v[192:195], v[112:115]
	v_mfma_f32_16x16x32_bf16 v[100:103], v[176:179], v[200:203], v[100:103]
	v_mfma_f32_16x16x32_bf16 v[96:99], v[184:187], v[200:203], v[96:99]
	v_mfma_f32_16x16x32_bf16 v[84:87], v[176:179], v[208:211], v[84:87]
	v_mfma_f32_16x16x32_bf16 v[80:83], v[184:187], v[208:211], v[80:83]
	v_mfma_f32_16x16x32_bf16 v[68:71], v[176:179], v[216:219], v[68:71]
	v_mfma_f32_16x16x32_bf16 v[64:67], v[184:187], v[216:219], v[64:67]
	s_barrier
; template <class Epi, class Sched, class Hook = NoHook>
; __device__ __forceinline__ void gemm_phase_w(LAS unsigned char* lds, const Sched& S, const Epi& E, int wave_id, const Hook& HK = Hook()) {
;     ...
;         if constexpr (!SEG2) {
;             for (int tt = 0; tt < nt; tt += 2) {
	s_bitset1_b32 s68, 7
	s_add_i32 s23, s68, s23
	s_ashr_i32 s67, s23, 31
	s_add_u32 s66, s10, s23
	s_addc_u32 s67, s11, s67
	s_add_i32 s23, s71, s34
	v_lshl_add_u64 v[220:221], s[66:67], 0, v[130:131]
	s_mov_b32 m0, s23
	s_nop 0
	global_load_lds_dwordx4 v[220:221], off
	s_add_i32 m0, s23, 0x2000
	s_add_i32 s23, s68, s69
	v_lshl_add_u64 v[220:221], s[66:67], 0, v[132:133]
	s_ashr_i32 s67, s23, 31
	s_add_u32 s66, s10, s23
	s_addc_u32 s67, s11, s67
	s_add_i32 s23, s72, s34
	global_load_lds_dwordx4 v[220:221], off
	v_lshl_add_u64 v[220:221], s[66:67], 0, v[130:131]
	s_mov_b32 m0, s23
	s_add_i32 s68, s68, s22
	global_load_lds_dwordx4 v[220:221], off
	s_add_i32 m0, s23, 0x2000
	s_add_u32 s22, s28, s68
	v_lshl_add_u64 v[220:221], s[66:67], 0, v[132:133]
	s_addc_u32 s23, s29, 0
	global_load_lds_dwordx4 v[220:221], off
	v_lshl_add_u64 v[220:221], s[22:23], 0, v[130:131]
	s_mov_b32 m0, s39
	s_nop 0
	global_load_lds_dwordx4 v[220:221], off
	v_lshl_add_u64 v[220:221], s[22:23], 0, v[132:133]
	s_mov_b32 m0, s43
	s_nop 0
	global_load_lds_dwordx4 v[220:221], off
	ds_read_b128 v[188:191], v155 offset:49152
	ds_read_b128 v[192:195], v155 offset:50176
	ds_read_b128 v[196:199], v155 offset:51200
	ds_read_b128 v[200:203], v155 offset:52224
	ds_read_b128 v[204:207], v155 offset:53248
	ds_read_b128 v[208:211], v155 offset:54272
	ds_read_b128 v[212:215], v155 offset:55296
	ds_read_b128 v[216:219], v155 offset:56320
	s_waitcnt vmcnt(8)
	s_waitcnt lgkmcnt(0)
	s_barrier
	s_waitcnt lgkmcnt(0)
	v_mfma_f32_16x16x32_bf16 v[60:63], v[156:159], v[188:191], v[60:63]
	v_mfma_f32_16x16x32_bf16 v[56:59], v[164:167], v[188:191], v[56:59]
	v_mfma_f32_16x16x32_bf16 v[44:47], v[156:159], v[196:199], v[44:47]
	v_mfma_f32_16x16x32_bf16 v[40:43], v[164:167], v[196:199], v[40:43]
	v_mfma_f32_16x16x32_bf16 v[28:31], v[156:159], v[204:207], v[28:31]
	v_mfma_f32_16x16x32_bf16 v[24:27], v[164:167], v[204:207], v[24:27]
	v_mfma_f32_16x16x32_bf16 v[12:15], v[156:159], v[212:215], v[12:15]
	v_mfma_f32_16x16x32_bf16 v[8:11], v[164:167], v[212:215], v[8:11]
	v_mfma_f32_16x16x32_bf16 v[60:63], v[160:163], v[192:195], v[60:63]
	v_mfma_f32_16x16x32_bf16 v[56:59], v[168:171], v[192:195], v[56:59]
	v_mfma_f32_16x16x32_bf16 v[44:47], v[160:163], v[200:203], v[44:47]
	v_mfma_f32_16x16x32_bf16 v[40:43], v[168:171], v[200:203], v[40:43]
	v_mfma_f32_16x16x32_bf16 v[28:31], v[160:163], v[208:211], v[28:31]
	v_mfma_f32_16x16x32_bf16 v[24:27], v[168:171], v[208:211], v[24:27]
	v_mfma_f32_16x16x32_bf16 v[12:15], v[160:163], v[216:219], v[12:15]
	v_mfma_f32_16x16x32_bf16 v[8:11], v[168:171], v[216:219], v[8:11]
	v_mfma_f32_16x16x32_bf16 v[52:55], v[172:175], v[188:191], v[52:55]
	v_mfma_f32_16x16x32_bf16 v[48:51], v[180:183], v[188:191], v[48:51]
	v_mfma_f32_16x16x32_bf16 v[36:39], v[172:175], v[196:199], v[36:39]
	v_mfma_f32_16x16x32_bf16 v[32:35], v[180:183], v[196:199], v[32:35]
	v_mfma_f32_16x16x32_bf16 v[20:23], v[172:175], v[204:207], v[20:23]
	v_mfma_f32_16x16x32_bf16 v[16:19], v[180:183], v[204:207], v[16:19]
	v_mfma_f32_16x16x32_bf16 v[4:7], v[172:175], v[212:215], v[4:7]
	v_mfma_f32_16x16x32_bf16 v[0:3], v[180:183], v[212:215], v[0:3]
	v_mfma_f32_16x16x32_bf16 v[52:55], v[176:179], v[192:195], v[52:55]
	v_mfma_f32_16x16x32_bf16 v[48:51], v[184:187], v[192:195], v[48:51]
	v_mfma_f32_16x16x32_bf16 v[36:39], v[176:179], v[200:203], v[36:39]
	v_mfma_f32_16x16x32_bf16 v[32:35], v[184:187], v[200:203], v[32:35]
	v_mfma_f32_16x16x32_bf16 v[20:23], v[176:179], v[208:211], v[20:23]
	v_mfma_f32_16x16x32_bf16 v[16:19], v[184:187], v[208:211], v[16:19]
	v_mfma_f32_16x16x32_bf16 v[4:7], v[176:179], v[216:219], v[4:7]
	v_mfma_f32_16x16x32_bf16 v[0:3], v[184:187], v[216:219], v[0:3]
	s_barrier
	s_addk_i32 s12, 0x100
	s_add_i32 s19, s19, 2
	s_cmp_gt_u32 s19, 13
	s_cbranch_scc0 .LBB0_1442
	s_and_b64 vcc, exec, s[0:1]
	s_cbranch_vccz .LBB0_1445
	s_barrier

.LBB0_1776:
	s_add_i32 s27, 0, 0x10000
	s_add_i32 s59, 0, 0x14000
	s_add_i32 s26, s84, s5
	s_add_u32 s60, s3, s26
	s_addc_u32 s61, s36, 0
	s_add_i32 vcc_lo, s63, 0xc000
	s_add_i32 s35, s63, 0xe000
	s_add_i32 s42, s5, 0xfffe0080
	s_cmp_eq_u32 s70, s34
	s_cselect_b32 s50, s4, s84
	s_cselect_b32 s58, s85, s97
	s_mov_b32 m0, vcc_lo
	v_lshl_add_u64 v[134:135], s[60:61], 0, v[148:149]
	global_load_lds_dwordx4 v[134:135], off
	v_lshl_add_u64 v[134:135], s[60:61], 0, v[146:147]
	s_mov_b32 m0, s35
	s_nop 0
	global_load_lds_dwordx4 v[134:135], off
	v_add_u32_e32 v128, s27, v171
	v_add_u32_e32 v129, s59, v171
	ds_read_b128 v[130:133], v128
	ds_read_b128 v[162:165], v128 offset:1024
	ds_read_b128 v[178:181], v128 offset:2048
	ds_read_b128 v[182:185], v128 offset:3072
	ds_read_b128 v[186:189], v129
	ds_read_b128 v[190:193], v129 offset:1024
	ds_read_b128 v[194:197], v129 offset:2048
	ds_read_b128 v[198:201], v129 offset:3072
	ds_read_b128 v[202:205], v172
	ds_read_b128 v[206:209], v172 offset:1024
	ds_read_b128 v[210:213], v172 offset:2048
	ds_read_b128 v[214:217], v172 offset:3072
	ds_read_b128 v[218:221], v172 offset:4096
	ds_read_b128 v[222:225], v172 offset:5120
	ds_read_b128 v[226:229], v172 offset:6144
	ds_read_b128 v[230:233], v172 offset:7168
	s_waitcnt vmcnt(8)
	s_waitcnt lgkmcnt(0)
	s_barrier
	s_waitcnt lgkmcnt(0)
	v_mfma_f32_16x16x32_bf16 v[124:127], v[130:133], v[202:205], v[124:127]
	v_mfma_f32_16x16x32_bf16 v[120:123], v[178:181], v[202:205], v[120:123]
	v_mfma_f32_16x16x32_bf16 v[116:119], v[130:133], v[210:213], v[116:119]
	v_mfma_f32_16x16x32_bf16 v[112:115], v[178:181], v[210:213], v[112:115]
	v_mfma_f32_16x16x32_bf16 v[108:111], v[130:133], v[218:221], v[108:111]
	v_mfma_f32_16x16x32_bf16 v[104:107], v[178:181], v[218:221], v[104:107]
	v_mfma_f32_16x16x32_bf16 v[100:103], v[130:133], v[226:229], v[100:103]
	v_mfma_f32_16x16x32_bf16 v[96:99], v[178:181], v[226:229], v[96:99]
	v_mfma_f32_16x16x32_bf16 v[124:127], v[162:165], v[206:209], v[124:127]
	v_mfma_f32_16x16x32_bf16 v[120:123], v[182:185], v[206:209], v[120:123]
	v_mfma_f32_16x16x32_bf16 v[116:119], v[162:165], v[214:217], v[116:119]
	v_mfma_f32_16x16x32_bf16 v[112:115], v[182:185], v[214:217], v[112:115]
	v_mfma_f32_16x16x32_bf16 v[108:111], v[162:165], v[222:225], v[108:111]
	v_mfma_f32_16x16x32_bf16 v[104:107], v[182:185], v[222:225], v[104:107]
	v_mfma_f32_16x16x32_bf16 v[100:103], v[162:165], v[230:233], v[100:103]
	v_mfma_f32_16x16x32_bf16 v[96:99], v[182:185], v[230:233], v[96:99]
	v_mfma_f32_16x16x32_bf16 v[92:95], v[186:189], v[202:205], v[92:95]
	v_mfma_f32_16x16x32_bf16 v[88:91], v[194:197], v[202:205], v[88:91]
	v_mfma_f32_16x16x32_bf16 v[84:87], v[186:189], v[210:213], v[84:87]
	v_mfma_f32_16x16x32_bf16 v[80:83], v[194:197], v[210:213], v[80:83]
	v_mfma_f32_16x16x32_bf16 v[76:79], v[186:189], v[218:221], v[76:79]
	v_mfma_f32_16x16x32_bf16 v[72:75], v[194:197], v[218:221], v[72:75]
	v_mfma_f32_16x16x32_bf16 v[68:71], v[186:189], v[226:229], v[68:71]
	v_mfma_f32_16x16x32_bf16 v[64:67], v[194:197], v[226:229], v[64:67]
	v_mfma_f32_16x16x32_bf16 v[92:95], v[190:193], v[206:209], v[92:95]
	v_mfma_f32_16x16x32_bf16 v[88:91], v[198:201], v[206:209], v[88:91]
	v_mfma_f32_16x16x32_bf16 v[84:87], v[190:193], v[214:217], v[84:87]
	v_mfma_f32_16x16x32_bf16 v[80:83], v[198:201], v[214:217], v[80:83]
	v_mfma_f32_16x16x32_bf16 v[76:79], v[190:193], v[222:225], v[76:79]
	v_mfma_f32_16x16x32_bf16 v[72:75], v[198:201], v[222:225], v[72:75]
	v_mfma_f32_16x16x32_bf16 v[68:71], v[190:193], v[230:233], v[68:71]
	v_mfma_f32_16x16x32_bf16 v[64:67], v[198:201], v[230:233], v[64:67]
	s_barrier
	s_cselect_b32 s44, 0, s42
	s_add_i32 s42, s44, s58
	s_ashr_i32 s43, s42, 31
	s_add_u32 s60, s6, s42
	s_addc_u32 s61, s7, s43
	s_add_i32 s51, s58, 0xffffff00
	s_add_i32 s27, s27, s48
	s_add_i32 s42, s51, s44
	v_lshl_add_u64 v[134:135], s[60:61], 0, v[144:145]
	s_mov_b32 m0, s27
	s_add_i32 vcc_hi, s27, 0x2000
	s_ashr_i32 s43, s42, 31
	global_load_lds_dwordx4 v[134:135], off
	v_lshl_add_u64 v[134:135], s[60:61], 0, v[142:143]
	s_add_u32 s60, s6, s42
	s_mov_b32 m0, vcc_hi
	s_addc_u32 s61, s7, s43
	s_add_i32 s59, s59, s48
	global_load_lds_dwordx4 v[134:135], off
	v_lshl_add_u64 v[134:135], s[60:61], 0, v[144:145]
	s_mov_b32 m0, s59
	s_add_i32 s49, s44, s50
	global_load_lds_dwordx4 v[134:135], off
	v_lshl_add_u64 v[134:135], s[60:61], 0, v[142:143]
	s_add_i32 s60, s59, 0x2000
	s_add_u32 s42, s3, s49
	s_mov_b32 m0, s60
	s_addc_u32 s43, s36, 0
	global_load_lds_dwordx4 v[134:135], off
	v_lshl_add_u64 v[134:135], s[42:43], 0, v[148:149]
	s_mov_b32 m0, s63
	s_nop 0
	global_load_lds_dwordx4 v[134:135], off
	v_lshl_add_u64 v[134:135], s[42:43], 0, v[146:147]
	s_mov_b32 m0, s66
	s_nop 0
	global_load_lds_dwordx4 v[134:135], off
	ds_read_b128 v[202:205], v172 offset:16384
	ds_read_b128 v[206:209], v172 offset:17408
	ds_read_b128 v[210:213], v172 offset:18432
	ds_read_b128 v[214:217], v172 offset:19456
	ds_read_b128 v[218:221], v172 offset:20480
	ds_read_b128 v[222:225], v172 offset:21504
	ds_read_b128 v[226:229], v172 offset:22528
	ds_read_b128 v[230:233], v172 offset:23552
	s_waitcnt vmcnt(8)
	s_waitcnt lgkmcnt(0)
	s_barrier
	s_waitcnt lgkmcnt(0)
	v_mfma_f32_16x16x32_bf16 v[60:63], v[130:133], v[202:205], v[60:63]
	v_mfma_f32_16x16x32_bf16 v[56:59], v[178:181], v[202:205], v[56:59]
	v_mfma_f32_16x16x32_bf16 v[52:55], v[130:133], v[210:213], v[52:55]
	v_mfma_f32_16x16x32_bf16 v[48:51], v[178:181], v[210:213], v[48:51]
	v_mfma_f32_16x16x32_bf16 v[44:47], v[130:133], v[218:221], v[44:47]
	v_mfma_f32_16x16x32_bf16 v[40:43], v[178:181], v[218:221], v[40:43]
	v_mfma_f32_16x16x32_bf16 v[36:39], v[130:133], v[226:229], v[36:39]
	v_mfma_f32_16x16x32_bf16 v[32:35], v[178:181], v[226:229], v[32:35]
	v_mfma_f32_16x16x32_bf16 v[60:63], v[162:165], v[206:209], v[60:63]
	v_mfma_f32_16x16x32_bf16 v[56:59], v[182:185], v[206:209], v[56:59]
	v_mfma_f32_16x16x32_bf16 v[52:55], v[162:165], v[214:217], v[52:55]
	v_mfma_f32_16x16x32_bf16 v[48:51], v[182:185], v[214:217], v[48:51]
	v_mfma_f32_16x16x32_bf16 v[44:47], v[162:165], v[222:225], v[44:47]
	v_mfma_f32_16x16x32_bf16 v[40:43], v[182:185], v[222:225], v[40:43]
	v_mfma_f32_16x16x32_bf16 v[36:39], v[162:165], v[230:233], v[36:39]
	v_mfma_f32_16x16x32_bf16 v[32:35], v[182:185], v[230:233], v[32:35]
	v_mfma_f32_16x16x32_bf16 v[28:31], v[186:189], v[202:205], v[28:31]
	v_mfma_f32_16x16x32_bf16 v[24:27], v[194:197], v[202:205], v[24:27]
	v_mfma_f32_16x16x32_bf16 v[20:23], v[186:189], v[210:213], v[20:23]
	v_mfma_f32_16x16x32_bf16 v[16:19], v[194:197], v[210:213], v[16:19]
	v_mfma_f32_16x16x32_bf16 v[12:15], v[186:189], v[218:221], v[12:15]
	v_mfma_f32_16x16x32_bf16 v[8:11], v[194:197], v[218:221], v[8:11]
	v_mfma_f32_16x16x32_bf16 v[4:7], v[186:189], v[226:229], v[4:7]
	v_mfma_f32_16x16x32_bf16 v[0:3], v[194:197], v[226:229], v[0:3]
	v_mfma_f32_16x16x32_bf16 v[28:31], v[190:193], v[206:209], v[28:31]
	v_mfma_f32_16x16x32_bf16 v[24:27], v[198:201], v[206:209], v[24:27]
	v_mfma_f32_16x16x32_bf16 v[20:23], v[190:193], v[214:217], v[20:23]
	v_mfma_f32_16x16x32_bf16 v[16:19], v[198:201], v[214:217], v[16:19]
	v_mfma_f32_16x16x32_bf16 v[12:15], v[190:193], v[222:225], v[12:15]
	v_mfma_f32_16x16x32_bf16 v[8:11], v[198:201], v[222:225], v[8:11]
	v_mfma_f32_16x16x32_bf16 v[4:7], v[190:193], v[230:233], v[4:7]
	v_mfma_f32_16x16x32_bf16 v[0:3], v[198:201], v[230:233], v[0:3]
	s_barrier
	s_add_i32 s61, 0, 0x18000
	s_add_i32 s26, 0, 0x1c000
	s_add_i32 s49, s49, 0x20000
	s_add_u32 s42, s3, s49
	s_addc_u32 s43, s36, 0
	s_mov_b32 m0, s67
	v_lshl_add_u64 v[166:167], s[42:43], 0, v[148:149]
	global_load_lds_dwordx4 v[166:167], off
	v_lshl_add_u64 v[166:167], s[42:43], 0, v[146:147]
	s_mov_b32 m0, s68
	s_nop 0
	global_load_lds_dwordx4 v[166:167], off
	v_add_u32_e32 v130, s61, v171
	v_add_u32_e32 v131, s26, v171
	ds_read_b128 v[132:135], v130
	ds_read_b128 v[162:165], v130 offset:1024
	ds_read_b128 v[178:181], v130 offset:2048
	ds_read_b128 v[182:185], v130 offset:3072
	ds_read_b128 v[186:189], v131
	ds_read_b128 v[190:193], v131 offset:1024
	ds_read_b128 v[194:197], v131 offset:2048
	ds_read_b128 v[198:201], v131 offset:3072
	ds_read_b128 v[202:205], v172 offset:32768
	ds_read_b128 v[206:209], v172 offset:33792
	ds_read_b128 v[210:213], v172 offset:34816
	ds_read_b128 v[214:217], v172 offset:35840
	ds_read_b128 v[218:221], v172 offset:36864
	ds_read_b128 v[222:225], v172 offset:37888
	ds_read_b128 v[226:229], v172 offset:38912
	ds_read_b128 v[230:233], v172 offset:39936
	s_waitcnt vmcnt(8)
	s_waitcnt lgkmcnt(0)
	s_barrier
	s_waitcnt lgkmcnt(0)
	v_mfma_f32_16x16x32_bf16 v[124:127], v[132:135], v[202:205], v[124:127]
	v_mfma_f32_16x16x32_bf16 v[120:123], v[178:181], v[202:205], v[120:123]
	v_mfma_f32_16x16x32_bf16 v[116:119], v[132:135], v[210:213], v[116:119]
	v_mfma_f32_16x16x32_bf16 v[112:115], v[178:181], v[210:213], v[112:115]
	v_mfma_f32_16x16x32_bf16 v[108:111], v[132:135], v[218:221], v[108:111]
	v_mfma_f32_16x16x32_bf16 v[104:107], v[178:181], v[218:221], v[104:107]
	v_mfma_f32_16x16x32_bf16 v[100:103], v[132:135], v[226:229], v[100:103]
	v_mfma_f32_16x16x32_bf16 v[96:99], v[178:181], v[226:229], v[96:99]
	v_mfma_f32_16x16x32_bf16 v[124:127], v[162:165], v[206:209], v[124:127]
	v_mfma_f32_16x16x32_bf16 v[120:123], v[182:185], v[206:209], v[120:123]
	v_mfma_f32_16x16x32_bf16 v[116:119], v[162:165], v[214:217], v[116:119]
	v_mfma_f32_16x16x32_bf16 v[112:115], v[182:185], v[214:217], v[112:115]
	v_mfma_f32_16x16x32_bf16 v[108:111], v[162:165], v[222:225], v[108:111]
	v_mfma_f32_16x16x32_bf16 v[104:107], v[182:185], v[222:225], v[104:107]
	v_mfma_f32_16x16x32_bf16 v[100:103], v[162:165], v[230:233], v[100:103]
	v_mfma_f32_16x16x32_bf16 v[96:99], v[182:185], v[230:233], v[96:99]
	v_mfma_f32_16x16x32_bf16 v[92:95], v[186:189], v[202:205], v[92:95]
	v_mfma_f32_16x16x32_bf16 v[88:91], v[194:197], v[202:205], v[88:91]
	v_mfma_f32_16x16x32_bf16 v[84:87], v[186:189], v[210:213], v[84:87]
	v_mfma_f32_16x16x32_bf16 v[80:83], v[194:197], v[210:213], v[80:83]
	v_mfma_f32_16x16x32_bf16 v[76:79], v[186:189], v[218:221], v[76:79]
	v_mfma_f32_16x16x32_bf16 v[72:75], v[194:197], v[218:221], v[72:75]
	v_mfma_f32_16x16x32_bf16 v[68:71], v[186:189], v[226:229], v[68:71]
	v_mfma_f32_16x16x32_bf16 v[64:67], v[194:197], v[226:229], v[64:67]
	v_mfma_f32_16x16x32_bf16 v[92:95], v[190:193], v[206:209], v[92:95]
	v_mfma_f32_16x16x32_bf16 v[88:91], v[198:201], v[206:209], v[88:91]
	v_mfma_f32_16x16x32_bf16 v[84:87], v[190:193], v[214:217], v[84:87]
	v_mfma_f32_16x16x32_bf16 v[80:83], v[198:201], v[214:217], v[80:83]
	v_mfma_f32_16x16x32_bf16 v[76:79], v[190:193], v[222:225], v[76:79]
	v_mfma_f32_16x16x32_bf16 v[72:75], v[198:201], v[222:225], v[72:75]
	v_mfma_f32_16x16x32_bf16 v[68:71], v[190:193], v[230:233], v[68:71]
	v_mfma_f32_16x16x32_bf16 v[64:67], v[198:201], v[230:233], v[64:67]
	s_barrier
; template <class Epi, class Sched, class Hook = NoHook>
; __device__ __forceinline__ void gemm_phase_w(LAS unsigned char* lds, const Sched& S, const Epi& E, int wave_id, const Hook& HK = Hook()) {
;     ...
;         if constexpr (!SEG2) {
;             for (int tt = 0; tt < nt; tt += 2) {
;                 if constexpr (GATHER) { if (tt == nt - 2) {
;                     if (has_next) { gnxt_00 = S.grow_l(nxt, lds, nbuf, R0) + (unsigned)(C0 * 2); gnxt_01 = S.grow_l(nxt, lds, nbuf, R1) + (unsigned)(C1 * 2); gnxt_10 = S.grow_l(nxt, lds, nbuf, 128 + R0) + (unsigned)(C0 * 2); gnxt_11 = S.grow_l(nxt, lds, nbuf, 128 + R1) + (unsigned)(C1 * 2); }
;                     else { gnxt_00 = gcur_00; gnxt_01 = gcur_01; gnxt_10 = gcur_10; gnxt_11 = gcur_11; } } }
;                 PG_TRIP(tt, false, false, false);
;             }
;         } else {
;             for (int tt = 0; tt < nt - 4; tt += 2) PG_TRIP(tt, false, false, false);
;             PG_TRIP(nt - 4, false, true, false);
	s_or_b32 s18, s44, 0x80
	s_add_i32 s19, s18, s58
	s_ashr_i32 s43, s19, 31
	s_add_u32 s42, s6, s19
	s_addc_u32 s43, s7, s43
	s_add_i32 s61, s61, s48
	v_lshl_add_u64 v[166:167], s[42:43], 0, v[144:145]
	s_mov_b32 m0, s61
	s_add_i32 s19, s18, s51
	global_load_lds_dwordx4 v[166:167], off
	v_lshl_add_u64 v[166:167], s[42:43], 0, v[142:143]
	s_add_i32 s49, s61, 0x2000
	s_ashr_i32 s43, s19, 31
	s_add_u32 s42, s6, s19
	s_mov_b32 m0, s49
	s_addc_u32 s43, s7, s43
	s_add_i32 s26, s26, s48
	global_load_lds_dwordx4 v[166:167], off
	v_lshl_add_u64 v[166:167], s[42:43], 0, v[144:145]
	s_mov_b32 m0, s26
	s_add_i32 s44, s26, 0x2000
	s_add_i32 s18, s18, s50
	global_load_lds_dwordx4 v[166:167], off
	v_lshl_add_u64 v[166:167], s[42:43], 0, v[142:143]
	s_add_u32 s42, s3, s18
	s_mov_b32 m0, s44
	s_addc_u32 s43, s36, 0
	global_load_lds_dwordx4 v[166:167], off
	v_lshl_add_u64 v[166:167], s[42:43], 0, v[148:149]
	s_mov_b32 m0, s71
	s_nop 0
	global_load_lds_dwordx4 v[166:167], off
	v_lshl_add_u64 v[166:167], s[42:43], 0, v[146:147]
	s_mov_b32 m0, s72
	s_nop 0
	global_load_lds_dwordx4 v[166:167], off
	ds_read_b128 v[202:205], v172 offset:49152
	ds_read_b128 v[206:209], v172 offset:50176
	ds_read_b128 v[210:213], v172 offset:51200
	ds_read_b128 v[214:217], v172 offset:52224
	ds_read_b128 v[218:221], v172 offset:53248
	ds_read_b128 v[222:225], v172 offset:54272
	ds_read_b128 v[226:229], v172 offset:55296
	ds_read_b128 v[230:233], v172 offset:56320
	s_waitcnt vmcnt(8)
	s_waitcnt lgkmcnt(0)
	s_barrier
	s_waitcnt lgkmcnt(0)
	v_mfma_f32_16x16x32_bf16 v[60:63], v[132:135], v[202:205], v[60:63]
	v_mfma_f32_16x16x32_bf16 v[56:59], v[178:181], v[202:205], v[56:59]
	v_mfma_f32_16x16x32_bf16 v[52:55], v[132:135], v[210:213], v[52:55]
	v_mfma_f32_16x16x32_bf16 v[48:51], v[178:181], v[210:213], v[48:51]
	v_mfma_f32_16x16x32_bf16 v[44:47], v[132:135], v[218:221], v[44:47]
	v_mfma_f32_16x16x32_bf16 v[40:43], v[178:181], v[218:221], v[40:43]
	v_mfma_f32_16x16x32_bf16 v[36:39], v[132:135], v[226:229], v[36:39]
	v_mfma_f32_16x16x32_bf16 v[32:35], v[178:181], v[226:229], v[32:35]
	v_mfma_f32_16x16x32_bf16 v[60:63], v[162:165], v[206:209], v[60:63]
	v_mfma_f32_16x16x32_bf16 v[56:59], v[182:185], v[206:209], v[56:59]
	v_mfma_f32_16x16x32_bf16 v[52:55], v[162:165], v[214:217], v[52:55]
	v_mfma_f32_16x16x32_bf16 v[48:51], v[182:185], v[214:217], v[48:51]
	v_mfma_f32_16x16x32_bf16 v[44:47], v[162:165], v[222:225], v[44:47]
	v_mfma_f32_16x16x32_bf16 v[40:43], v[182:185], v[222:225], v[40:43]
	v_mfma_f32_16x16x32_bf16 v[36:39], v[162:165], v[230:233], v[36:39]
	v_mfma_f32_16x16x32_bf16 v[32:35], v[182:185], v[230:233], v[32:35]
	v_mfma_f32_16x16x32_bf16 v[28:31], v[186:189], v[202:205], v[28:31]
	v_mfma_f32_16x16x32_bf16 v[24:27], v[194:197], v[202:205], v[24:27]
	v_mfma_f32_16x16x32_bf16 v[20:23], v[186:189], v[210:213], v[20:23]
	v_mfma_f32_16x16x32_bf16 v[16:19], v[194:197], v[210:213], v[16:19]
	v_mfma_f32_16x16x32_bf16 v[12:15], v[186:189], v[218:221], v[12:15]
	v_mfma_f32_16x16x32_bf16 v[8:11], v[194:197], v[218:221], v[8:11]
	v_mfma_f32_16x16x32_bf16 v[4:7], v[186:189], v[226:229], v[4:7]
	v_mfma_f32_16x16x32_bf16 v[0:3], v[194:197], v[226:229], v[0:3]
	v_mfma_f32_16x16x32_bf16 v[28:31], v[190:193], v[206:209], v[28:31]
	v_mfma_f32_16x16x32_bf16 v[24:27], v[198:201], v[206:209], v[24:27]
	v_mfma_f32_16x16x32_bf16 v[20:23], v[190:193], v[214:217], v[20:23]
	v_mfma_f32_16x16x32_bf16 v[16:19], v[198:201], v[214:217], v[16:19]
	v_mfma_f32_16x16x32_bf16 v[12:15], v[190:193], v[222:225], v[12:15]
	v_mfma_f32_16x16x32_bf16 v[8:11], v[198:201], v[222:225], v[8:11]
	v_mfma_f32_16x16x32_bf16 v[4:7], v[190:193], v[230:233], v[4:7]
	v_mfma_f32_16x16x32_bf16 v[0:3], v[198:201], v[230:233], v[0:3]
	s_barrier
	s_addk_i32 s5, 0x100
	s_add_i32 s18, s34, 2
	s_add_i32 s19, s34, 4
	s_cmp_ge_u32 s19, s70
	s_mov_b32 s34, s18
	s_cbranch_scc0 .LBB0_1776
	ds_read_b128 v[132:135], v128
	ds_read_b128 v[162:165], v128 offset:1024
	ds_read_b128 v[178:181], v128 offset:2048
	ds_read_b128 v[182:185], v128 offset:3072
	ds_read_b128 v[186:189], v129
	ds_read_b128 v[190:193], v129 offset:1024
	ds_read_b128 v[194:197], v129 offset:2048
	ds_read_b128 v[198:201], v129 offset:3072
	s_add_i32 s5, s73, s84
	s_add_u32 s50, s3, s5
	s_addc_u32 s51, s36, 0
	s_mov_b32 m0, vcc_lo
	v_lshl_add_u64 v[166:167], s[50:51], 0, v[148:149]
	ds_read_b128 v[202:205], v172
	ds_read_b128 v[206:209], v172 offset:1024
	ds_read_b128 v[210:213], v172 offset:2048
	ds_read_b128 v[214:217], v172 offset:3072
	ds_read_b128 v[218:221], v172 offset:4096
	ds_read_b128 v[222:225], v172 offset:5120
	ds_read_b128 v[226:229], v172 offset:6144
	ds_read_b128 v[230:233], v172 offset:7168
	global_load_lds_dwordx4 v[166:167], off
	v_lshl_add_u64 v[166:167], s[50:51], 0, v[146:147]
	s_mov_b32 m0, s35
	s_nop 0
	global_load_lds_dwordx4 v[166:167], off
	s_waitcnt vmcnt(8)
	s_waitcnt lgkmcnt(0)
	s_barrier
	s_waitcnt lgkmcnt(0)
	v_mfma_f32_16x16x32_bf16 v[124:127], v[132:135], v[202:205], v[124:127]
	v_mfma_f32_16x16x32_bf16 v[120:123], v[178:181], v[202:205], v[120:123]
	v_mfma_f32_16x16x32_bf16 v[116:119], v[132:135], v[210:213], v[116:119]
	v_mfma_f32_16x16x32_bf16 v[112:115], v[178:181], v[210:213], v[112:115]
	v_mfma_f32_16x16x32_bf16 v[108:111], v[132:135], v[218:221], v[108:111]
	v_mfma_f32_16x16x32_bf16 v[104:107], v[178:181], v[218:221], v[104:107]
	v_mfma_f32_16x16x32_bf16 v[100:103], v[132:135], v[226:229], v[100:103]
	v_mfma_f32_16x16x32_bf16 v[96:99], v[178:181], v[226:229], v[96:99]
	v_mfma_f32_16x16x32_bf16 v[124:127], v[162:165], v[206:209], v[124:127]
	v_mfma_f32_16x16x32_bf16 v[120:123], v[182:185], v[206:209], v[120:123]
	v_mfma_f32_16x16x32_bf16 v[116:119], v[162:165], v[214:217], v[116:119]
	v_mfma_f32_16x16x32_bf16 v[112:115], v[182:185], v[214:217], v[112:115]
	v_mfma_f32_16x16x32_bf16 v[108:111], v[162:165], v[222:225], v[108:111]
	v_mfma_f32_16x16x32_bf16 v[104:107], v[182:185], v[222:225], v[104:107]
	v_mfma_f32_16x16x32_bf16 v[100:103], v[162:165], v[230:233], v[100:103]
	v_mfma_f32_16x16x32_bf16 v[96:99], v[182:185], v[230:233], v[96:99]
	v_mfma_f32_16x16x32_bf16 v[92:95], v[186:189], v[202:205], v[92:95]
	v_mfma_f32_16x16x32_bf16 v[88:91], v[194:197], v[202:205], v[88:91]
	v_mfma_f32_16x16x32_bf16 v[84:87], v[186:189], v[210:213], v[84:87]
	v_mfma_f32_16x16x32_bf16 v[80:83], v[194:197], v[210:213], v[80:83]
	v_mfma_f32_16x16x32_bf16 v[76:79], v[186:189], v[218:221], v[76:79]
	v_mfma_f32_16x16x32_bf16 v[72:75], v[194:197], v[218:221], v[72:75]
	v_mfma_f32_16x16x32_bf16 v[68:71], v[186:189], v[226:229], v[68:71]
	v_mfma_f32_16x16x32_bf16 v[64:67], v[194:197], v[226:229], v[64:67]
	v_mfma_f32_16x16x32_bf16 v[92:95], v[190:193], v[206:209], v[92:95]
	v_mfma_f32_16x16x32_bf16 v[88:91], v[198:201], v[206:209], v[88:91]
	v_mfma_f32_16x16x32_bf16 v[84:87], v[190:193], v[214:217], v[84:87]
	v_mfma_f32_16x16x32_bf16 v[80:83], v[198:201], v[214:217], v[80:83]
	v_mfma_f32_16x16x32_bf16 v[76:79], v[190:193], v[222:225], v[76:79]
	v_mfma_f32_16x16x32_bf16 v[72:75], v[198:201], v[222:225], v[72:75]
	v_mfma_f32_16x16x32_bf16 v[68:71], v[190:193], v[230:233], v[68:71]
	v_mfma_f32_16x16x32_bf16 v[64:67], v[198:201], v[230:233], v[64:67]
	s_barrier
	s_ashr_i32 s5, s31, 31
	s_add_u32 s50, s8, s31
	s_addc_u32 s51, s9, s5
	s_add_i32 s5, s31, 0x8000
	s_mov_b32 m0, s27
	v_lshl_add_u64 v[166:167], s[50:51], 0, v[138:139]
	s_ashr_i32 s34, s5, 31
	ds_read_b128 v[202:205], v172 offset:16384
	ds_read_b128 v[206:209], v172 offset:17408
	ds_read_b128 v[210:213], v172 offset:18432
	ds_read_b128 v[214:217], v172 offset:19456
	ds_read_b128 v[218:221], v172 offset:20480
	ds_read_b128 v[222:225], v172 offset:21504
	ds_read_b128 v[226:229], v172 offset:22528
	ds_read_b128 v[230:233], v172 offset:23552
	global_load_lds_dwordx4 v[166:167], off
	v_lshl_add_u64 v[166:167], s[50:51], 0, v[140:141]
	s_add_u32 s50, s8, s5
	s_mov_b32 m0, vcc_hi
	s_addc_u32 s51, s9, s34
	global_load_lds_dwordx4 v[166:167], off
	v_lshl_add_u64 v[166:167], s[50:51], 0, v[138:139]
	s_mov_b32 m0, s59
	s_nop 0
	global_load_lds_dwordx4 v[166:167], off
	v_lshl_add_u64 v[166:167], s[50:51], 0, v[140:141]
	s_add_u32 s50, s37, s89
	s_mov_b32 m0, s60
	s_addc_u32 s51, s38, 0
	global_load_lds_dwordx4 v[166:167], off
	v_lshl_add_u64 v[166:167], s[50:51], 0, v[138:139]
	s_mov_b32 m0, s63
	s_nop 0
	global_load_lds_dwordx4 v[166:167], off
	v_lshl_add_u64 v[166:167], s[50:51], 0, v[140:141]
	s_mov_b32 m0, s66
	s_nop 0
	global_load_lds_dwordx4 v[166:167], off
	s_waitcnt vmcnt(8)
	s_waitcnt lgkmcnt(0)
	s_barrier
	s_waitcnt lgkmcnt(0)
	v_mfma_f32_16x16x32_bf16 v[60:63], v[132:135], v[202:205], v[60:63]
	v_mfma_f32_16x16x32_bf16 v[56:59], v[178:181], v[202:205], v[56:59]
	v_mfma_f32_16x16x32_bf16 v[52:55], v[132:135], v[210:213], v[52:55]
	v_mfma_f32_16x16x32_bf16 v[48:51], v[178:181], v[210:213], v[48:51]
	v_mfma_f32_16x16x32_bf16 v[44:47], v[132:135], v[218:221], v[44:47]
	v_mfma_f32_16x16x32_bf16 v[40:43], v[178:181], v[218:221], v[40:43]
	v_mfma_f32_16x16x32_bf16 v[36:39], v[132:135], v[226:229], v[36:39]
	v_mfma_f32_16x16x32_bf16 v[32:35], v[178:181], v[226:229], v[32:35]
	v_mfma_f32_16x16x32_bf16 v[60:63], v[162:165], v[206:209], v[60:63]
	v_mfma_f32_16x16x32_bf16 v[56:59], v[182:185], v[206:209], v[56:59]
	v_mfma_f32_16x16x32_bf16 v[52:55], v[162:165], v[214:217], v[52:55]
	v_mfma_f32_16x16x32_bf16 v[48:51], v[182:185], v[214:217], v[48:51]
	v_mfma_f32_16x16x32_bf16 v[44:47], v[162:165], v[222:225], v[44:47]
	v_mfma_f32_16x16x32_bf16 v[40:43], v[182:185], v[222:225], v[40:43]
	v_mfma_f32_16x16x32_bf16 v[36:39], v[162:165], v[230:233], v[36:39]
	v_mfma_f32_16x16x32_bf16 v[32:35], v[182:185], v[230:233], v[32:35]
	v_mfma_f32_16x16x32_bf16 v[28:31], v[186:189], v[202:205], v[28:31]
	v_mfma_f32_16x16x32_bf16 v[24:27], v[194:197], v[202:205], v[24:27]
	v_mfma_f32_16x16x32_bf16 v[20:23], v[186:189], v[210:213], v[20:23]
	v_mfma_f32_16x16x32_bf16 v[16:19], v[194:197], v[210:213], v[16:19]
	v_mfma_f32_16x16x32_bf16 v[4:7], v[186:189], v[226:229], v[4:7]
	v_mfma_f32_16x16x32_bf16 v[0:3], v[194:197], v[226:229], v[0:3]
	v_mfma_f32_16x16x32_bf16 v[28:31], v[190:193], v[206:209], v[28:31]
	v_mfma_f32_16x16x32_bf16 v[24:27], v[198:201], v[206:209], v[24:27]
	v_mfma_f32_16x16x32_bf16 v[20:23], v[190:193], v[214:217], v[20:23]
	v_mfma_f32_16x16x32_bf16 v[16:19], v[198:201], v[214:217], v[16:19]
	v_mfma_f32_16x16x32_bf16 v[12:15], v[186:189], v[218:221], v[12:15]
	v_mfma_f32_16x16x32_bf16 v[8:11], v[194:197], v[218:221], v[8:11]
	v_mfma_f32_16x16x32_bf16 v[4:7], v[190:193], v[230:233], v[4:7]
	v_mfma_f32_16x16x32_bf16 v[0:3], v[198:201], v[230:233], v[0:3]
	v_mfma_f32_16x16x32_bf16 v[12:15], v[190:193], v[222:225], v[12:15]
	v_mfma_f32_16x16x32_bf16 v[8:11], v[198:201], v[222:225], v[8:11]
	s_barrier
	ds_read_b128 v[132:135], v130
	ds_read_b128 v[162:165], v130 offset:1024
	ds_read_b128 v[178:181], v130 offset:2048
	ds_read_b128 v[182:185], v130 offset:3072
	ds_read_b128 v[186:189], v131
	ds_read_b128 v[190:193], v131 offset:1024
	ds_read_b128 v[194:197], v131 offset:2048
	ds_read_b128 v[198:201], v131 offset:3072
	s_add_i32 s5, s89, 0x8000
	s_add_u32 s50, s37, s5
	s_addc_u32 s51, s38, 0
	s_mov_b32 m0, s67
	v_lshl_add_u64 v[166:167], s[50:51], 0, v[138:139]
	ds_read_b128 v[202:205], v172 offset:32768
	ds_read_b128 v[206:209], v172 offset:33792
	ds_read_b128 v[210:213], v172 offset:34816
	ds_read_b128 v[214:217], v172 offset:35840
	ds_read_b128 v[218:221], v172 offset:36864
	ds_read_b128 v[222:225], v172 offset:37888
	ds_read_b128 v[226:229], v172 offset:38912
	ds_read_b128 v[230:233], v172 offset:39936
	global_load_lds_dwordx4 v[166:167], off
	v_lshl_add_u64 v[166:167], s[50:51], 0, v[140:141]
	s_mov_b32 m0, s68
	s_nop 0
	global_load_lds_dwordx4 v[166:167], off
	s_waitcnt vmcnt(8)
	s_waitcnt lgkmcnt(0)
	s_barrier
	s_waitcnt lgkmcnt(0)
	v_mfma_f32_16x16x32_bf16 v[124:127], v[132:135], v[202:205], v[124:127]
	v_mfma_f32_16x16x32_bf16 v[120:123], v[178:181], v[202:205], v[120:123]
	v_mfma_f32_16x16x32_bf16 v[116:119], v[132:135], v[210:213], v[116:119]
	v_mfma_f32_16x16x32_bf16 v[112:115], v[178:181], v[210:213], v[112:115]
	v_mfma_f32_16x16x32_bf16 v[108:111], v[132:135], v[218:221], v[108:111]
	v_mfma_f32_16x16x32_bf16 v[104:107], v[178:181], v[218:221], v[104:107]
	v_mfma_f32_16x16x32_bf16 v[100:103], v[132:135], v[226:229], v[100:103]
	v_mfma_f32_16x16x32_bf16 v[96:99], v[178:181], v[226:229], v[96:99]
	v_mfma_f32_16x16x32_bf16 v[124:127], v[162:165], v[206:209], v[124:127]
	v_mfma_f32_16x16x32_bf16 v[120:123], v[182:185], v[206:209], v[120:123]
	v_mfma_f32_16x16x32_bf16 v[116:119], v[162:165], v[214:217], v[116:119]
	v_mfma_f32_16x16x32_bf16 v[112:115], v[182:185], v[214:217], v[112:115]
	v_mfma_f32_16x16x32_bf16 v[108:111], v[162:165], v[222:225], v[108:111]
	v_mfma_f32_16x16x32_bf16 v[104:107], v[182:185], v[222:225], v[104:107]
	v_mfma_f32_16x16x32_bf16 v[100:103], v[162:165], v[230:233], v[100:103]
	v_mfma_f32_16x16x32_bf16 v[96:99], v[182:185], v[230:233], v[96:99]
	v_mfma_f32_16x16x32_bf16 v[92:95], v[186:189], v[202:205], v[92:95]
	v_mfma_f32_16x16x32_bf16 v[88:91], v[194:197], v[202:205], v[88:91]
	v_mfma_f32_16x16x32_bf16 v[84:87], v[186:189], v[210:213], v[84:87]
	v_mfma_f32_16x16x32_bf16 v[80:83], v[194:197], v[210:213], v[80:83]
	v_mfma_f32_16x16x32_bf16 v[76:79], v[186:189], v[218:221], v[76:79]
	v_mfma_f32_16x16x32_bf16 v[72:75], v[194:197], v[218:221], v[72:75]
	v_mfma_f32_16x16x32_bf16 v[68:71], v[186:189], v[226:229], v[68:71]
	v_mfma_f32_16x16x32_bf16 v[64:67], v[194:197], v[226:229], v[64:67]
	v_mfma_f32_16x16x32_bf16 v[92:95], v[190:193], v[206:209], v[92:95]
	v_mfma_f32_16x16x32_bf16 v[88:91], v[198:201], v[206:209], v[88:91]
	v_mfma_f32_16x16x32_bf16 v[84:87], v[190:193], v[214:217], v[84:87]
	v_mfma_f32_16x16x32_bf16 v[80:83], v[198:201], v[214:217], v[80:83]
	v_mfma_f32_16x16x32_bf16 v[76:79], v[190:193], v[222:225], v[76:79]
	v_mfma_f32_16x16x32_bf16 v[72:75], v[198:201], v[222:225], v[72:75]
	v_mfma_f32_16x16x32_bf16 v[68:71], v[190:193], v[230:233], v[68:71]
	v_mfma_f32_16x16x32_bf16 v[64:67], v[198:201], v[230:233], v[64:67]
	s_barrier
	s_add_i32 s50, s31, 0x80
	s_ashr_i32 s51, s50, 31
	s_add_i32 s5, s31, 0x8080
	s_mov_b32 m0, s61
	v_lshl_add_u64 v[166:167], v[154:155], 0, s[50:51]
	s_ashr_i32 s31, s5, 31
	ds_read_b128 v[202:205], v172 offset:49152
	ds_read_b128 v[206:209], v172 offset:50176
	ds_read_b128 v[210:213], v172 offset:51200
	ds_read_b128 v[214:217], v172 offset:52224
	ds_read_b128 v[218:221], v172 offset:53248
	ds_read_b128 v[222:225], v172 offset:54272
	ds_read_b128 v[226:229], v172 offset:55296
	ds_read_b128 v[230:233], v172 offset:56320
	global_load_lds_dwordx4 v[166:167], off
	v_lshl_add_u64 v[166:167], v[156:157], 0, s[50:51]
	s_add_u32 s50, s8, s5
	s_mov_b32 m0, s49
	s_addc_u32 s51, s9, s31
	global_load_lds_dwordx4 v[166:167], off
	v_lshl_add_u64 v[166:167], s[50:51], 0, v[138:139]
	s_mov_b32 m0, s26
	s_add_i32 s5, s89, 0x80
	global_load_lds_dwordx4 v[166:167], off
	v_lshl_add_u64 v[166:167], s[50:51], 0, v[140:141]
	s_add_u32 s50, s37, s5
	s_mov_b32 m0, s44
	s_addc_u32 s51, s38, 0
	global_load_lds_dwordx4 v[166:167], off
	v_lshl_add_u64 v[166:167], s[50:51], 0, v[138:139]
	s_mov_b32 m0, s71
	s_nop 0
	global_load_lds_dwordx4 v[166:167], off
	v_lshl_add_u64 v[166:167], s[50:51], 0, v[140:141]
	s_mov_b32 m0, s72
	s_nop 0
	global_load_lds_dwordx4 v[166:167], off
	s_waitcnt vmcnt(8)
	s_waitcnt lgkmcnt(0)
	s_barrier
	s_waitcnt lgkmcnt(0)
	v_mfma_f32_16x16x32_bf16 v[60:63], v[132:135], v[202:205], v[60:63]
	v_mfma_f32_16x16x32_bf16 v[56:59], v[178:181], v[202:205], v[56:59]
	v_mfma_f32_16x16x32_bf16 v[52:55], v[132:135], v[210:213], v[52:55]
	v_mfma_f32_16x16x32_bf16 v[48:51], v[178:181], v[210:213], v[48:51]
	v_mfma_f32_16x16x32_bf16 v[44:47], v[132:135], v[218:221], v[44:47]
	v_mfma_f32_16x16x32_bf16 v[40:43], v[178:181], v[218:221], v[40:43]
	v_mfma_f32_16x16x32_bf16 v[36:39], v[132:135], v[226:229], v[36:39]
	v_mfma_f32_16x16x32_bf16 v[32:35], v[178:181], v[226:229], v[32:35]
	v_mfma_f32_16x16x32_bf16 v[60:63], v[162:165], v[206:209], v[60:63]
	v_mfma_f32_16x16x32_bf16 v[56:59], v[182:185], v[206:209], v[56:59]
	v_mfma_f32_16x16x32_bf16 v[52:55], v[162:165], v[214:217], v[52:55]
	v_mfma_f32_16x16x32_bf16 v[48:51], v[182:185], v[214:217], v[48:51]
	v_mfma_f32_16x16x32_bf16 v[44:47], v[162:165], v[222:225], v[44:47]
	v_mfma_f32_16x16x32_bf16 v[40:43], v[182:185], v[222:225], v[40:43]
	v_mfma_f32_16x16x32_bf16 v[36:39], v[162:165], v[230:233], v[36:39]
	v_mfma_f32_16x16x32_bf16 v[32:35], v[182:185], v[230:233], v[32:35]
	v_mfma_f32_16x16x32_bf16 v[28:31], v[186:189], v[202:205], v[28:31]
	v_mfma_f32_16x16x32_bf16 v[24:27], v[194:197], v[202:205], v[24:27]
	v_mfma_f32_16x16x32_bf16 v[20:23], v[186:189], v[210:213], v[20:23]
	v_mfma_f32_16x16x32_bf16 v[16:19], v[194:197], v[210:213], v[16:19]
	v_mfma_f32_16x16x32_bf16 v[4:7], v[186:189], v[226:229], v[4:7]
	v_mfma_f32_16x16x32_bf16 v[0:3], v[194:197], v[226:229], v[0:3]
	v_mfma_f32_16x16x32_bf16 v[28:31], v[190:193], v[206:209], v[28:31]
	v_mfma_f32_16x16x32_bf16 v[24:27], v[198:201], v[206:209], v[24:27]
	v_mfma_f32_16x16x32_bf16 v[20:23], v[190:193], v[214:217], v[20:23]
	v_mfma_f32_16x16x32_bf16 v[16:19], v[198:201], v[214:217], v[16:19]
	v_mfma_f32_16x16x32_bf16 v[12:15], v[186:189], v[218:221], v[12:15]
	v_mfma_f32_16x16x32_bf16 v[8:11], v[194:197], v[218:221], v[8:11]
	v_mfma_f32_16x16x32_bf16 v[4:7], v[190:193], v[230:233], v[4:7]
	v_mfma_f32_16x16x32_bf16 v[0:3], v[198:201], v[230:233], v[0:3]
	v_mfma_f32_16x16x32_bf16 v[12:15], v[190:193], v[222:225], v[12:15]
	v_mfma_f32_16x16x32_bf16 v[8:11], v[198:201], v[222:225], v[8:11]
	s_barrier
	ds_read_b128 v[132:135], v128
	ds_read_b128 v[162:165], v128 offset:1024
	ds_read_b128 v[178:181], v128 offset:2048
	ds_read_b128 v[182:185], v128 offset:3072
	ds_read_b128 v[186:189], v129
	ds_read_b128 v[190:193], v129 offset:1024
	ds_read_b128 v[194:197], v129 offset:2048
	ds_read_b128 v[198:201], v129 offset:3072
	s_add_i32 s5, s89, 0x8080
	s_add_u32 s50, s37, s5
	s_addc_u32 s51, s38, 0
	s_mov_b32 m0, vcc_lo
	v_lshl_add_u64 v[128:129], s[50:51], 0, v[138:139]
	ds_read_b128 v[202:205], v172
	ds_read_b128 v[206:209], v172 offset:1024
	ds_read_b128 v[210:213], v172 offset:2048
	ds_read_b128 v[214:217], v172 offset:3072
	ds_read_b128 v[218:221], v172 offset:4096
	ds_read_b128 v[222:225], v172 offset:5120
	ds_read_b128 v[226:229], v172 offset:6144
	ds_read_b128 v[230:233], v172 offset:7168
	global_load_lds_dwordx4 v[128:129], off
	v_lshl_add_u64 v[128:129], s[50:51], 0, v[140:141]
	s_mov_b32 m0, s35
	s_nop 0
	global_load_lds_dwordx4 v[128:129], off
	s_waitcnt vmcnt(8)
	s_waitcnt lgkmcnt(0)
	s_barrier
	s_waitcnt lgkmcnt(0)
	v_mfma_f32_16x16x32_bf16 v[124:127], v[132:135], v[202:205], v[124:127]
	v_mfma_f32_16x16x32_bf16 v[120:123], v[178:181], v[202:205], v[120:123]
	v_mfma_f32_16x16x32_bf16 v[116:119], v[132:135], v[210:213], v[116:119]
	v_mfma_f32_16x16x32_bf16 v[112:115], v[178:181], v[210:213], v[112:115]
	v_mfma_f32_16x16x32_bf16 v[108:111], v[132:135], v[218:221], v[108:111]
	v_mfma_f32_16x16x32_bf16 v[104:107], v[178:181], v[218:221], v[104:107]
	v_mfma_f32_16x16x32_bf16 v[124:127], v[162:165], v[206:209], v[124:127]
	v_mfma_f32_16x16x32_bf16 v[120:123], v[182:185], v[206:209], v[120:123]
	v_mfma_f32_16x16x32_bf16 v[116:119], v[162:165], v[214:217], v[116:119]
	v_mfma_f32_16x16x32_bf16 v[112:115], v[182:185], v[214:217], v[112:115]
	v_mfma_f32_16x16x32_bf16 v[108:111], v[162:165], v[222:225], v[108:111]
	v_mfma_f32_16x16x32_bf16 v[104:107], v[182:185], v[222:225], v[104:107]
	v_mfma_f32_16x16x32_bf16 v[100:103], v[132:135], v[226:229], v[100:103]
	v_mfma_f32_16x16x32_bf16 v[96:99], v[178:181], v[226:229], v[96:99]
	v_mfma_f32_16x16x32_bf16 v[234:237], v[162:165], v[230:233], v[100:103]
	v_mfma_f32_16x16x32_bf16 v[238:241], v[182:185], v[230:233], v[96:99]
	v_mfma_f32_16x16x32_bf16 v[92:95], v[186:189], v[202:205], v[92:95]
	v_mfma_f32_16x16x32_bf16 v[88:91], v[194:197], v[202:205], v[88:91]
	v_mfma_f32_16x16x32_bf16 v[76:79], v[186:189], v[218:221], v[76:79]
	v_mfma_f32_16x16x32_bf16 v[72:75], v[194:197], v[218:221], v[72:75]
	v_mfma_f32_16x16x32_bf16 v[68:71], v[186:189], v[226:229], v[68:71]
	v_mfma_f32_16x16x32_bf16 v[64:67], v[194:197], v[226:229], v[64:67]
	v_mfma_f32_16x16x32_bf16 v[92:95], v[190:193], v[206:209], v[92:95]
	v_mfma_f32_16x16x32_bf16 v[88:91], v[198:201], v[206:209], v[88:91]
	v_mfma_f32_16x16x32_bf16 v[84:87], v[186:189], v[210:213], v[84:87]
	v_mfma_f32_16x16x32_bf16 v[80:83], v[194:197], v[210:213], v[80:83]
	v_mfma_f32_16x16x32_bf16 v[76:79], v[190:193], v[222:225], v[76:79]
	v_mfma_f32_16x16x32_bf16 v[72:75], v[198:201], v[222:225], v[72:75]
	v_mfma_f32_16x16x32_bf16 v[68:71], v[190:193], v[230:233], v[68:71]
	v_mfma_f32_16x16x32_bf16 v[64:67], v[198:201], v[230:233], v[64:67]
	v_mfma_f32_16x16x32_bf16 v[202:205], v[190:193], v[214:217], v[84:87]
	v_mfma_f32_16x16x32_bf16 v[206:209], v[198:201], v[214:217], v[80:83]
	s_barrier
	s_ashr_i32 s5, s85, 31
	s_add_u32 s34, s6, s85
	s_addc_u32 s35, s7, s5
	s_add_i32 s5, s85, 0xffffff00
	s_mov_b32 m0, s27
	v_lshl_add_u64 v[128:129], s[34:35], 0, v[144:145]
	s_ashr_i32 s27, s5, 31
	ds_read_b128 v[80:83], v172 offset:16384
	ds_read_b128 v[84:87], v172 offset:17408
	ds_read_b128 v[96:99], v172 offset:18432
	ds_read_b128 v[100:103], v172 offset:19456
	ds_read_b128 v[210:213], v172 offset:20480
	ds_read_b128 v[214:217], v172 offset:21504
	ds_read_b128 v[218:221], v172 offset:22528
	ds_read_b128 v[222:225], v172 offset:23552
	global_load_lds_dwordx4 v[128:129], off
	v_lshl_add_u64 v[128:129], s[34:35], 0, v[142:143]
	s_add_u32 s34, s6, s5
	s_mov_b32 m0, vcc_hi
	s_addc_u32 s35, s7, s27
	global_load_lds_dwordx4 v[128:129], off
	v_lshl_add_u64 v[128:129], s[34:35], 0, v[144:145]
	s_mov_b32 m0, s59
	s_nop 0
	global_load_lds_dwordx4 v[128:129], off
	v_lshl_add_u64 v[128:129], s[34:35], 0, v[142:143]
	s_add_u32 s34, s3, s4
	s_mov_b32 m0, s60
	s_addc_u32 s35, s36, 0
	global_load_lds_dwordx4 v[128:129], off
	v_lshl_add_u64 v[128:129], s[34:35], 0, v[148:149]
	s_mov_b32 m0, s63
	s_nop 0
	global_load_lds_dwordx4 v[128:129], off
	v_lshl_add_u64 v[128:129], s[34:35], 0, v[146:147]
	s_mov_b32 m0, s66
	s_nop 0
	global_load_lds_dwordx4 v[128:129], off
	s_waitcnt vmcnt(8)
	s_waitcnt lgkmcnt(0)
	s_barrier
	s_waitcnt lgkmcnt(0)
	v_mfma_f32_16x16x32_bf16 v[60:63], v[132:135], v[80:83], v[60:63]
	v_mfma_f32_16x16x32_bf16 v[56:59], v[178:181], v[80:83], v[56:59]
	v_mfma_f32_16x16x32_bf16 v[52:55], v[132:135], v[96:99], v[52:55]
	v_mfma_f32_16x16x32_bf16 v[48:51], v[178:181], v[96:99], v[48:51]
	v_mfma_f32_16x16x32_bf16 v[44:47], v[132:135], v[210:213], v[44:47]
	v_mfma_f32_16x16x32_bf16 v[40:43], v[178:181], v[210:213], v[40:43]
	v_mfma_f32_16x16x32_bf16 v[60:63], v[162:165], v[84:87], v[60:63]
	v_mfma_f32_16x16x32_bf16 v[56:59], v[182:185], v[84:87], v[56:59]
	v_mfma_f32_16x16x32_bf16 v[52:55], v[162:165], v[100:103], v[52:55]
	v_mfma_f32_16x16x32_bf16 v[48:51], v[182:185], v[100:103], v[48:51]
	v_mfma_f32_16x16x32_bf16 v[44:47], v[162:165], v[214:217], v[44:47]
	v_mfma_f32_16x16x32_bf16 v[40:43], v[182:185], v[214:217], v[40:43]
	v_mfma_f32_16x16x32_bf16 v[36:39], v[132:135], v[218:221], v[36:39]
	v_mfma_f32_16x16x32_bf16 v[32:35], v[178:181], v[218:221], v[32:35]
	v_mfma_f32_16x16x32_bf16 v[162:165], v[162:165], v[222:225], v[36:39]
	v_mfma_f32_16x16x32_bf16 v[178:181], v[182:185], v[222:225], v[32:35]
	v_mfma_f32_16x16x32_bf16 v[28:31], v[186:189], v[80:83], v[28:31]
	v_mfma_f32_16x16x32_bf16 v[24:27], v[194:197], v[80:83], v[24:27]
	v_mfma_f32_16x16x32_bf16 v[4:7], v[186:189], v[218:221], v[4:7]
	v_mfma_f32_16x16x32_bf16 v[0:3], v[194:197], v[218:221], v[0:3]
	v_mfma_f32_16x16x32_bf16 v[28:31], v[190:193], v[84:87], v[28:31]
	v_mfma_f32_16x16x32_bf16 v[24:27], v[198:201], v[84:87], v[24:27]
	v_mfma_f32_16x16x32_bf16 v[20:23], v[186:189], v[96:99], v[20:23]
	v_mfma_f32_16x16x32_bf16 v[16:19], v[194:197], v[96:99], v[16:19]
	v_mfma_f32_16x16x32_bf16 v[12:15], v[186:189], v[210:213], v[12:15]
	v_mfma_f32_16x16x32_bf16 v[8:11], v[194:197], v[210:213], v[8:11]
	v_mfma_f32_16x16x32_bf16 v[4:7], v[190:193], v[222:225], v[4:7]
	v_mfma_f32_16x16x32_bf16 v[0:3], v[198:201], v[222:225], v[0:3]
	v_mfma_f32_16x16x32_bf16 v[182:185], v[190:193], v[100:103], v[20:23]
	v_mfma_f32_16x16x32_bf16 v[226:229], v[198:201], v[100:103], v[16:19]
	v_mfma_f32_16x16x32_bf16 v[12:15], v[190:193], v[214:217], v[12:15]
	v_mfma_f32_16x16x32_bf16 v[8:11], v[198:201], v[214:217], v[8:11]
	s_barrier
	ds_read_b128 v[16:19], v130
	ds_read_b128 v[20:23], v130 offset:1024
	ds_read_b128 v[186:189], v130 offset:2048
	ds_read_b128 v[190:193], v130 offset:3072
	ds_read_b128 v[194:197], v131
	ds_read_b128 v[198:201], v131 offset:1024
	ds_read_b128 v[210:213], v131 offset:2048
	ds_read_b128 v[214:217], v131 offset:3072
	s_add_i32 s5, s4, 0x20000
	s_add_u32 s34, s3, s5
	s_addc_u32 s35, s36, 0
	s_mov_b32 m0, s67
	v_lshl_add_u64 v[80:81], s[34:35], 0, v[148:149]
	ds_read_b128 v[32:35], v172 offset:32768
	ds_read_b128 v[36:39], v172 offset:33792
	ds_read_b128 v[218:221], v172 offset:34816
	ds_read_b128 v[222:225], v172 offset:35840
	ds_read_b128 v[230:233], v172 offset:36864
	ds_read_b128 v[242:245], v172 offset:37888
	ds_read_b128 v[246:249], v172 offset:38912
	ds_read_b128 v[250:253], v172 offset:39936
	global_load_lds_dwordx4 v[80:81], off
	v_lshl_add_u64 v[80:81], s[34:35], 0, v[146:147]
	s_mov_b32 m0, s68
	s_nop 0
	global_load_lds_dwordx4 v[80:81], off
	s_waitcnt vmcnt(8)
	s_waitcnt lgkmcnt(0)
	s_barrier
; #define PG_BAR __builtin_amdgcn_s_barrier()
; template <class Epi, class Sched, class Hook = NoHook>
; __device__ __forceinline__ void gemm_phase_w(LAS unsigned char* lds, const Sched& S, const Epi& E, int wave_id, const Hook& HK = Hook()) {
;     ...
;         if constexpr (!SEG2) {
;             for (int tt = 0; tt < nt; tt += 2) {
;                 if constexpr (GATHER) { if (tt == nt - 2) {
;                     if (has_next) { gnxt_00 = S.grow_l(nxt, lds, nbuf, R0) + (unsigned)(C0 * 2); gnxt_01 = S.grow_l(nxt, lds, nbuf, R1) + (unsigned)(C1 * 2); gnxt_10 = S.grow_l(nxt, lds, nbuf, 128 + R0) + (unsigned)(C0 * 2); gnxt_11 = S.grow_l(nxt, lds, nbuf, 128 + R1) + (unsigned)(C1 * 2); }
;                     else { gnxt_00 = gcur_00; gnxt_01 = gcur_01; gnxt_10 = gcur_10; gnxt_11 = gcur_11; } } }
;                 PG_TRIP(tt, false, false, false);
;             }
;         } else {
;             for (int tt = 0; tt < nt - 4; tt += 2) PG_TRIP(tt, false, false, false);
;             PG_TRIP(nt - 4, false, true, false);
;             PG_TRIP(nt - 2, true, false, true);
;         }
;     ...
;         if (wr == 0) PG_BAR;
	s_waitcnt lgkmcnt(0)
	v_mfma_f32_16x16x32_bf16 v[80:83], v[16:19], v[32:35], v[124:127]
	v_mfma_f32_16x16x32_bf16 v[132:135], v[20:23], v[36:39], v[80:83]
	v_mfma_f32_16x16x32_bf16 v[80:83], v[186:189], v[32:35], v[120:123]
	v_mfma_f32_16x16x32_bf16 v[128:131], v[190:193], v[36:39], v[80:83]
	v_mfma_f32_16x16x32_bf16 v[80:83], v[16:19], v[218:221], v[116:119]
	v_mfma_f32_16x16x32_bf16 v[116:119], v[20:23], v[222:225], v[80:83]
	v_mfma_f32_16x16x32_bf16 v[80:83], v[186:189], v[218:221], v[112:115]
	v_mfma_f32_16x16x32_bf16 v[112:115], v[190:193], v[222:225], v[80:83]
	v_mfma_f32_16x16x32_bf16 v[80:83], v[16:19], v[230:233], v[108:111]
	v_mfma_f32_16x16x32_bf16 v[100:103], v[20:23], v[242:245], v[80:83]
	v_mfma_f32_16x16x32_bf16 v[80:83], v[186:189], v[230:233], v[104:107]
	v_mfma_f32_16x16x32_bf16 v[96:99], v[190:193], v[242:245], v[80:83]
	v_mfma_f32_16x16x32_bf16 v[80:83], v[16:19], v[246:249], v[234:237]
	v_mfma_f32_16x16x32_bf16 v[84:87], v[20:23], v[250:253], v[80:83]
	v_mfma_f32_16x16x32_bf16 v[80:83], v[186:189], v[246:249], v[238:241]
	v_mfma_f32_16x16x32_bf16 v[80:83], v[190:193], v[250:253], v[80:83]
	v_mfma_f32_16x16x32_bf16 v[92:95], v[194:197], v[32:35], v[92:95]
	v_mfma_f32_16x16x32_bf16 v[32:35], v[210:213], v[32:35], v[88:91]
	v_mfma_f32_16x16x32_bf16 v[120:123], v[214:217], v[36:39], v[32:35]
	v_mfma_f32_16x16x32_bf16 v[32:35], v[194:197], v[218:221], v[202:205]
	v_mfma_f32_16x16x32_bf16 v[108:111], v[198:201], v[222:225], v[32:35]
	v_mfma_f32_16x16x32_bf16 v[32:35], v[210:213], v[218:221], v[206:209]
	v_mfma_f32_16x16x32_bf16 v[104:107], v[214:217], v[222:225], v[32:35]
	v_mfma_f32_16x16x32_bf16 v[32:35], v[194:197], v[230:233], v[76:79]
	v_mfma_f32_16x16x32_bf16 v[124:127], v[198:201], v[36:39], v[92:95]
	v_mfma_f32_16x16x32_bf16 v[92:95], v[198:201], v[242:245], v[32:35]
	v_mfma_f32_16x16x32_bf16 v[32:35], v[210:213], v[230:233], v[72:75]
	v_mfma_f32_16x16x32_bf16 v[88:91], v[214:217], v[242:245], v[32:35]
	v_mfma_f32_16x16x32_bf16 v[32:35], v[194:197], v[246:249], v[68:71]
	v_mfma_f32_16x16x32_bf16 v[76:79], v[198:201], v[250:253], v[32:35]
	v_mfma_f32_16x16x32_bf16 v[32:35], v[210:213], v[246:249], v[64:67]
	v_mfma_f32_16x16x32_bf16 v[72:75], v[214:217], v[250:253], v[32:35]
	s_barrier
	s_add_i32 s34, s85, 0x80
	s_ashr_i32 s35, s34, 31
	s_add_i32 s5, s85, 0xffffff80
	s_mov_b32 m0, s61
	s_nop 0
	v_lshl_add_u64 v[32:33], v[158:159], 0, s[34:35]
	s_ashr_i32 s27, s5, 31
	ds_read_b128 v[202:205], v172 offset:49152
	ds_read_b128 v[206:209], v172 offset:50176
	ds_read_b128 v[218:221], v172 offset:51200
	ds_read_b128 v[222:225], v172 offset:52224
	ds_read_b128 v[230:233], v172 offset:53248
	ds_read_b128 v[234:237], v172 offset:54272
	ds_read_b128 v[238:241], v172 offset:55296
	ds_read_b128 v[242:245], v172 offset:56320
	global_load_lds_dwordx4 v[32:33], off
	v_lshl_add_u64 v[32:33], v[160:161], 0, s[34:35]
	s_add_u32 s34, s6, s5
	s_mov_b32 m0, s49
	s_addc_u32 s35, s7, s27
	s_add_i32 s5, s4, 0x80
	global_load_lds_dwordx4 v[32:33], off
	v_lshl_add_u64 v[32:33], s[34:35], 0, v[144:145]
	s_mov_b32 m0, s26
	s_add_u32 s26, s3, s5
	global_load_lds_dwordx4 v[32:33], off
	v_lshl_add_u64 v[32:33], s[34:35], 0, v[142:143]
	s_mov_b32 m0, s44
	s_addc_u32 s27, s36, 0
	global_load_lds_dwordx4 v[32:33], off
	v_lshl_add_u64 v[32:33], s[26:27], 0, v[148:149]
	s_mov_b32 m0, s71
	s_nop 0
	global_load_lds_dwordx4 v[32:33], off
	v_lshl_add_u64 v[32:33], s[26:27], 0, v[146:147]
	s_mov_b32 m0, s72
	s_nop 0
	global_load_lds_dwordx4 v[32:33], off
	s_waitcnt vmcnt(8)
	s_waitcnt lgkmcnt(0)
	s_barrier
	s_waitcnt lgkmcnt(0)
	v_mfma_f32_16x16x32_bf16 v[32:35], v[16:19], v[202:205], v[60:63]
	v_mfma_f32_16x16x32_bf16 v[68:71], v[20:23], v[206:209], v[32:35]
	v_mfma_f32_16x16x32_bf16 v[32:35], v[186:189], v[202:205], v[56:59]
	v_mfma_f32_16x16x32_bf16 v[64:67], v[190:193], v[206:209], v[32:35]
	v_mfma_f32_16x16x32_bf16 v[32:35], v[16:19], v[218:221], v[52:55]
	v_mfma_f32_16x16x32_bf16 v[52:55], v[20:23], v[222:225], v[32:35]
	v_mfma_f32_16x16x32_bf16 v[32:35], v[186:189], v[218:221], v[48:51]
	v_mfma_f32_16x16x32_bf16 v[48:51], v[190:193], v[222:225], v[32:35]
	v_mfma_f32_16x16x32_bf16 v[32:35], v[16:19], v[230:233], v[44:47]
	v_mfma_f32_16x16x32_bf16 v[16:19], v[16:19], v[238:241], v[162:165]
	v_mfma_f32_16x16x32_bf16 v[36:39], v[20:23], v[234:237], v[32:35]
	v_mfma_f32_16x16x32_bf16 v[32:35], v[186:189], v[230:233], v[40:43]
	v_mfma_f32_16x16x32_bf16 v[20:23], v[20:23], v[242:245], v[16:19]
	v_mfma_f32_16x16x32_bf16 v[16:19], v[186:189], v[238:241], v[178:181]
	v_mfma_f32_16x16x32_bf16 v[32:35], v[190:193], v[234:237], v[32:35]
	v_mfma_f32_16x16x32_bf16 v[16:19], v[190:193], v[242:245], v[16:19]
	v_mfma_f32_16x16x32_bf16 v[24:27], v[210:213], v[202:205], v[24:27]
	v_mfma_f32_16x16x32_bf16 v[56:59], v[214:217], v[206:209], v[24:27]
	v_mfma_f32_16x16x32_bf16 v[24:27], v[194:197], v[218:221], v[182:185]
	v_mfma_f32_16x16x32_bf16 v[28:31], v[194:197], v[202:205], v[28:31]
	v_mfma_f32_16x16x32_bf16 v[44:47], v[198:201], v[222:225], v[24:27]
	v_mfma_f32_16x16x32_bf16 v[24:27], v[210:213], v[218:221], v[226:229]
	v_mfma_f32_16x16x32_bf16 v[12:15], v[194:197], v[230:233], v[12:15]
	v_mfma_f32_16x16x32_bf16 v[8:11], v[210:213], v[230:233], v[8:11]
	v_mfma_f32_16x16x32_bf16 v[4:7], v[194:197], v[238:241], v[4:7]
	v_mfma_f32_16x16x32_bf16 v[0:3], v[210:213], v[238:241], v[0:3]
	v_mfma_f32_16x16x32_bf16 v[60:63], v[198:201], v[206:209], v[28:31]
	v_mfma_f32_16x16x32_bf16 v[40:43], v[214:217], v[222:225], v[24:27]
	v_mfma_f32_16x16x32_bf16 v[28:31], v[198:201], v[234:237], v[12:15]
	v_mfma_f32_16x16x32_bf16 v[24:27], v[214:217], v[234:237], v[8:11]
	v_mfma_f32_16x16x32_bf16 v[4:7], v[198:201], v[242:245], v[4:7]
	v_mfma_f32_16x16x32_bf16 v[0:3], v[214:217], v[242:245], v[0:3]
	s_barrier
	s_and_b64 vcc, exec, s[64:65]
	s_cbranch_vccz .LBB0_1779
	s_barrier

.LBB0_1854:
	s_add_i32 s53, s21, 2
	s_cmp_eq_u32 s20, 0x9f000
	s_cselect_b32 s59, s48, s51
	s_cselect_b32 s60, 0, s53
	s_cselect_b32 s58, s49, s52
	s_add_i32 s61, s52, s20
	s_add_u32 s62, s3, s61
	s_addc_u32 s63, s30, 0
	v_lshl_add_u64 v[190:191], s[62:63], 0, v[164:165]
	s_add_i32 m0, s23, 0xc000
	s_nop 0
	global_load_lds_dwordx4 v[190:191], off
	v_lshl_add_u64 v[190:191], s[62:63], 0, v[166:167]
	s_add_i32 m0, s23, 0xe000
	s_nop 0
	global_load_lds_dwordx4 v[190:191], off
	ds_read_b128 v[100:103], v197
	ds_read_b128 v[132:135], v197 offset:1024
	ds_read_b128 v[136:139], v197 offset:2048
	ds_read_b128 v[140:143], v197 offset:3072
	ds_read_b128 v[144:147], v198
	ds_read_b128 v[148:151], v198 offset:1024
	ds_read_b128 v[152:155], v198 offset:2048
	ds_read_b128 v[156:159], v198 offset:3072
	ds_read_b128 v[160:163], v199
	ds_read_b128 v[174:177], v199 offset:1024
	ds_read_b128 v[178:181], v199 offset:2048
	ds_read_b128 v[182:185], v199 offset:3072
	ds_read_b128 v[186:189], v199 offset:4096
	ds_read_b128 v[200:203], v199 offset:5120
	ds_read_b128 v[204:207], v199 offset:6144
	ds_read_b128 v[208:211], v199 offset:7168
	s_waitcnt vmcnt(8)
	s_waitcnt lgkmcnt(0)
	s_barrier
	s_waitcnt lgkmcnt(0)
	v_mfma_f32_16x16x32_bf16 v[128:131], v[100:103], v[160:163], v[128:131]
	v_mfma_f32_16x16x32_bf16 v[124:127], v[136:139], v[160:163], v[124:127]
	v_mfma_f32_16x16x32_bf16 v[116:119], v[100:103], v[178:181], v[116:119]
	v_mfma_f32_16x16x32_bf16 v[108:111], v[136:139], v[178:181], v[108:111]
	v_mfma_f32_16x16x32_bf16 v[92:95], v[100:103], v[186:189], v[92:95]
	v_mfma_f32_16x16x32_bf16 v[84:87], v[136:139], v[186:189], v[84:87]
	v_mfma_f32_16x16x32_bf16 v[76:79], v[100:103], v[204:207], v[76:79]
	v_mfma_f32_16x16x32_bf16 v[68:71], v[136:139], v[204:207], v[68:71]
	v_mfma_f32_16x16x32_bf16 v[128:131], v[132:135], v[174:177], v[128:131]
	v_mfma_f32_16x16x32_bf16 v[124:127], v[140:143], v[174:177], v[124:127]
	v_mfma_f32_16x16x32_bf16 v[116:119], v[132:135], v[182:185], v[116:119]
	v_mfma_f32_16x16x32_bf16 v[108:111], v[140:143], v[182:185], v[108:111]
	v_mfma_f32_16x16x32_bf16 v[92:95], v[132:135], v[200:203], v[92:95]
	v_mfma_f32_16x16x32_bf16 v[84:87], v[140:143], v[200:203], v[84:87]
	v_mfma_f32_16x16x32_bf16 v[76:79], v[132:135], v[208:211], v[76:79]
	v_mfma_f32_16x16x32_bf16 v[68:71], v[140:143], v[208:211], v[68:71]
	v_mfma_f32_16x16x32_bf16 v[96:99], v[144:147], v[160:163], v[96:99]
	v_mfma_f32_16x16x32_bf16 v[120:123], v[152:155], v[160:163], v[120:123]
	v_mfma_f32_16x16x32_bf16 v[112:115], v[144:147], v[178:181], v[112:115]
	v_mfma_f32_16x16x32_bf16 v[104:107], v[152:155], v[178:181], v[104:107]
	v_mfma_f32_16x16x32_bf16 v[88:91], v[144:147], v[186:189], v[88:91]
	v_mfma_f32_16x16x32_bf16 v[80:83], v[152:155], v[186:189], v[80:83]
	v_mfma_f32_16x16x32_bf16 v[72:75], v[144:147], v[204:207], v[72:75]
	v_mfma_f32_16x16x32_bf16 v[64:67], v[152:155], v[204:207], v[64:67]
	v_mfma_f32_16x16x32_bf16 v[96:99], v[148:151], v[174:177], v[96:99]
	v_mfma_f32_16x16x32_bf16 v[120:123], v[156:159], v[174:177], v[120:123]
	v_mfma_f32_16x16x32_bf16 v[112:115], v[148:151], v[182:185], v[112:115]
	v_mfma_f32_16x16x32_bf16 v[104:107], v[156:159], v[182:185], v[104:107]
	v_mfma_f32_16x16x32_bf16 v[88:91], v[148:151], v[200:203], v[88:91]
	v_mfma_f32_16x16x32_bf16 v[80:83], v[156:159], v[200:203], v[80:83]
	v_mfma_f32_16x16x32_bf16 v[72:75], v[148:151], v[208:211], v[72:75]
	v_mfma_f32_16x16x32_bf16 v[64:67], v[156:159], v[208:211], v[64:67]
	s_barrier
	s_lshl_b32 s61, s60, 7
	s_add_i32 s62, s61, s59
	s_ashr_i32 s63, s62, 31
	s_add_u32 s62, s4, s62
	s_addc_u32 s63, s5, s63
	s_add_i32 s66, s42, s31
	v_lshl_add_u64 v[190:191], s[62:63], 0, v[168:169]
	s_mov_b32 m0, s66
	s_nop 0
	global_load_lds_dwordx4 v[190:191], off
	s_add_i32 m0, s66, 0x2000
	s_add_i32 s66, s59, 0x80000
	s_add_i32 s61, s66, s61
	v_lshl_add_u64 v[190:191], s[62:63], 0, v[170:171]
	s_ashr_i32 s63, s61, 31
	s_add_u32 s62, s4, s61
	s_addc_u32 s63, s5, s63
	s_add_i32 s61, s43, s31
	global_load_lds_dwordx4 v[190:191], off
	v_lshl_add_u64 v[190:191], s[62:63], 0, v[168:169]
	s_mov_b32 m0, s61
	s_nop 0
	global_load_lds_dwordx4 v[190:191], off
	s_add_i32 m0, s61, 0x2000
	s_lshl_b32 s61, s60, 12
	s_add_i32 s61, s61, s58
	v_lshl_add_u64 v[190:191], s[62:63], 0, v[170:171]
	s_add_u32 s62, s3, s61
	s_addc_u32 s63, s30, 0
	global_load_lds_dwordx4 v[190:191], off
	v_lshl_add_u64 v[190:191], s[62:63], 0, v[164:165]
	s_mov_b32 m0, s23
	s_nop 0
	global_load_lds_dwordx4 v[190:191], off
	v_lshl_add_u64 v[190:191], s[62:63], 0, v[166:167]
	s_mov_b32 m0, s24
	s_nop 0
	global_load_lds_dwordx4 v[190:191], off
	ds_read_b128 v[160:163], v199 offset:16384
	ds_read_b128 v[174:177], v199 offset:17408
	ds_read_b128 v[178:181], v199 offset:18432
	ds_read_b128 v[182:185], v199 offset:19456
	ds_read_b128 v[186:189], v199 offset:20480
	ds_read_b128 v[200:203], v199 offset:21504
	ds_read_b128 v[204:207], v199 offset:22528
	ds_read_b128 v[208:211], v199 offset:23552
	s_waitcnt vmcnt(8)
	s_waitcnt lgkmcnt(0)
	s_barrier
	s_waitcnt lgkmcnt(0)
	v_mfma_f32_16x16x32_bf16 v[60:63], v[100:103], v[160:163], v[60:63]
	v_mfma_f32_16x16x32_bf16 v[52:55], v[136:139], v[160:163], v[52:55]
	v_mfma_f32_16x16x32_bf16 v[44:47], v[100:103], v[178:181], v[44:47]
	v_mfma_f32_16x16x32_bf16 v[36:39], v[136:139], v[178:181], v[36:39]
	v_mfma_f32_16x16x32_bf16 v[28:31], v[100:103], v[186:189], v[28:31]
	v_mfma_f32_16x16x32_bf16 v[20:23], v[136:139], v[186:189], v[20:23]
	v_mfma_f32_16x16x32_bf16 v[12:15], v[100:103], v[204:207], v[12:15]
	v_mfma_f32_16x16x32_bf16 v[4:7], v[136:139], v[204:207], v[4:7]
	v_mfma_f32_16x16x32_bf16 v[60:63], v[132:135], v[174:177], v[60:63]
	v_mfma_f32_16x16x32_bf16 v[52:55], v[140:143], v[174:177], v[52:55]
	v_mfma_f32_16x16x32_bf16 v[44:47], v[132:135], v[182:185], v[44:47]
	v_mfma_f32_16x16x32_bf16 v[36:39], v[140:143], v[182:185], v[36:39]
	v_mfma_f32_16x16x32_bf16 v[28:31], v[132:135], v[200:203], v[28:31]
	v_mfma_f32_16x16x32_bf16 v[20:23], v[140:143], v[200:203], v[20:23]
	v_mfma_f32_16x16x32_bf16 v[12:15], v[132:135], v[208:211], v[12:15]
	v_mfma_f32_16x16x32_bf16 v[4:7], v[140:143], v[208:211], v[4:7]
	v_mfma_f32_16x16x32_bf16 v[56:59], v[144:147], v[160:163], v[56:59]
	v_mfma_f32_16x16x32_bf16 v[48:51], v[152:155], v[160:163], v[48:51]
	v_mfma_f32_16x16x32_bf16 v[40:43], v[144:147], v[178:181], v[40:43]
	v_mfma_f32_16x16x32_bf16 v[32:35], v[152:155], v[178:181], v[32:35]
	v_mfma_f32_16x16x32_bf16 v[24:27], v[144:147], v[186:189], v[24:27]
	v_mfma_f32_16x16x32_bf16 v[16:19], v[152:155], v[186:189], v[16:19]
	v_mfma_f32_16x16x32_bf16 v[8:11], v[144:147], v[204:207], v[8:11]
	v_mfma_f32_16x16x32_bf16 v[0:3], v[152:155], v[204:207], v[0:3]
	v_mfma_f32_16x16x32_bf16 v[56:59], v[148:151], v[174:177], v[56:59]
	v_mfma_f32_16x16x32_bf16 v[48:51], v[156:159], v[174:177], v[48:51]
	v_mfma_f32_16x16x32_bf16 v[40:43], v[148:151], v[182:185], v[40:43]
	v_mfma_f32_16x16x32_bf16 v[32:35], v[156:159], v[182:185], v[32:35]
	v_mfma_f32_16x16x32_bf16 v[24:27], v[148:151], v[200:203], v[24:27]
	v_mfma_f32_16x16x32_bf16 v[16:19], v[156:159], v[200:203], v[16:19]
	v_mfma_f32_16x16x32_bf16 v[8:11], v[148:151], v[208:211], v[8:11]
	v_mfma_f32_16x16x32_bf16 v[0:3], v[156:159], v[208:211], v[0:3]
	s_barrier
	s_add_i32 s67, 0, 0x18000
	s_add_i32 s68, 0, 0x1c000
	s_add_i32 s61, s61, 0x80000
	s_add_u32 s62, s3, s61
	s_addc_u32 s63, s30, 0
	s_mov_b32 m0, s25
	v_lshl_add_u64 v[190:191], s[62:63], 0, v[164:165]
	global_load_lds_dwordx4 v[190:191], off
	v_lshl_add_u64 v[190:191], s[62:63], 0, v[166:167]
	s_mov_b32 m0, s26
	s_nop 0
	global_load_lds_dwordx4 v[190:191], off
	v_add_u32_e32 v140, s67, v195
	v_add_u32_e32 v156, s68, v195
	ds_read_b128 v[100:103], v140
	ds_read_b128 v[132:135], v140 offset:1024
	ds_read_b128 v[136:139], v140 offset:2048
	ds_read_b128 v[140:143], v140 offset:3072
	ds_read_b128 v[144:147], v156
	ds_read_b128 v[148:151], v156 offset:1024
	ds_read_b128 v[152:155], v156 offset:2048
	ds_read_b128 v[156:159], v156 offset:3072
	ds_read_b128 v[160:163], v199 offset:32768
	ds_read_b128 v[174:177], v199 offset:33792
	ds_read_b128 v[178:181], v199 offset:34816
	ds_read_b128 v[182:185], v199 offset:35840
	ds_read_b128 v[186:189], v199 offset:36864
	ds_read_b128 v[200:203], v199 offset:37888
	ds_read_b128 v[204:207], v199 offset:38912
	ds_read_b128 v[208:211], v199 offset:39936
	s_waitcnt vmcnt(8)
	s_waitcnt lgkmcnt(0)
	s_barrier
	s_waitcnt lgkmcnt(0)
	v_mfma_f32_16x16x32_bf16 v[128:131], v[100:103], v[160:163], v[128:131]
	v_mfma_f32_16x16x32_bf16 v[124:127], v[136:139], v[160:163], v[124:127]
	v_mfma_f32_16x16x32_bf16 v[116:119], v[100:103], v[178:181], v[116:119]
	v_mfma_f32_16x16x32_bf16 v[108:111], v[136:139], v[178:181], v[108:111]
	v_mfma_f32_16x16x32_bf16 v[92:95], v[100:103], v[186:189], v[92:95]
	v_mfma_f32_16x16x32_bf16 v[84:87], v[136:139], v[186:189], v[84:87]
	v_mfma_f32_16x16x32_bf16 v[76:79], v[100:103], v[204:207], v[76:79]
	v_mfma_f32_16x16x32_bf16 v[68:71], v[136:139], v[204:207], v[68:71]
	v_mfma_f32_16x16x32_bf16 v[128:131], v[132:135], v[174:177], v[128:131]
	v_mfma_f32_16x16x32_bf16 v[124:127], v[140:143], v[174:177], v[124:127]
	v_mfma_f32_16x16x32_bf16 v[116:119], v[132:135], v[182:185], v[116:119]
	v_mfma_f32_16x16x32_bf16 v[108:111], v[140:143], v[182:185], v[108:111]
	v_mfma_f32_16x16x32_bf16 v[92:95], v[132:135], v[200:203], v[92:95]
	v_mfma_f32_16x16x32_bf16 v[84:87], v[140:143], v[200:203], v[84:87]
	v_mfma_f32_16x16x32_bf16 v[76:79], v[132:135], v[208:211], v[76:79]
	v_mfma_f32_16x16x32_bf16 v[68:71], v[140:143], v[208:211], v[68:71]
	v_mfma_f32_16x16x32_bf16 v[96:99], v[144:147], v[160:163], v[96:99]
	v_mfma_f32_16x16x32_bf16 v[120:123], v[152:155], v[160:163], v[120:123]
	v_mfma_f32_16x16x32_bf16 v[112:115], v[144:147], v[178:181], v[112:115]
	v_mfma_f32_16x16x32_bf16 v[104:107], v[152:155], v[178:181], v[104:107]
	v_mfma_f32_16x16x32_bf16 v[88:91], v[144:147], v[186:189], v[88:91]
	v_mfma_f32_16x16x32_bf16 v[80:83], v[152:155], v[186:189], v[80:83]
	v_mfma_f32_16x16x32_bf16 v[72:75], v[144:147], v[204:207], v[72:75]
	v_mfma_f32_16x16x32_bf16 v[64:67], v[152:155], v[204:207], v[64:67]
	v_mfma_f32_16x16x32_bf16 v[96:99], v[148:151], v[174:177], v[96:99]
	v_mfma_f32_16x16x32_bf16 v[120:123], v[156:159], v[174:177], v[120:123]
	v_mfma_f32_16x16x32_bf16 v[112:115], v[148:151], v[182:185], v[112:115]
	v_mfma_f32_16x16x32_bf16 v[104:107], v[156:159], v[182:185], v[104:107]
	v_mfma_f32_16x16x32_bf16 v[88:91], v[148:151], v[200:203], v[88:91]
	v_mfma_f32_16x16x32_bf16 v[80:83], v[156:159], v[200:203], v[80:83]
	v_mfma_f32_16x16x32_bf16 v[72:75], v[148:151], v[208:211], v[72:75]
	v_mfma_f32_16x16x32_bf16 v[64:67], v[156:159], v[208:211], v[64:67]
	s_barrier
; template <class Epi, class Sched, class Hook = NoHook>
; __device__ __forceinline__ void gemm_phase_w(LAS unsigned char* lds, const Sched& S, const Epi& E, int wave_id, const Hook& HK = Hook()) {
;     ...
;         if constexpr (!SEG2) {
;             for (int tt = 0; tt < nt; tt += 2) {
;                 if constexpr (GATHER) { if (tt == nt - 2) {
;                     if (has_next) { gnxt_00 = S.grow_l(nxt, lds, nbuf, R0) + (unsigned)(C0 * 2); gnxt_01 = S.grow_l(nxt, lds, nbuf, R1) + (unsigned)(C1 * 2); gnxt_10 = S.grow_l(nxt, lds, nbuf, 128 + R0) + (unsigned)(C0 * 2); gnxt_11 = S.grow_l(nxt, lds, nbuf, 128 + R1) + (unsigned)(C1 * 2); }
;                     else { gnxt_00 = gcur_00; gnxt_01 = gcur_01; gnxt_10 = gcur_10; gnxt_11 = gcur_11; } } }
;                 PG_TRIP(tt, false, false, false);
;             }
	s_or_b32 s62, s60, 1
	s_lshl_b32 s63, s62, 7
	s_add_i32 s59, s63, s59
	s_ashr_i32 s61, s59, 31
	s_add_u32 s60, s4, s59
	s_addc_u32 s61, s5, s61
	s_add_i32 s59, s67, s31
	v_lshl_add_u64 v[190:191], s[60:61], 0, v[168:169]
	s_mov_b32 m0, s59
	s_add_i32 s63, s63, s66
	global_load_lds_dwordx4 v[190:191], off
	s_add_i32 m0, s59, 0x2000
	s_ashr_i32 s59, s63, 31
	v_lshl_add_u64 v[190:191], s[60:61], 0, v[170:171]
	s_add_u32 s60, s4, s63
	s_addc_u32 s61, s5, s59
	s_add_i32 s59, s68, s31
	global_load_lds_dwordx4 v[190:191], off
	v_lshl_add_u64 v[190:191], s[60:61], 0, v[168:169]
	s_mov_b32 m0, s59
	s_nop 0
	global_load_lds_dwordx4 v[190:191], off
	s_add_i32 m0, s59, 0x2000
	s_lshl_b32 s59, s62, 12
	s_add_i32 s59, s59, s58
	s_add_u32 s58, s3, s59
	v_lshl_add_u64 v[190:191], s[60:61], 0, v[170:171]
	s_addc_u32 s59, s30, 0
	global_load_lds_dwordx4 v[190:191], off
	v_lshl_add_u64 v[190:191], s[58:59], 0, v[164:165]
	s_mov_b32 m0, s28
	s_nop 0
	global_load_lds_dwordx4 v[190:191], off
	v_lshl_add_u64 v[190:191], s[58:59], 0, v[166:167]
	s_mov_b32 m0, s29
	s_nop 0
	global_load_lds_dwordx4 v[190:191], off
	ds_read_b128 v[160:163], v199 offset:49152
	ds_read_b128 v[174:177], v199 offset:50176
	ds_read_b128 v[178:181], v199 offset:51200
	ds_read_b128 v[182:185], v199 offset:52224
	ds_read_b128 v[186:189], v199 offset:53248
	ds_read_b128 v[200:203], v199 offset:54272
	ds_read_b128 v[204:207], v199 offset:55296
	ds_read_b128 v[208:211], v199 offset:56320
	s_waitcnt vmcnt(8)
	s_waitcnt lgkmcnt(0)
	s_barrier
	s_waitcnt lgkmcnt(0)
	v_mfma_f32_16x16x32_bf16 v[60:63], v[100:103], v[160:163], v[60:63]
	v_mfma_f32_16x16x32_bf16 v[52:55], v[136:139], v[160:163], v[52:55]
	v_mfma_f32_16x16x32_bf16 v[44:47], v[100:103], v[178:181], v[44:47]
	v_mfma_f32_16x16x32_bf16 v[36:39], v[136:139], v[178:181], v[36:39]
	v_mfma_f32_16x16x32_bf16 v[28:31], v[100:103], v[186:189], v[28:31]
	v_mfma_f32_16x16x32_bf16 v[20:23], v[136:139], v[186:189], v[20:23]
	v_mfma_f32_16x16x32_bf16 v[12:15], v[100:103], v[204:207], v[12:15]
	v_mfma_f32_16x16x32_bf16 v[4:7], v[136:139], v[204:207], v[4:7]
	v_mfma_f32_16x16x32_bf16 v[60:63], v[132:135], v[174:177], v[60:63]
	v_mfma_f32_16x16x32_bf16 v[52:55], v[140:143], v[174:177], v[52:55]
	v_mfma_f32_16x16x32_bf16 v[44:47], v[132:135], v[182:185], v[44:47]
	v_mfma_f32_16x16x32_bf16 v[36:39], v[140:143], v[182:185], v[36:39]
	v_mfma_f32_16x16x32_bf16 v[28:31], v[132:135], v[200:203], v[28:31]
	v_mfma_f32_16x16x32_bf16 v[20:23], v[140:143], v[200:203], v[20:23]
	v_mfma_f32_16x16x32_bf16 v[12:15], v[132:135], v[208:211], v[12:15]
	v_mfma_f32_16x16x32_bf16 v[4:7], v[140:143], v[208:211], v[4:7]
	v_mfma_f32_16x16x32_bf16 v[56:59], v[144:147], v[160:163], v[56:59]
	v_mfma_f32_16x16x32_bf16 v[48:51], v[152:155], v[160:163], v[48:51]
	v_mfma_f32_16x16x32_bf16 v[40:43], v[144:147], v[178:181], v[40:43]
	v_mfma_f32_16x16x32_bf16 v[32:35], v[152:155], v[178:181], v[32:35]
	v_mfma_f32_16x16x32_bf16 v[24:27], v[144:147], v[186:189], v[24:27]
	v_mfma_f32_16x16x32_bf16 v[16:19], v[152:155], v[186:189], v[16:19]
	v_mfma_f32_16x16x32_bf16 v[8:11], v[144:147], v[204:207], v[8:11]
	v_mfma_f32_16x16x32_bf16 v[0:3], v[152:155], v[204:207], v[0:3]
	v_mfma_f32_16x16x32_bf16 v[56:59], v[148:151], v[174:177], v[56:59]
	v_mfma_f32_16x16x32_bf16 v[48:51], v[156:159], v[174:177], v[48:51]
	v_mfma_f32_16x16x32_bf16 v[40:43], v[148:151], v[182:185], v[40:43]
	v_mfma_f32_16x16x32_bf16 v[32:35], v[156:159], v[182:185], v[32:35]
	v_mfma_f32_16x16x32_bf16 v[24:27], v[148:151], v[200:203], v[24:27]
	v_mfma_f32_16x16x32_bf16 v[16:19], v[156:159], v[200:203], v[16:19]
	v_mfma_f32_16x16x32_bf16 v[8:11], v[148:151], v[208:211], v[8:11]
	v_mfma_f32_16x16x32_bf16 v[0:3], v[156:159], v[208:211], v[0:3]
	s_barrier
	s_addk_i32 s20, 0x2000
	s_cmp_gt_u32 s21, 29
	s_mov_b32 s21, s53
	s_cbranch_scc0 .LBB0_1854
	s_and_b64 vcc, exec, s[16:17]
	s_cbranch_vccz .LBB0_1857
	s_barrier

.LBB0_1983:
	s_add_i32 s45, s21, 2
	s_cmp_eq_u32 s20, 0x9f000
	s_cselect_b32 s49, s40, s43
	s_cselect_b32 s50, 0, s45
	s_cselect_b32 s48, s41, s44
	s_add_i32 s51, s44, s20
	s_add_u32 s52, s3, s51
	s_addc_u32 s53, s30, 0
	v_lshl_add_u64 v[190:191], s[52:53], 0, v[164:165]
	s_add_i32 m0, s24, 0xc000
	s_nop 0
	global_load_lds_dwordx4 v[190:191], off
	v_lshl_add_u64 v[190:191], s[52:53], 0, v[166:167]
	s_add_i32 m0, s24, 0xe000
	s_nop 0
	global_load_lds_dwordx4 v[190:191], off
	ds_read_b128 v[100:103], v195
	ds_read_b128 v[132:135], v195 offset:1024
	ds_read_b128 v[136:139], v195 offset:2048
	ds_read_b128 v[140:143], v195 offset:3072
	ds_read_b128 v[144:147], v196
	ds_read_b128 v[148:151], v196 offset:1024
	ds_read_b128 v[152:155], v196 offset:2048
	ds_read_b128 v[156:159], v196 offset:3072
	ds_read_b128 v[160:163], v197
	ds_read_b128 v[174:177], v197 offset:1024
	ds_read_b128 v[178:181], v197 offset:2048
	ds_read_b128 v[182:185], v197 offset:3072
	ds_read_b128 v[186:189], v197 offset:4096
	ds_read_b128 v[198:201], v197 offset:5120
	ds_read_b128 v[202:205], v197 offset:6144
	ds_read_b128 v[206:209], v197 offset:7168
	s_waitcnt vmcnt(8)
	s_waitcnt lgkmcnt(0)
	s_barrier
	s_waitcnt lgkmcnt(0)
	v_mfma_f32_16x16x32_bf16 v[128:131], v[100:103], v[160:163], v[128:131]
	v_mfma_f32_16x16x32_bf16 v[124:127], v[136:139], v[160:163], v[124:127]
	v_mfma_f32_16x16x32_bf16 v[116:119], v[100:103], v[178:181], v[116:119]
	v_mfma_f32_16x16x32_bf16 v[108:111], v[136:139], v[178:181], v[108:111]
	v_mfma_f32_16x16x32_bf16 v[92:95], v[100:103], v[186:189], v[92:95]
	v_mfma_f32_16x16x32_bf16 v[84:87], v[136:139], v[186:189], v[84:87]
	v_mfma_f32_16x16x32_bf16 v[76:79], v[100:103], v[202:205], v[76:79]
	v_mfma_f32_16x16x32_bf16 v[68:71], v[136:139], v[202:205], v[68:71]
	v_mfma_f32_16x16x32_bf16 v[128:131], v[132:135], v[174:177], v[128:131]
	v_mfma_f32_16x16x32_bf16 v[124:127], v[140:143], v[174:177], v[124:127]
	v_mfma_f32_16x16x32_bf16 v[116:119], v[132:135], v[182:185], v[116:119]
	v_mfma_f32_16x16x32_bf16 v[108:111], v[140:143], v[182:185], v[108:111]
	v_mfma_f32_16x16x32_bf16 v[92:95], v[132:135], v[198:201], v[92:95]
	v_mfma_f32_16x16x32_bf16 v[84:87], v[140:143], v[198:201], v[84:87]
	v_mfma_f32_16x16x32_bf16 v[76:79], v[132:135], v[206:209], v[76:79]
	v_mfma_f32_16x16x32_bf16 v[68:71], v[140:143], v[206:209], v[68:71]
	v_mfma_f32_16x16x32_bf16 v[96:99], v[144:147], v[160:163], v[96:99]
	v_mfma_f32_16x16x32_bf16 v[120:123], v[152:155], v[160:163], v[120:123]
	v_mfma_f32_16x16x32_bf16 v[112:115], v[144:147], v[178:181], v[112:115]
	v_mfma_f32_16x16x32_bf16 v[104:107], v[152:155], v[178:181], v[104:107]
	v_mfma_f32_16x16x32_bf16 v[88:91], v[144:147], v[186:189], v[88:91]
	v_mfma_f32_16x16x32_bf16 v[80:83], v[152:155], v[186:189], v[80:83]
	v_mfma_f32_16x16x32_bf16 v[72:75], v[144:147], v[202:205], v[72:75]
	v_mfma_f32_16x16x32_bf16 v[64:67], v[152:155], v[202:205], v[64:67]
	v_mfma_f32_16x16x32_bf16 v[96:99], v[148:151], v[174:177], v[96:99]
	v_mfma_f32_16x16x32_bf16 v[120:123], v[156:159], v[174:177], v[120:123]
	v_mfma_f32_16x16x32_bf16 v[112:115], v[148:151], v[182:185], v[112:115]
	v_mfma_f32_16x16x32_bf16 v[104:107], v[156:159], v[182:185], v[104:107]
	v_mfma_f32_16x16x32_bf16 v[88:91], v[148:151], v[198:201], v[88:91]
	v_mfma_f32_16x16x32_bf16 v[80:83], v[156:159], v[198:201], v[80:83]
	v_mfma_f32_16x16x32_bf16 v[72:75], v[148:151], v[206:209], v[72:75]
	v_mfma_f32_16x16x32_bf16 v[64:67], v[156:159], v[206:209], v[64:67]
	s_barrier
	s_lshl_b32 s51, s50, 7
	s_add_i32 s52, s51, s49
	s_ashr_i32 s53, s52, 31
	s_add_u32 s52, s4, s52
	s_addc_u32 s53, s5, s53
	s_add_i32 s58, s34, s31
	v_lshl_add_u64 v[190:191], s[52:53], 0, v[168:169]
	s_mov_b32 m0, s58
	s_nop 0
	global_load_lds_dwordx4 v[190:191], off
	s_add_i32 m0, s58, 0x2000
	s_add_i32 s58, s49, 0x80000
	s_add_i32 s51, s58, s51
	v_lshl_add_u64 v[190:191], s[52:53], 0, v[170:171]
	s_ashr_i32 s53, s51, 31
	s_add_u32 s52, s4, s51
	s_addc_u32 s53, s5, s53
	s_add_i32 s51, s36, s31
	global_load_lds_dwordx4 v[190:191], off
	v_lshl_add_u64 v[190:191], s[52:53], 0, v[168:169]
	s_mov_b32 m0, s51
	s_nop 0
	global_load_lds_dwordx4 v[190:191], off
	s_add_i32 m0, s51, 0x2000
	s_lshl_b32 s51, s50, 12
	s_add_i32 s51, s51, s48
	v_lshl_add_u64 v[190:191], s[52:53], 0, v[170:171]
	s_add_u32 s52, s3, s51
	s_addc_u32 s53, s30, 0
	global_load_lds_dwordx4 v[190:191], off
	v_lshl_add_u64 v[190:191], s[52:53], 0, v[164:165]
	s_mov_b32 m0, s24
	s_nop 0
	global_load_lds_dwordx4 v[190:191], off
	v_lshl_add_u64 v[190:191], s[52:53], 0, v[166:167]
	s_mov_b32 m0, s25
	s_nop 0
	global_load_lds_dwordx4 v[190:191], off
	ds_read_b128 v[160:163], v197 offset:16384
	ds_read_b128 v[174:177], v197 offset:17408
	ds_read_b128 v[178:181], v197 offset:18432
	ds_read_b128 v[182:185], v197 offset:19456
	ds_read_b128 v[186:189], v197 offset:20480
	ds_read_b128 v[198:201], v197 offset:21504
	ds_read_b128 v[202:205], v197 offset:22528
	ds_read_b128 v[206:209], v197 offset:23552
	s_waitcnt vmcnt(8)
	s_waitcnt lgkmcnt(0)
	s_barrier
	s_waitcnt lgkmcnt(0)
	v_mfma_f32_16x16x32_bf16 v[60:63], v[100:103], v[160:163], v[60:63]
	v_mfma_f32_16x16x32_bf16 v[52:55], v[136:139], v[160:163], v[52:55]
	v_mfma_f32_16x16x32_bf16 v[44:47], v[100:103], v[178:181], v[44:47]
	v_mfma_f32_16x16x32_bf16 v[36:39], v[136:139], v[178:181], v[36:39]
	v_mfma_f32_16x16x32_bf16 v[28:31], v[100:103], v[186:189], v[28:31]
	v_mfma_f32_16x16x32_bf16 v[20:23], v[136:139], v[186:189], v[20:23]
	v_mfma_f32_16x16x32_bf16 v[12:15], v[100:103], v[202:205], v[12:15]
	v_mfma_f32_16x16x32_bf16 v[4:7], v[136:139], v[202:205], v[4:7]
	v_mfma_f32_16x16x32_bf16 v[60:63], v[132:135], v[174:177], v[60:63]
	v_mfma_f32_16x16x32_bf16 v[52:55], v[140:143], v[174:177], v[52:55]
	v_mfma_f32_16x16x32_bf16 v[44:47], v[132:135], v[182:185], v[44:47]
	v_mfma_f32_16x16x32_bf16 v[36:39], v[140:143], v[182:185], v[36:39]
	v_mfma_f32_16x16x32_bf16 v[28:31], v[132:135], v[198:201], v[28:31]
	v_mfma_f32_16x16x32_bf16 v[20:23], v[140:143], v[198:201], v[20:23]
	v_mfma_f32_16x16x32_bf16 v[12:15], v[132:135], v[206:209], v[12:15]
	v_mfma_f32_16x16x32_bf16 v[4:7], v[140:143], v[206:209], v[4:7]
	v_mfma_f32_16x16x32_bf16 v[56:59], v[144:147], v[160:163], v[56:59]
	v_mfma_f32_16x16x32_bf16 v[48:51], v[152:155], v[160:163], v[48:51]
	v_mfma_f32_16x16x32_bf16 v[40:43], v[144:147], v[178:181], v[40:43]
	v_mfma_f32_16x16x32_bf16 v[32:35], v[152:155], v[178:181], v[32:35]
	v_mfma_f32_16x16x32_bf16 v[24:27], v[144:147], v[186:189], v[24:27]
	v_mfma_f32_16x16x32_bf16 v[16:19], v[152:155], v[186:189], v[16:19]
	v_mfma_f32_16x16x32_bf16 v[8:11], v[144:147], v[202:205], v[8:11]
	v_mfma_f32_16x16x32_bf16 v[0:3], v[152:155], v[202:205], v[0:3]
	v_mfma_f32_16x16x32_bf16 v[56:59], v[148:151], v[174:177], v[56:59]
	v_mfma_f32_16x16x32_bf16 v[48:51], v[156:159], v[174:177], v[48:51]
	v_mfma_f32_16x16x32_bf16 v[40:43], v[148:151], v[182:185], v[40:43]
	v_mfma_f32_16x16x32_bf16 v[32:35], v[156:159], v[182:185], v[32:35]
	v_mfma_f32_16x16x32_bf16 v[24:27], v[148:151], v[198:201], v[24:27]
	v_mfma_f32_16x16x32_bf16 v[16:19], v[156:159], v[198:201], v[16:19]
	v_mfma_f32_16x16x32_bf16 v[8:11], v[148:151], v[206:209], v[8:11]
	v_mfma_f32_16x16x32_bf16 v[0:3], v[156:159], v[206:209], v[0:3]
	s_barrier
	s_add_i32 s59, 0, 0x18000
	s_add_i32 s60, 0, 0x1c000
	s_add_i32 s51, s51, 0x80000
	s_add_u32 s52, s3, s51
	s_addc_u32 s53, s30, 0
	s_mov_b32 m0, s26
	v_lshl_add_u64 v[190:191], s[52:53], 0, v[164:165]
	global_load_lds_dwordx4 v[190:191], off
	v_lshl_add_u64 v[190:191], s[52:53], 0, v[166:167]
	s_mov_b32 m0, s27
	s_nop 0
	global_load_lds_dwordx4 v[190:191], off
	v_add_u32_e32 v140, s59, v193
	v_add_u32_e32 v156, s60, v193
	ds_read_b128 v[100:103], v140
	ds_read_b128 v[132:135], v140 offset:1024
	ds_read_b128 v[136:139], v140 offset:2048
	ds_read_b128 v[140:143], v140 offset:3072
	ds_read_b128 v[144:147], v156
	ds_read_b128 v[148:151], v156 offset:1024
	ds_read_b128 v[152:155], v156 offset:2048
	ds_read_b128 v[156:159], v156 offset:3072
	ds_read_b128 v[160:163], v197 offset:32768
	ds_read_b128 v[174:177], v197 offset:33792
	ds_read_b128 v[178:181], v197 offset:34816
	ds_read_b128 v[182:185], v197 offset:35840
	ds_read_b128 v[186:189], v197 offset:36864
	ds_read_b128 v[198:201], v197 offset:37888
	ds_read_b128 v[202:205], v197 offset:38912
	ds_read_b128 v[206:209], v197 offset:39936
	s_waitcnt vmcnt(8)
	s_waitcnt lgkmcnt(0)
	s_barrier
	s_waitcnt lgkmcnt(0)
	v_mfma_f32_16x16x32_bf16 v[128:131], v[100:103], v[160:163], v[128:131]
	v_mfma_f32_16x16x32_bf16 v[124:127], v[136:139], v[160:163], v[124:127]
	v_mfma_f32_16x16x32_bf16 v[116:119], v[100:103], v[178:181], v[116:119]
	v_mfma_f32_16x16x32_bf16 v[108:111], v[136:139], v[178:181], v[108:111]
	v_mfma_f32_16x16x32_bf16 v[92:95], v[100:103], v[186:189], v[92:95]
	v_mfma_f32_16x16x32_bf16 v[84:87], v[136:139], v[186:189], v[84:87]
	v_mfma_f32_16x16x32_bf16 v[76:79], v[100:103], v[202:205], v[76:79]
	v_mfma_f32_16x16x32_bf16 v[68:71], v[136:139], v[202:205], v[68:71]
	v_mfma_f32_16x16x32_bf16 v[128:131], v[132:135], v[174:177], v[128:131]
	v_mfma_f32_16x16x32_bf16 v[124:127], v[140:143], v[174:177], v[124:127]
	v_mfma_f32_16x16x32_bf16 v[116:119], v[132:135], v[182:185], v[116:119]
	v_mfma_f32_16x16x32_bf16 v[108:111], v[140:143], v[182:185], v[108:111]
	v_mfma_f32_16x16x32_bf16 v[92:95], v[132:135], v[198:201], v[92:95]
	v_mfma_f32_16x16x32_bf16 v[84:87], v[140:143], v[198:201], v[84:87]
	v_mfma_f32_16x16x32_bf16 v[76:79], v[132:135], v[206:209], v[76:79]
	v_mfma_f32_16x16x32_bf16 v[68:71], v[140:143], v[206:209], v[68:71]
	v_mfma_f32_16x16x32_bf16 v[96:99], v[144:147], v[160:163], v[96:99]
	v_mfma_f32_16x16x32_bf16 v[120:123], v[152:155], v[160:163], v[120:123]
	v_mfma_f32_16x16x32_bf16 v[112:115], v[144:147], v[178:181], v[112:115]
	v_mfma_f32_16x16x32_bf16 v[104:107], v[152:155], v[178:181], v[104:107]
	v_mfma_f32_16x16x32_bf16 v[88:91], v[144:147], v[186:189], v[88:91]
	v_mfma_f32_16x16x32_bf16 v[80:83], v[152:155], v[186:189], v[80:83]
	v_mfma_f32_16x16x32_bf16 v[72:75], v[144:147], v[202:205], v[72:75]
	v_mfma_f32_16x16x32_bf16 v[64:67], v[152:155], v[202:205], v[64:67]
	v_mfma_f32_16x16x32_bf16 v[96:99], v[148:151], v[174:177], v[96:99]
	v_mfma_f32_16x16x32_bf16 v[120:123], v[156:159], v[174:177], v[120:123]
	v_mfma_f32_16x16x32_bf16 v[112:115], v[148:151], v[182:185], v[112:115]
	v_mfma_f32_16x16x32_bf16 v[104:107], v[156:159], v[182:185], v[104:107]
	v_mfma_f32_16x16x32_bf16 v[88:91], v[148:151], v[198:201], v[88:91]
	v_mfma_f32_16x16x32_bf16 v[80:83], v[156:159], v[198:201], v[80:83]
	v_mfma_f32_16x16x32_bf16 v[72:75], v[148:151], v[206:209], v[72:75]
	v_mfma_f32_16x16x32_bf16 v[64:67], v[156:159], v[206:209], v[64:67]
	s_barrier
; template <class Epi, class Sched, class Hook = NoHook>
; __device__ __forceinline__ void gemm_phase_w(LAS unsigned char* lds, const Sched& S, const Epi& E, int wave_id, const Hook& HK = Hook()) {
;     ...
;         if constexpr (!SEG2) {
;             for (int tt = 0; tt < nt; tt += 2) {
;                 if constexpr (GATHER) { if (tt == nt - 2) {
;                     if (has_next) { gnxt_00 = S.grow_l(nxt, lds, nbuf, R0) + (unsigned)(C0 * 2); gnxt_01 = S.grow_l(nxt, lds, nbuf, R1) + (unsigned)(C1 * 2); gnxt_10 = S.grow_l(nxt, lds, nbuf, 128 + R0) + (unsigned)(C0 * 2); gnxt_11 = S.grow_l(nxt, lds, nbuf, 128 + R1) + (unsigned)(C1 * 2); }
;                     else { gnxt_00 = gcur_00; gnxt_01 = gcur_01; gnxt_10 = gcur_10; gnxt_11 = gcur_11; } } }
;                 PG_TRIP(tt, false, false, false);
;             }
	s_or_b32 s52, s50, 1
	s_lshl_b32 s53, s52, 7
	s_add_i32 s49, s53, s49
	s_ashr_i32 s51, s49, 31
	s_add_u32 s50, s4, s49
	s_addc_u32 s51, s5, s51
	s_add_i32 s49, s59, s31
	v_lshl_add_u64 v[190:191], s[50:51], 0, v[168:169]
	s_mov_b32 m0, s49
	s_add_i32 s53, s53, s58
	global_load_lds_dwordx4 v[190:191], off
	s_add_i32 m0, s49, 0x2000
	s_ashr_i32 s49, s53, 31
	v_lshl_add_u64 v[190:191], s[50:51], 0, v[170:171]
	s_add_u32 s50, s4, s53
	s_addc_u32 s51, s5, s49
	s_add_i32 s49, s60, s31
	global_load_lds_dwordx4 v[190:191], off
	v_lshl_add_u64 v[190:191], s[50:51], 0, v[168:169]
	s_mov_b32 m0, s49
	s_nop 0
	global_load_lds_dwordx4 v[190:191], off
	s_add_i32 m0, s49, 0x2000
	s_lshl_b32 s49, s52, 12
	s_add_i32 s49, s49, s48
	s_add_u32 s48, s3, s49
	v_lshl_add_u64 v[190:191], s[50:51], 0, v[170:171]
	s_addc_u32 s49, s30, 0
	global_load_lds_dwordx4 v[190:191], off
	v_lshl_add_u64 v[190:191], s[48:49], 0, v[164:165]
	s_mov_b32 m0, s29
	s_nop 0
	global_load_lds_dwordx4 v[190:191], off
	v_lshl_add_u64 v[190:191], s[48:49], 0, v[166:167]
	s_mov_b32 m0, s38
	s_nop 0
	global_load_lds_dwordx4 v[190:191], off
	ds_read_b128 v[160:163], v197 offset:49152
	ds_read_b128 v[174:177], v197 offset:50176
	ds_read_b128 v[178:181], v197 offset:51200
	ds_read_b128 v[182:185], v197 offset:52224
	ds_read_b128 v[186:189], v197 offset:53248
	ds_read_b128 v[198:201], v197 offset:54272
	ds_read_b128 v[202:205], v197 offset:55296
	ds_read_b128 v[206:209], v197 offset:56320
	s_waitcnt vmcnt(8)
	s_waitcnt lgkmcnt(0)
	s_barrier
	s_waitcnt lgkmcnt(0)
	v_mfma_f32_16x16x32_bf16 v[60:63], v[100:103], v[160:163], v[60:63]
	v_mfma_f32_16x16x32_bf16 v[52:55], v[136:139], v[160:163], v[52:55]
	v_mfma_f32_16x16x32_bf16 v[44:47], v[100:103], v[178:181], v[44:47]
	v_mfma_f32_16x16x32_bf16 v[36:39], v[136:139], v[178:181], v[36:39]
	v_mfma_f32_16x16x32_bf16 v[28:31], v[100:103], v[186:189], v[28:31]
	v_mfma_f32_16x16x32_bf16 v[20:23], v[136:139], v[186:189], v[20:23]
	v_mfma_f32_16x16x32_bf16 v[12:15], v[100:103], v[202:205], v[12:15]
	v_mfma_f32_16x16x32_bf16 v[4:7], v[136:139], v[202:205], v[4:7]
	v_mfma_f32_16x16x32_bf16 v[60:63], v[132:135], v[174:177], v[60:63]
	v_mfma_f32_16x16x32_bf16 v[52:55], v[140:143], v[174:177], v[52:55]
	v_mfma_f32_16x16x32_bf16 v[44:47], v[132:135], v[182:185], v[44:47]
	v_mfma_f32_16x16x32_bf16 v[36:39], v[140:143], v[182:185], v[36:39]
	v_mfma_f32_16x16x32_bf16 v[28:31], v[132:135], v[198:201], v[28:31]
	v_mfma_f32_16x16x32_bf16 v[20:23], v[140:143], v[198:201], v[20:23]
	v_mfma_f32_16x16x32_bf16 v[12:15], v[132:135], v[206:209], v[12:15]
	v_mfma_f32_16x16x32_bf16 v[4:7], v[140:143], v[206:209], v[4:7]
	v_mfma_f32_16x16x32_bf16 v[56:59], v[144:147], v[160:163], v[56:59]
	v_mfma_f32_16x16x32_bf16 v[48:51], v[152:155], v[160:163], v[48:51]
	v_mfma_f32_16x16x32_bf16 v[40:43], v[144:147], v[178:181], v[40:43]
	v_mfma_f32_16x16x32_bf16 v[32:35], v[152:155], v[178:181], v[32:35]
	v_mfma_f32_16x16x32_bf16 v[24:27], v[144:147], v[186:189], v[24:27]
	v_mfma_f32_16x16x32_bf16 v[16:19], v[152:155], v[186:189], v[16:19]
	v_mfma_f32_16x16x32_bf16 v[8:11], v[144:147], v[202:205], v[8:11]
	v_mfma_f32_16x16x32_bf16 v[0:3], v[152:155], v[202:205], v[0:3]
	v_mfma_f32_16x16x32_bf16 v[56:59], v[148:151], v[174:177], v[56:59]
	v_mfma_f32_16x16x32_bf16 v[48:51], v[156:159], v[174:177], v[48:51]
	v_mfma_f32_16x16x32_bf16 v[40:43], v[148:151], v[182:185], v[40:43]
	v_mfma_f32_16x16x32_bf16 v[32:35], v[156:159], v[182:185], v[32:35]
	v_mfma_f32_16x16x32_bf16 v[24:27], v[148:151], v[198:201], v[24:27]
	v_mfma_f32_16x16x32_bf16 v[16:19], v[156:159], v[198:201], v[16:19]
	v_mfma_f32_16x16x32_bf16 v[8:11], v[148:151], v[206:209], v[8:11]
	v_mfma_f32_16x16x32_bf16 v[0:3], v[156:159], v[206:209], v[0:3]
	s_barrier
	s_addk_i32 s20, 0x2000
	s_cmp_gt_u32 s21, 29
	s_mov_b32 s21, s45
	s_cbranch_scc0 .LBB0_1983
	s_and_b64 vcc, exec, s[16:17]
	s_cbranch_vccz .LBB0_1986
	s_barrier

.LBB0_2522:
	s_add_i32 s22, s53, s10
	s_add_u32 s58, s28, s22
	s_addc_u32 s59, s29, 0
	s_add_i32 m0, s31, 0xc000
	s_add_i32 s60, s31, 0xe000
	s_add_i32 s61, s10, 0xfffc0080
	s_cmp_eq_u32 s19, 12
	s_cselect_b32 s22, s50, s53
	s_cselect_b32 s23, s51, s56
	v_lshl_add_u64 v[220:221], s[58:59], 0, v[130:131]
	global_load_lds_dwordx4 v[220:221], off
	v_lshl_add_u64 v[220:221], s[58:59], 0, v[132:133]
	s_mov_b32 m0, s60
	s_nop 0
	global_load_lds_dwordx4 v[220:221], off
	ds_read_b128 v[156:159], v153
	ds_read_b128 v[160:163], v153 offset:1024
	ds_read_b128 v[164:167], v153 offset:2048
	ds_read_b128 v[168:171], v153 offset:3072
	ds_read_b128 v[172:175], v154
	ds_read_b128 v[176:179], v154 offset:1024
	ds_read_b128 v[180:183], v154 offset:2048
	ds_read_b128 v[184:187], v154 offset:3072
	ds_read_b128 v[188:191], v155
	ds_read_b128 v[192:195], v155 offset:1024
	ds_read_b128 v[196:199], v155 offset:2048
	ds_read_b128 v[200:203], v155 offset:3072
	ds_read_b128 v[204:207], v155 offset:4096
	ds_read_b128 v[208:211], v155 offset:5120
	ds_read_b128 v[212:215], v155 offset:6144
	ds_read_b128 v[216:219], v155 offset:7168
	s_waitcnt vmcnt(8)
	s_waitcnt lgkmcnt(0)
	s_barrier
	s_waitcnt lgkmcnt(0)
	v_mfma_f32_16x16x32_bf16 v[124:127], v[156:159], v[188:191], v[124:127]
	v_mfma_f32_16x16x32_bf16 v[120:123], v[164:167], v[188:191], v[120:123]
	v_mfma_f32_16x16x32_bf16 v[108:111], v[156:159], v[196:199], v[108:111]
	v_mfma_f32_16x16x32_bf16 v[104:107], v[164:167], v[196:199], v[104:107]
	v_mfma_f32_16x16x32_bf16 v[92:95], v[156:159], v[204:207], v[92:95]
	v_mfma_f32_16x16x32_bf16 v[88:91], v[164:167], v[204:207], v[88:91]
	v_mfma_f32_16x16x32_bf16 v[76:79], v[156:159], v[212:215], v[76:79]
	v_mfma_f32_16x16x32_bf16 v[72:75], v[164:167], v[212:215], v[72:75]
	v_mfma_f32_16x16x32_bf16 v[124:127], v[160:163], v[192:195], v[124:127]
	v_mfma_f32_16x16x32_bf16 v[120:123], v[168:171], v[192:195], v[120:123]
	v_mfma_f32_16x16x32_bf16 v[108:111], v[160:163], v[200:203], v[108:111]
	v_mfma_f32_16x16x32_bf16 v[104:107], v[168:171], v[200:203], v[104:107]
	v_mfma_f32_16x16x32_bf16 v[92:95], v[160:163], v[208:211], v[92:95]
	v_mfma_f32_16x16x32_bf16 v[88:91], v[168:171], v[208:211], v[88:91]
	v_mfma_f32_16x16x32_bf16 v[76:79], v[160:163], v[216:219], v[76:79]
	v_mfma_f32_16x16x32_bf16 v[72:75], v[168:171], v[216:219], v[72:75]
	v_mfma_f32_16x16x32_bf16 v[116:119], v[172:175], v[188:191], v[116:119]
	v_mfma_f32_16x16x32_bf16 v[112:115], v[180:183], v[188:191], v[112:115]
	v_mfma_f32_16x16x32_bf16 v[100:103], v[172:175], v[196:199], v[100:103]
	v_mfma_f32_16x16x32_bf16 v[96:99], v[180:183], v[196:199], v[96:99]
	v_mfma_f32_16x16x32_bf16 v[84:87], v[172:175], v[204:207], v[84:87]
	v_mfma_f32_16x16x32_bf16 v[80:83], v[180:183], v[204:207], v[80:83]
	v_mfma_f32_16x16x32_bf16 v[68:71], v[172:175], v[212:215], v[68:71]
	v_mfma_f32_16x16x32_bf16 v[64:67], v[180:183], v[212:215], v[64:67]
	v_mfma_f32_16x16x32_bf16 v[116:119], v[176:179], v[192:195], v[116:119]
	v_mfma_f32_16x16x32_bf16 v[112:115], v[184:187], v[192:195], v[112:115]
	v_mfma_f32_16x16x32_bf16 v[100:103], v[176:179], v[200:203], v[100:103]
	v_mfma_f32_16x16x32_bf16 v[96:99], v[184:187], v[200:203], v[96:99]
	v_mfma_f32_16x16x32_bf16 v[84:87], v[176:179], v[208:211], v[84:87]
	v_mfma_f32_16x16x32_bf16 v[80:83], v[184:187], v[208:211], v[80:83]
	v_mfma_f32_16x16x32_bf16 v[68:71], v[176:179], v[216:219], v[68:71]
	v_mfma_f32_16x16x32_bf16 v[64:67], v[184:187], v[216:219], v[64:67]
	s_barrier
	s_cselect_b32 s60, 0, s61
	s_add_i32 s58, s60, s23
	s_ashr_i32 s59, s58, 31
	s_add_u32 s58, s8, s58
	s_addc_u32 s59, s9, s59
	s_add_i32 s61, s42, s26
	v_lshl_add_u64 v[220:221], s[58:59], 0, v[130:131]
	s_mov_b32 m0, s61
	s_nop 0
	global_load_lds_dwordx4 v[220:221], off
	s_add_i32 m0, s61, 0x2000
	s_add_i32 s61, s23, 0x40000
	v_lshl_add_u64 v[220:221], s[58:59], 0, v[132:133]
	s_add_i32 s58, s61, s60
	s_ashr_i32 s59, s58, 31
	s_add_u32 s58, s8, s58
	s_addc_u32 s59, s9, s59
	s_add_i32 s62, s43, s26
	global_load_lds_dwordx4 v[220:221], off
	v_lshl_add_u64 v[220:221], s[58:59], 0, v[130:131]
	s_mov_b32 m0, s62
	s_nop 0
	global_load_lds_dwordx4 v[220:221], off
	s_add_i32 m0, s62, 0x2000
	s_add_i32 s62, s60, s22
	v_lshl_add_u64 v[220:221], s[58:59], 0, v[132:133]
	s_add_u32 s58, s28, s62
	s_addc_u32 s59, s29, 0
	global_load_lds_dwordx4 v[220:221], off
	v_lshl_add_u64 v[220:221], s[58:59], 0, v[130:131]
	s_mov_b32 m0, s31
	s_nop 0
	global_load_lds_dwordx4 v[220:221], off
	v_lshl_add_u64 v[220:221], s[58:59], 0, v[132:133]
	s_mov_b32 m0, s33
	s_nop 0
	global_load_lds_dwordx4 v[220:221], off
	ds_read_b128 v[188:191], v155 offset:16384
	ds_read_b128 v[192:195], v155 offset:17408
	ds_read_b128 v[196:199], v155 offset:18432
	ds_read_b128 v[200:203], v155 offset:19456
	ds_read_b128 v[204:207], v155 offset:20480
	ds_read_b128 v[208:211], v155 offset:21504
	ds_read_b128 v[212:215], v155 offset:22528
	ds_read_b128 v[216:219], v155 offset:23552
	s_waitcnt vmcnt(8)
	s_waitcnt lgkmcnt(0)
	s_barrier
	s_waitcnt lgkmcnt(0)
	v_mfma_f32_16x16x32_bf16 v[60:63], v[156:159], v[188:191], v[60:63]
	v_mfma_f32_16x16x32_bf16 v[56:59], v[164:167], v[188:191], v[56:59]
	v_mfma_f32_16x16x32_bf16 v[44:47], v[156:159], v[196:199], v[44:47]
	v_mfma_f32_16x16x32_bf16 v[40:43], v[164:167], v[196:199], v[40:43]
	v_mfma_f32_16x16x32_bf16 v[28:31], v[156:159], v[204:207], v[28:31]
	v_mfma_f32_16x16x32_bf16 v[24:27], v[164:167], v[204:207], v[24:27]
	v_mfma_f32_16x16x32_bf16 v[12:15], v[156:159], v[212:215], v[12:15]
	v_mfma_f32_16x16x32_bf16 v[8:11], v[164:167], v[212:215], v[8:11]
	v_mfma_f32_16x16x32_bf16 v[60:63], v[160:163], v[192:195], v[60:63]
	v_mfma_f32_16x16x32_bf16 v[56:59], v[168:171], v[192:195], v[56:59]
	v_mfma_f32_16x16x32_bf16 v[44:47], v[160:163], v[200:203], v[44:47]
	v_mfma_f32_16x16x32_bf16 v[40:43], v[168:171], v[200:203], v[40:43]
	v_mfma_f32_16x16x32_bf16 v[28:31], v[160:163], v[208:211], v[28:31]
	v_mfma_f32_16x16x32_bf16 v[24:27], v[168:171], v[208:211], v[24:27]
	v_mfma_f32_16x16x32_bf16 v[12:15], v[160:163], v[216:219], v[12:15]
	v_mfma_f32_16x16x32_bf16 v[8:11], v[168:171], v[216:219], v[8:11]
	v_mfma_f32_16x16x32_bf16 v[52:55], v[172:175], v[188:191], v[52:55]
	v_mfma_f32_16x16x32_bf16 v[48:51], v[180:183], v[188:191], v[48:51]
	v_mfma_f32_16x16x32_bf16 v[36:39], v[172:175], v[196:199], v[36:39]
	v_mfma_f32_16x16x32_bf16 v[32:35], v[180:183], v[196:199], v[32:35]
	v_mfma_f32_16x16x32_bf16 v[20:23], v[172:175], v[204:207], v[20:23]
	v_mfma_f32_16x16x32_bf16 v[16:19], v[180:183], v[204:207], v[16:19]
	v_mfma_f32_16x16x32_bf16 v[4:7], v[172:175], v[212:215], v[4:7]
	v_mfma_f32_16x16x32_bf16 v[0:3], v[180:183], v[212:215], v[0:3]
	v_mfma_f32_16x16x32_bf16 v[52:55], v[176:179], v[192:195], v[52:55]
	v_mfma_f32_16x16x32_bf16 v[48:51], v[184:187], v[192:195], v[48:51]
	v_mfma_f32_16x16x32_bf16 v[36:39], v[176:179], v[200:203], v[36:39]
	v_mfma_f32_16x16x32_bf16 v[32:35], v[184:187], v[200:203], v[32:35]
	v_mfma_f32_16x16x32_bf16 v[20:23], v[176:179], v[208:211], v[20:23]
	v_mfma_f32_16x16x32_bf16 v[16:19], v[184:187], v[208:211], v[16:19]
	v_mfma_f32_16x16x32_bf16 v[4:7], v[176:179], v[216:219], v[4:7]
	v_mfma_f32_16x16x32_bf16 v[0:3], v[184:187], v[216:219], v[0:3]
	s_barrier
	s_add_i32 s63, 0, 0x18000
	s_add_i32 s64, 0, 0x1c000
	s_add_i32 s62, s62, 0x40000
	s_add_u32 s58, s28, s62
	s_addc_u32 s59, s29, 0
	s_mov_b32 m0, s34
	v_lshl_add_u64 v[220:221], s[58:59], 0, v[130:131]
	global_load_lds_dwordx4 v[220:221], off
	v_lshl_add_u64 v[220:221], s[58:59], 0, v[132:133]
	s_mov_b32 m0, s35
	s_nop 0
	global_load_lds_dwordx4 v[220:221], off
	v_add_u32_e32 v168, s63, v137
	v_add_u32_e32 v184, s64, v137
	ds_read_b128 v[156:159], v168
	ds_read_b128 v[160:163], v168 offset:1024
	ds_read_b128 v[164:167], v168 offset:2048
	ds_read_b128 v[168:171], v168 offset:3072
	ds_read_b128 v[172:175], v184
	ds_read_b128 v[176:179], v184 offset:1024
	ds_read_b128 v[180:183], v184 offset:2048
	ds_read_b128 v[184:187], v184 offset:3072
	ds_read_b128 v[188:191], v155 offset:32768
	ds_read_b128 v[192:195], v155 offset:33792
	ds_read_b128 v[196:199], v155 offset:34816
	ds_read_b128 v[200:203], v155 offset:35840
	ds_read_b128 v[204:207], v155 offset:36864
	ds_read_b128 v[208:211], v155 offset:37888
	ds_read_b128 v[212:215], v155 offset:38912
	ds_read_b128 v[216:219], v155 offset:39936
	s_waitcnt vmcnt(8)
	s_waitcnt lgkmcnt(0)
	s_barrier
	s_waitcnt lgkmcnt(0)
	v_mfma_f32_16x16x32_bf16 v[124:127], v[156:159], v[188:191], v[124:127]
	v_mfma_f32_16x16x32_bf16 v[120:123], v[164:167], v[188:191], v[120:123]
	v_mfma_f32_16x16x32_bf16 v[108:111], v[156:159], v[196:199], v[108:111]
	v_mfma_f32_16x16x32_bf16 v[104:107], v[164:167], v[196:199], v[104:107]
	v_mfma_f32_16x16x32_bf16 v[92:95], v[156:159], v[204:207], v[92:95]
	v_mfma_f32_16x16x32_bf16 v[88:91], v[164:167], v[204:207], v[88:91]
	v_mfma_f32_16x16x32_bf16 v[76:79], v[156:159], v[212:215], v[76:79]
	v_mfma_f32_16x16x32_bf16 v[72:75], v[164:167], v[212:215], v[72:75]
	v_mfma_f32_16x16x32_bf16 v[124:127], v[160:163], v[192:195], v[124:127]
	v_mfma_f32_16x16x32_bf16 v[120:123], v[168:171], v[192:195], v[120:123]
	v_mfma_f32_16x16x32_bf16 v[108:111], v[160:163], v[200:203], v[108:111]
	v_mfma_f32_16x16x32_bf16 v[104:107], v[168:171], v[200:203], v[104:107]
	v_mfma_f32_16x16x32_bf16 v[92:95], v[160:163], v[208:211], v[92:95]
	v_mfma_f32_16x16x32_bf16 v[88:91], v[168:171], v[208:211], v[88:91]
	v_mfma_f32_16x16x32_bf16 v[76:79], v[160:163], v[216:219], v[76:79]
	v_mfma_f32_16x16x32_bf16 v[72:75], v[168:171], v[216:219], v[72:75]
	v_mfma_f32_16x16x32_bf16 v[116:119], v[172:175], v[188:191], v[116:119]
	v_mfma_f32_16x16x32_bf16 v[112:115], v[180:183], v[188:191], v[112:115]
	v_mfma_f32_16x16x32_bf16 v[100:103], v[172:175], v[196:199], v[100:103]
	v_mfma_f32_16x16x32_bf16 v[96:99], v[180:183], v[196:199], v[96:99]
	v_mfma_f32_16x16x32_bf16 v[84:87], v[172:175], v[204:207], v[84:87]
	v_mfma_f32_16x16x32_bf16 v[80:83], v[180:183], v[204:207], v[80:83]
	v_mfma_f32_16x16x32_bf16 v[68:71], v[172:175], v[212:215], v[68:71]
	v_mfma_f32_16x16x32_bf16 v[64:67], v[180:183], v[212:215], v[64:67]
	v_mfma_f32_16x16x32_bf16 v[116:119], v[176:179], v[192:195], v[116:119]
	v_mfma_f32_16x16x32_bf16 v[112:115], v[184:187], v[192:195], v[112:115]
	v_mfma_f32_16x16x32_bf16 v[100:103], v[176:179], v[200:203], v[100:103]
	v_mfma_f32_16x16x32_bf16 v[96:99], v[184:187], v[200:203], v[96:99]
	v_mfma_f32_16x16x32_bf16 v[84:87], v[176:179], v[208:211], v[84:87]
	v_mfma_f32_16x16x32_bf16 v[80:83], v[184:187], v[208:211], v[80:83]
	v_mfma_f32_16x16x32_bf16 v[68:71], v[176:179], v[216:219], v[68:71]
	v_mfma_f32_16x16x32_bf16 v[64:67], v[184:187], v[216:219], v[64:67]
	s_barrier
; template <class Epi, class Sched, class Hook = NoHook>
; __device__ __forceinline__ void gemm_phase_w(LAS unsigned char* lds, const Sched& S, const Epi& E, int wave_id, const Hook& HK = Hook()) {
;     ...
;         if constexpr (!SEG2) {
;             for (int tt = 0; tt < nt; tt += 2) {
;                 if constexpr (GATHER) { if (tt == nt - 2) {
;                     if (has_next) { gnxt_00 = S.grow_l(nxt, lds, nbuf, R0) + (unsigned)(C0 * 2); gnxt_01 = S.grow_l(nxt, lds, nbuf, R1) + (unsigned)(C1 * 2); gnxt_10 = S.grow_l(nxt, lds, nbuf, 128 + R0) + (unsigned)(C0 * 2); gnxt_11 = S.grow_l(nxt, lds, nbuf, 128 + R1) + (unsigned)(C1 * 2); }
;                     else { gnxt_00 = gcur_00; gnxt_01 = gcur_01; gnxt_10 = gcur_10; gnxt_11 = gcur_11; } } }
;                 PG_TRIP(tt, false, false, false);
;             }
	s_bitset1_b32 s60, 7
	s_add_i32 s23, s60, s23
	s_ashr_i32 s59, s23, 31
	s_add_u32 s58, s8, s23
	s_addc_u32 s59, s9, s59
	s_add_i32 s23, s63, s26
	v_lshl_add_u64 v[220:221], s[58:59], 0, v[130:131]
	s_mov_b32 m0, s23
	s_nop 0
	global_load_lds_dwordx4 v[220:221], off
	s_add_i32 m0, s23, 0x2000
	s_add_i32 s23, s60, s61
	v_lshl_add_u64 v[220:221], s[58:59], 0, v[132:133]
	s_ashr_i32 s59, s23, 31
	s_add_u32 s58, s8, s23
	s_addc_u32 s59, s9, s59
	s_add_i32 s23, s64, s26
	global_load_lds_dwordx4 v[220:221], off
	v_lshl_add_u64 v[220:221], s[58:59], 0, v[130:131]
	s_mov_b32 m0, s23
	s_add_i32 s60, s60, s22
	global_load_lds_dwordx4 v[220:221], off
	s_add_i32 m0, s23, 0x2000
	s_add_u32 s22, s28, s60
	v_lshl_add_u64 v[220:221], s[58:59], 0, v[132:133]
	s_addc_u32 s23, s29, 0
	global_load_lds_dwordx4 v[220:221], off
	v_lshl_add_u64 v[220:221], s[22:23], 0, v[130:131]
	s_mov_b32 m0, s37
	s_nop 0
	global_load_lds_dwordx4 v[220:221], off
	v_lshl_add_u64 v[220:221], s[22:23], 0, v[132:133]
	s_mov_b32 m0, s38
	s_nop 0
	global_load_lds_dwordx4 v[220:221], off
	ds_read_b128 v[188:191], v155 offset:49152
	ds_read_b128 v[192:195], v155 offset:50176
	ds_read_b128 v[196:199], v155 offset:51200
	ds_read_b128 v[200:203], v155 offset:52224
	ds_read_b128 v[204:207], v155 offset:53248
	ds_read_b128 v[208:211], v155 offset:54272
	ds_read_b128 v[212:215], v155 offset:55296
	ds_read_b128 v[216:219], v155 offset:56320
	s_waitcnt vmcnt(8)
	s_waitcnt lgkmcnt(0)
	s_barrier
	s_waitcnt lgkmcnt(0)
	v_mfma_f32_16x16x32_bf16 v[60:63], v[156:159], v[188:191], v[60:63]
	v_mfma_f32_16x16x32_bf16 v[56:59], v[164:167], v[188:191], v[56:59]
	v_mfma_f32_16x16x32_bf16 v[44:47], v[156:159], v[196:199], v[44:47]
	v_mfma_f32_16x16x32_bf16 v[40:43], v[164:167], v[196:199], v[40:43]
	v_mfma_f32_16x16x32_bf16 v[28:31], v[156:159], v[204:207], v[28:31]
	v_mfma_f32_16x16x32_bf16 v[24:27], v[164:167], v[204:207], v[24:27]
	v_mfma_f32_16x16x32_bf16 v[12:15], v[156:159], v[212:215], v[12:15]
	v_mfma_f32_16x16x32_bf16 v[8:11], v[164:167], v[212:215], v[8:11]
	v_mfma_f32_16x16x32_bf16 v[60:63], v[160:163], v[192:195], v[60:63]
	v_mfma_f32_16x16x32_bf16 v[56:59], v[168:171], v[192:195], v[56:59]
	v_mfma_f32_16x16x32_bf16 v[44:47], v[160:163], v[200:203], v[44:47]
	v_mfma_f32_16x16x32_bf16 v[40:43], v[168:171], v[200:203], v[40:43]
	v_mfma_f32_16x16x32_bf16 v[28:31], v[160:163], v[208:211], v[28:31]
	v_mfma_f32_16x16x32_bf16 v[24:27], v[168:171], v[208:211], v[24:27]
	v_mfma_f32_16x16x32_bf16 v[12:15], v[160:163], v[216:219], v[12:15]
	v_mfma_f32_16x16x32_bf16 v[8:11], v[168:171], v[216:219], v[8:11]
	v_mfma_f32_16x16x32_bf16 v[52:55], v[172:175], v[188:191], v[52:55]
	v_mfma_f32_16x16x32_bf16 v[48:51], v[180:183], v[188:191], v[48:51]
	v_mfma_f32_16x16x32_bf16 v[36:39], v[172:175], v[196:199], v[36:39]
	v_mfma_f32_16x16x32_bf16 v[32:35], v[180:183], v[196:199], v[32:35]
	v_mfma_f32_16x16x32_bf16 v[20:23], v[172:175], v[204:207], v[20:23]
	v_mfma_f32_16x16x32_bf16 v[16:19], v[180:183], v[204:207], v[16:19]
	v_mfma_f32_16x16x32_bf16 v[4:7], v[172:175], v[212:215], v[4:7]
	v_mfma_f32_16x16x32_bf16 v[0:3], v[180:183], v[212:215], v[0:3]
	v_mfma_f32_16x16x32_bf16 v[52:55], v[176:179], v[192:195], v[52:55]
	v_mfma_f32_16x16x32_bf16 v[48:51], v[184:187], v[192:195], v[48:51]
	v_mfma_f32_16x16x32_bf16 v[36:39], v[176:179], v[200:203], v[36:39]
	v_mfma_f32_16x16x32_bf16 v[32:35], v[184:187], v[200:203], v[32:35]
	v_mfma_f32_16x16x32_bf16 v[20:23], v[176:179], v[208:211], v[20:23]
	v_mfma_f32_16x16x32_bf16 v[16:19], v[184:187], v[208:211], v[16:19]
	v_mfma_f32_16x16x32_bf16 v[4:7], v[176:179], v[216:219], v[4:7]
	v_mfma_f32_16x16x32_bf16 v[0:3], v[184:187], v[216:219], v[0:3]
	s_barrier
	s_addk_i32 s10, 0x100
	s_add_i32 s19, s19, 2
	s_cmp_gt_u32 s19, 13
	s_cbranch_scc0 .LBB0_2522
	s_and_b64 vcc, exec, s[6:7]
	s_cbranch_vccz .LBB0_2525
	s_barrier
